# T10 seam fill: 12288 of the prologue's MoE fp8 weight-conversion items moved into the grid-barrier waits of seams 0..15 (waves 1..3, LDS work counter, stop on release flag, drain at seam 15)
# speedup vs baseline: 1.0044x; 1.0019x over previous
; __device__ __forceinline__ void transpose_item_f8(const float* W, int N, unsigned char* WT, int ldt, int kind, int off, int item, int lane, float scale) {
;     const int nblk = N >> 6, kb = item / nblk, nb = item - kb * nblk, k0 = 128 * kb + 16 * (lane & 7), n = 64 * nb + 4 * (lane >> 3);
;     const f32x4* src = (const f32x4*)(W + (size_t)k0 * N + n);
;     f32x4 v[2][16];
; #pragma unroll
;     for (int hh = 0; hh < 2; ++hh)
; #pragma unroll
;         for (int j = 0; j < 16; ++j) v[hh][j] = __builtin_nontemporal_load(src + (size_t)j * (N >> 2) + 8 * hh);
; #pragma unroll
;     for (int hh = 0; hh < 2; ++hh)
; #pragma unroll
;         for (int i = 0; i < 4; ++i) { v4u o; o.x = pg8::pk4_fp8(v[hh][0][i] * scale, v[hh][1][i] * scale, v[hh][2][i] * scale, v[hh][3][i] * scale); o.y = pg8::pk4_fp8(v[hh][4][i] * scale, v[hh][5][i] * scale, v[hh][6][i] * scale, v[hh][7][i] * scale);
;             o.z = pg8::pk4_fp8(v[hh][8][i] * scale, v[hh][9][i] * scale, v[hh][10][i] * scale, v[hh][11][i] * scale); o.w = pg8::pk4_fp8(v[hh][12][i] * scale, v[hh][13][i] * scale, v[hh][14][i] * scale, v[hh][15][i] * scale);
;             __builtin_nontemporal_store(o, (v4u*)(WT + (size_t)rowmap(kind, off, n + 32 * hh + i) * ldt + k0)); }
; __device__ __forceinline__ void moe_convert(Frame& F, int lo, int hi, int rank, int nrank) {
;     if (MOE_DMA) { moe_convert_dma(F, lo, hi, rank, nrank); return; }
;     for (int it = lo + rank; it < hi; it += nrank) {
;         int r = it; const float* W; unsigned char* WT; int N, ldt, kind, off; float f8s;
;         if (r < 14336) { const int e = r / 1792; r -= e * 1792; W = F.in[IN_WMG] + (size_t)e * 2048 * DFFE; N = DFFE; WT = F.ws + WS_WGU1 + (size_t)e * 14336 * 2048; ldt = 2048; kind = 1; off = 0; f8s = 32.f; }
;         else if ((r -= 14336) < 14336) { const int e = r / 1792; r -= e * 1792; W = F.in[IN_WMU] + (size_t)e * 2048 * DFFE; N = DFFE; WT = F.ws + WS_WGU1 + (size_t)e * 14336 * 2048; ldt = 2048; kind = 1; off = 128; f8s = 256.f; }
;         else { r -= 14336; const int e = r / 1792; r -= e * 1792; W = F.in[IN_WMD] + (size_t)e * DFFE * 2048; N = 2048; WT = F.ws + WS_WDN1 + (size_t)e * 2048 * DFFE; ldt = DFFE; kind = 0; off = 0; f8s = 64.f; }
;         transpose_item_f8(W, N, WT, ldt, kind, off, r, F.lane, f8s);
;     }
.LBB0_235:
	s_cmp_gt_i32 s24, 0x57ff
	s_cbranch_scc1 .LBB0_246
	s_add_u32 s14, s86, 0x23800000
	s_addc_u32 s15, s87, 0
	v_lshlrev_b32_e32 v1, 4, v0
	s_waitcnt vmcnt(2)
	v_lshrrev_b32_e32 v2, 1, v0
	s_add_u32 s16, s86, 0x7800000
	v_and_b32_e32 v1, 0x70, v1
	v_and_b32_e32 v134, 28, v2
	s_addc_u32 s17, s87, 0
	s_add_i32 s18, s24, 0xffff9000
	s_mov_b32 s3, 0
	s_mov_b32 s19, 0xc3e00000
	v_mov_b32_e32 v135, 0x43e00000
	v_mov_b32_e32 v136, 0x5c
	s_movk_i32 s20, 0x5d
	s_movk_i32 s21, 0x5e
	s_movk_i32 s22, 0x5f
	s_movk_i32 s23, 0x7c
	s_movk_i32 s26, 0x7d
	s_movk_i32 s27, 0x7e
	s_movk_i32 s28, 0x7f
	s_mov_b32 s29, s24
	s_branch .LBB0_238
.LBB0_237:
	s_lshr_b32 s12, s2, 6
	v_cvt_f32_u32_e32 v2, s12
	s_sub_i32 s35, 0, s12
	s_abs_i32 s34, s33
	s_ashr_i32 s13, s33, 31
	v_rcp_iflag_f32_e32 v2, v2
	v_mov_b32_e32 v138, 0
	v_mov_b32_e32 v139, 0
	v_mov_b32_e32 v140, 0
	v_mul_f32_e32 v2, 0x4f7ffffe, v2
	v_cvt_u32_f32_e32 v2, v2
	v_mov_b32_e32 v141, 0
	v_readfirstlane_b32 s36, v2
	s_mul_i32 s35, s35, s36
	s_mul_hi_u32 s35, s36, s35
	s_add_i32 s36, s36, s35
	s_mul_hi_u32 s35, s34, s36
	s_mul_i32 s36, s35, s12
	s_sub_i32 s34, s34, s36
	s_add_i32 s37, s35, 1
	s_sub_i32 s36, s34, s12
	s_cmp_ge_u32 s34, s12
	s_cselect_b32 s35, s37, s35
	s_cselect_b32 s34, s36, s34
	s_add_i32 s36, s35, 1
	s_cmp_ge_u32 s34, s12
	s_cselect_b32 s34, s36, s35
	s_xor_b32 s34, s34, s13
	s_sub_i32 s13, s34, s13
	v_lshl_or_b32 v132, s13, 7, v1
	s_mul_i32 s12, s13, s12
	v_mad_u64_u32 v[2:3], s[34:35], v132, s2, 0
	s_sub_i32 s12, s33, s12
	v_ashrrev_i32_e32 v133, 31, v132
	v_mov_b32_e32 v4, v3
	s_lshl_b32 s13, s12, 6
	v_mad_u64_u32 v[4:5], s[34:35], v133, s2, v[4:5]
	v_or_b32_e32 v130, s13, v134
	v_mov_b32_e32 v3, v4
	v_lshl_add_u64 v[2:3], v[2:3], 2, s[10:11]
	v_ashrrev_i32_e32 v131, 31, v130
	v_lshl_add_u64 v[2:3], v[130:131], 2, v[2:3]
	s_lshr_b32 s10, s2, 2
	s_mov_b32 s11, s3
	v_lshl_add_u64 v[4:5], s[10:11], 4, v[2:3]
	s_lshr_b32 s34, s2, 1
	s_mov_b32 s35, s3
	global_load_dwordx4 v[66:69], v[2:3], off nt
	global_load_dwordx4 v[70:73], v[4:5], off nt
	s_waitcnt vmcnt(2)
	v_lshl_add_u64 v[6:7], s[34:35], 4, v[2:3]
	s_mul_i32 s34, s10, 3
	s_mul_i32 s36, s10, 6
	s_mov_b32 s37, s3
	v_lshl_add_u64 v[8:9], s[34:35], 4, v[2:3]
	s_ashr_i32 s35, s2, 31
	s_mov_b32 s34, s2
	v_lshl_add_u64 v[12:13], s[36:37], 4, v[2:3]
	s_mul_i32 s36, s10, 7
	v_lshl_add_u64 v[10:11], s[2:3], 4, v[2:3]
	v_lshl_add_u64 v[14:15], s[36:37], 4, v[2:3]
	v_lshl_add_u64 v[16:17], s[34:35], 4, v[4:5]
	global_load_dwordx4 v[74:77], v[10:11], off nt
	global_load_dwordx4 v[90:93], v[12:13], off nt
	global_load_dwordx4 v[86:89], v[14:15], off nt
	global_load_dwordx4 v[102:105], v[16:17], off nt
	s_lshl_b32 s2, s2, 1
	global_load_dwordx4 v[82:85], v[6:7], off nt
	global_load_dwordx4 v[78:81], v[8:9], off nt
	v_lshl_add_u64 v[18:19], s[2:3], 4, v[2:3]
	s_mul_i32 s2, s10, 9
	v_lshl_add_u64 v[20:21], s[2:3], 4, v[2:3]
	global_load_dwordx4 v[94:97], v[18:19], off nt
	global_load_dwordx4 v[98:101], v[20:21], off nt
	s_mul_i32 s2, s10, 10
	v_lshl_add_u64 v[54:55], s[2:3], 4, v[2:3]
	s_mul_i32 s2, s10, 11
	v_lshl_add_u64 v[56:57], s[2:3], 4, v[2:3]
	s_mul_i32 s2, s10, 12
	global_load_dwordx4 v[114:117], v[54:55], off nt
	global_load_dwordx4 v[106:109], v[56:57], off nt
	v_lshl_add_u64 v[58:59], s[2:3], 4, v[2:3]
	s_mul_i32 s2, s10, 13
	v_lshl_add_u64 v[60:61], s[2:3], 4, v[2:3]
	global_load_dwordx4 v[110:113], v[58:59], off nt
	global_load_dwordx4 v[118:121], v[60:61], off nt
	s_mul_i32 s2, s10, 14
	v_lshl_add_u64 v[62:63], s[2:3], 4, v[2:3]
	s_mul_i32 s2, s10, 15
	v_lshl_add_u64 v[142:143], s[2:3], 4, v[2:3]
	global_load_dwordx4 v[122:125], v[62:63], off nt
	global_load_dwordx4 v[126:129], v[142:143], off nt
	global_load_dwordx4 v[42:45], v[2:3], off offset:128 nt
	global_load_dwordx4 v[46:49], v[4:5], off offset:128 nt
	global_load_dwordx4 v[50:53], v[6:7], off offset:128 nt
	global_load_dwordx4 v[38:41], v[8:9], off offset:128 nt
	global_load_dwordx4 v[30:33], v[10:11], off offset:128 nt
	global_load_dwordx4 v[26:29], v[12:13], off offset:128 nt
	global_load_dwordx4 v[22:25], v[14:15], off offset:128 nt
	global_load_dwordx4 v[34:37], v[16:17], off offset:128 nt
	s_nop 0
	global_load_dwordx4 v[10:13], v[18:19], off offset:128 nt
	global_load_dwordx4 v[14:17], v[20:21], off offset:128 nt
	s_nop 0
	global_load_dwordx4 v[18:21], v[54:55], off offset:128 nt
	global_load_dwordx4 v[6:9], v[56:57], off offset:128 nt
	global_load_dwordx4 v[2:5], v[58:59], off offset:128 nt
	s_lshl_b32 s2, s12, 7
	s_and_b32 s2, s2, 0xffffff00
	s_or_b32 s2, s2, s30
	v_lshl_add_u64 v[132:133], s[8:9], 0, v[132:133]
	s_add_i32 s29, s29, s25
	s_add_i32 s18, s18, s25
	s_cmp_lt_i32 s29, 0x5800
	s_waitcnt vmcnt(28)
	v_mul_f32_e32 v54, s31, v66
	s_waitcnt vmcnt(27)
	v_mul_f32_e32 v55, s31, v70
	v_med3_f32 v54, v54, s19, v135
	v_med3_f32 v55, v55, s19, v135
	v_cvt_pk_fp8_f32 v138, v54, v55
	s_waitcnt vmcnt(26)
	v_mul_f32_e32 v58, s31, v74
	v_med3_f32 v58, v58, s19, v135
	s_waitcnt vmcnt(25)
	v_mul_f32_e32 v59, s31, v90
	s_waitcnt vmcnt(23)
	v_mul_f32_e32 v65, s31, v102
	v_med3_f32 v54, v65, s19, v135
	s_waitcnt vmcnt(22)
	v_mul_f32_e32 v56, s31, v82
	s_waitcnt vmcnt(21)
	v_mul_f32_e32 v57, s31, v78
	v_cvt_pk_fp8_f32 v139, v58, v54
	v_med3_f32 v54, v56, s19, v135
	v_med3_f32 v55, v57, s19, v135
	v_cvt_pk_fp8_f32 v138, v54, v55 op_sel:[0,0,1]
	s_waitcnt vmcnt(20)
	v_mul_f32_e32 v54, s31, v94
	s_waitcnt vmcnt(19)
	v_mul_f32_e32 v55, s31, v98
	v_med3_f32 v54, v54, s19, v135
	v_med3_f32 v55, v55, s19, v135
	v_mul_f32_e32 v64, s31, v86
	v_cvt_pk_fp8_f32 v140, v54, v55
	v_med3_f32 v56, v59, s19, v135
	v_med3_f32 v57, v64, s19, v135
	v_cvt_pk_fp8_f32 v139, v56, v57 op_sel:[0,0,1]
	s_waitcnt vmcnt(18)
; __device__ __forceinline__ unsigned pk4_fp8(float a, float b, float c, float d) { int w = 0; w = __builtin_amdgcn_cvt_pk_fp8_f32(clamp448(a), clamp448(b), w, false); w = __builtin_amdgcn_cvt_pk_fp8_f32(clamp448(c), clamp448(d), w, true); return (unsigned)w; }
; __device__ __forceinline__ int rowmap(int kind, int off, int n) {
;     if (kind == 0) return off + n;
;     if (kind == 1) return off + ((n >> 7) << 8) + (n & 127);
; __device__ __forceinline__ void transpose_item_f8(const float* W, int N, unsigned char* WT, int ldt, int kind, int off, int item, int lane, float scale) {
;     ...
; #pragma unroll
;     for (int hh = 0; hh < 2; ++hh)
; #pragma unroll
;         for (int i = 0; i < 4; ++i) { v4u o; o.x = pg8::pk4_fp8(v[hh][0][i] * scale, v[hh][1][i] * scale, v[hh][2][i] * scale, v[hh][3][i] * scale); o.y = pg8::pk4_fp8(v[hh][4][i] * scale, v[hh][5][i] * scale, v[hh][6][i] * scale, v[hh][7][i] * scale);
;             o.z = pg8::pk4_fp8(v[hh][8][i] * scale, v[hh][9][i] * scale, v[hh][10][i] * scale, v[hh][11][i] * scale); o.w = pg8::pk4_fp8(v[hh][12][i] * scale, v[hh][13][i] * scale, v[hh][14][i] * scale, v[hh][15][i] * scale);
;             __builtin_nontemporal_store(o, (v4u*)(WT + (size_t)rowmap(kind, off, n + 32 * hh + i) * ldt + k0)); }
	v_mul_f32_e32 v56, s31, v114
	s_waitcnt vmcnt(17)
	v_mul_f32_e32 v54, s31, v106
	v_med3_f32 v55, v56, s19, v135
	v_med3_f32 v54, v54, s19, v135
	v_cvt_pk_fp8_f32 v140, v55, v54 op_sel:[0,0,1]
	s_waitcnt vmcnt(16)
	v_mul_f32_e32 v54, s31, v110
	s_waitcnt vmcnt(15)
	v_mul_f32_e32 v59, s31, v118
	v_med3_f32 v58, v54, s19, v135
	v_med3_f32 v59, v59, s19, v135
	v_cvt_pk_fp8_f32 v141, v58, v59
	s_waitcnt vmcnt(14)
	v_mul_f32_e32 v58, s31, v122
	s_waitcnt vmcnt(13)
	v_mul_f32_e32 v70, s31, v126
	v_med3_f32 v66, v58, s19, v135
	v_med3_f32 v70, v70, s19, v135
	v_cvt_pk_fp8_f32 v141, v66, v70 op_sel:[0,0,1]
	v_bitop3_b32 v66, s13, v136, v134 bitop3:0xc8
	v_or_b32_e32 v66, s2, v66
	v_add_u32_e32 v70, s30, v130
	v_cndmask_b32_e64 v66, v66, v70, s[4:5]
	v_ashrrev_i32_e32 v70, 31, v66
	global_load_dwordx4 v[54:57], v[60:61], off offset:128 nt
	v_mul_lo_u32 v70, s6, v70
	global_load_dwordx4 v[62:65], v[62:63], off offset:128 nt
	v_mul_lo_u32 v74, s7, v66
	global_load_dwordx4 v[58:61], v[142:143], off offset:128 nt
	v_mad_u64_u32 v[142:143], s[8:9], s6, v66, v[132:133]
	v_add3_u32 v143, v74, v143, v70
	v_mul_f32_e32 v66, s31, v67
	v_mul_f32_e32 v67, s31, v71
	global_store_dwordx4 v[142:143], v[138:141], off nt
	v_med3_f32 v66, v66, s19, v135
	v_med3_f32 v67, v67, s19, v135
	v_mov_b32_e32 v138, 0
	v_cvt_pk_fp8_f32 v138, v66, v67
	v_mul_f32_e32 v66, s31, v83
	v_mul_f32_e32 v67, s31, v79
	v_med3_f32 v66, v66, s19, v135
	v_med3_f32 v67, v67, s19, v135
	v_cvt_pk_fp8_f32 v138, v66, v67 op_sel:[0,0,1]
	v_mul_f32_e32 v66, s31, v75
	v_mul_f32_e32 v67, s31, v103
	v_med3_f32 v66, v66, s19, v135
	v_med3_f32 v67, v67, s19, v135
	v_mov_b32_e32 v139, 0
	v_cvt_pk_fp8_f32 v139, v66, v67
	v_mul_f32_e32 v66, s31, v91
	v_mul_f32_e32 v67, s31, v87
	v_med3_f32 v66, v66, s19, v135
	v_med3_f32 v67, v67, s19, v135
	v_cvt_pk_fp8_f32 v139, v66, v67 op_sel:[0,0,1]
	v_mul_f32_e32 v66, s31, v95
	v_mul_f32_e32 v67, s31, v99
	v_med3_f32 v66, v66, s19, v135
	v_med3_f32 v67, v67, s19, v135
	v_mov_b32_e32 v140, 0
	v_cvt_pk_fp8_f32 v140, v66, v67
	v_mul_f32_e32 v66, s31, v115
	v_mul_f32_e32 v67, s31, v107
	v_med3_f32 v66, v66, s19, v135
	v_med3_f32 v67, v67, s19, v135
	v_cvt_pk_fp8_f32 v140, v66, v67 op_sel:[0,0,1]
	v_mul_f32_e32 v66, s31, v111
	v_mul_f32_e32 v67, s31, v119
	v_med3_f32 v66, v66, s19, v135
	v_med3_f32 v67, v67, s19, v135
	v_mov_b32_e32 v141, 0
	v_cvt_pk_fp8_f32 v141, v66, v67
	v_mul_f32_e32 v66, s31, v123
	v_mul_f32_e32 v67, s31, v127
	v_med3_f32 v66, v66, s19, v135
	v_med3_f32 v67, v67, s19, v135
	v_cvt_pk_fp8_f32 v141, v66, v67 op_sel:[0,0,1]
	v_or_b32_e32 v66, 1, v130
	v_bitop3_b32 v67, v130, s20, 1 bitop3:0xc8
	v_add_u32_e32 v66, s30, v66
	v_or_b32_e32 v67, s2, v67
	v_cndmask_b32_e64 v66, v67, v66, s[4:5]
	v_ashrrev_i32_e32 v67, 31, v66
	v_mul_lo_u32 v70, s6, v67
	v_mul_lo_u32 v71, s7, v66
	v_mad_u64_u32 v[66:67], s[8:9], s6, v66, v[132:133]
	v_add3_u32 v67, v71, v67, v70
	global_store_dwordx4 v[66:67], v[138:141], off nt
	v_mul_f32_e32 v66, s31, v68
	v_mul_f32_e32 v67, s31, v72
	v_med3_f32 v66, v66, s19, v135
	v_med3_f32 v67, v67, s19, v135
	v_mov_b32_e32 v138, 0
	v_cvt_pk_fp8_f32 v138, v66, v67
	v_mul_f32_e32 v66, s31, v84
	v_mul_f32_e32 v67, s31, v80
	v_med3_f32 v66, v66, s19, v135
	v_med3_f32 v67, v67, s19, v135
	v_cvt_pk_fp8_f32 v138, v66, v67 op_sel:[0,0,1]
	v_mul_f32_e32 v66, s31, v76
	v_mul_f32_e32 v67, s31, v104
	v_med3_f32 v66, v66, s19, v135
	v_med3_f32 v67, v67, s19, v135
	v_mov_b32_e32 v139, 0
	v_cvt_pk_fp8_f32 v139, v66, v67
	v_mul_f32_e32 v66, s31, v92
	v_mul_f32_e32 v67, s31, v88
	v_med3_f32 v66, v66, s19, v135
	v_med3_f32 v67, v67, s19, v135
	v_cvt_pk_fp8_f32 v139, v66, v67 op_sel:[0,0,1]
	v_mul_f32_e32 v66, s31, v96
	v_mul_f32_e32 v67, s31, v100
	v_med3_f32 v66, v66, s19, v135
	v_med3_f32 v67, v67, s19, v135
	v_mov_b32_e32 v140, 0
	v_cvt_pk_fp8_f32 v140, v66, v67
	v_mul_f32_e32 v66, s31, v116
	v_mul_f32_e32 v67, s31, v108
	v_med3_f32 v66, v66, s19, v135
	v_med3_f32 v67, v67, s19, v135
	v_cvt_pk_fp8_f32 v140, v66, v67 op_sel:[0,0,1]
	v_mul_f32_e32 v66, s31, v112
	v_mul_f32_e32 v67, s31, v120
	v_med3_f32 v66, v66, s19, v135
	v_med3_f32 v67, v67, s19, v135
	v_mov_b32_e32 v141, 0
	v_cvt_pk_fp8_f32 v141, v66, v67
	v_mul_f32_e32 v66, s31, v124
	v_mul_f32_e32 v67, s31, v128
	v_med3_f32 v66, v66, s19, v135
	v_med3_f32 v67, v67, s19, v135
	v_cvt_pk_fp8_f32 v141, v66, v67 op_sel:[0,0,1]
	v_or_b32_e32 v66, 2, v130
	v_bitop3_b32 v67, v130, s21, 2 bitop3:0xc8
	v_add_u32_e32 v66, s30, v66
	v_or_b32_e32 v67, s2, v67
	v_cndmask_b32_e64 v66, v67, v66, s[4:5]
	v_ashrrev_i32_e32 v67, 31, v66
	v_mul_lo_u32 v68, s6, v67
	v_mul_lo_u32 v70, s7, v66
	v_mad_u64_u32 v[66:67], s[8:9], s6, v66, v[132:133]
	v_add3_u32 v67, v70, v67, v68
	global_store_dwordx4 v[66:67], v[138:141], off nt
	v_mul_f32_e32 v66, s31, v69
	v_mul_f32_e32 v67, s31, v73
	v_med3_f32 v69, v66, s19, v135
	v_med3_f32 v67, v67, s19, v135
	v_mov_b32_e32 v66, 0
	v_cvt_pk_fp8_f32 v66, v69, v67
	v_mul_f32_e32 v68, s31, v85
	v_mul_f32_e32 v67, s31, v81
	v_med3_f32 v68, v68, s19, v135
	v_med3_f32 v67, v67, s19, v135
	v_cvt_pk_fp8_f32 v66, v68, v67 op_sel:[0,0,1]
	v_mul_f32_e32 v67, s31, v77
	v_mul_f32_e32 v68, s31, v105
	v_med3_f32 v70, v67, s19, v135
	v_med3_f32 v68, v68, s19, v135
	v_mov_b32_e32 v67, 0
	v_cvt_pk_fp8_f32 v67, v70, v68
	v_mul_f32_e32 v69, s31, v93
	v_mul_f32_e32 v68, s31, v89
	v_med3_f32 v69, v69, s19, v135
	v_med3_f32 v68, v68, s19, v135
	v_cvt_pk_fp8_f32 v67, v69, v68 op_sel:[0,0,1]
	v_mul_f32_e32 v68, s31, v97
	v_mul_f32_e32 v69, s31, v101
	v_med3_f32 v71, v68, s19, v135
	v_med3_f32 v69, v69, s19, v135
	v_mov_b32_e32 v68, 0
	v_cvt_pk_fp8_f32 v68, v71, v69
	v_mul_f32_e32 v70, s31, v117
	v_mul_f32_e32 v69, s31, v109
	v_med3_f32 v70, v70, s19, v135
	v_med3_f32 v69, v69, s19, v135
	v_cvt_pk_fp8_f32 v68, v70, v69 op_sel:[0,0,1]
	v_mul_f32_e32 v69, s31, v113
	v_mul_f32_e32 v70, s31, v121
	v_med3_f32 v72, v69, s19, v135
	v_med3_f32 v70, v70, s19, v135
	v_mov_b32_e32 v69, 0
	v_cvt_pk_fp8_f32 v69, v72, v70
	v_mul_f32_e32 v71, s31, v125
	v_mul_f32_e32 v70, s31, v129
	v_med3_f32 v71, v71, s19, v135
	v_med3_f32 v70, v70, s19, v135
	v_cvt_pk_fp8_f32 v69, v71, v70 op_sel:[0,0,1]
	v_or_b32_e32 v70, 3, v130
	v_bitop3_b32 v71, v130, s22, 3 bitop3:0xc8
	v_add_u32_e32 v70, s30, v70
	v_or_b32_e32 v71, s2, v71
	v_cndmask_b32_e64 v72, v71, v70, s[4:5]
	v_ashrrev_i32_e32 v70, 31, v72
	v_mul_lo_u32 v73, s6, v70
	v_mad_u64_u32 v[70:71], s[8:9], s6, v72, v[132:133]
	v_mul_lo_u32 v72, s7, v72
	v_add3_u32 v71, v72, v71, v73
	s_waitcnt vmcnt(10)
; __device__ __forceinline__ unsigned pk4_fp8(float a, float b, float c, float d) { int w = 0; w = __builtin_amdgcn_cvt_pk_fp8_f32(clamp448(a), clamp448(b), w, false); w = __builtin_amdgcn_cvt_pk_fp8_f32(clamp448(c), clamp448(d), w, true); return (unsigned)w; }
; __device__ __forceinline__ int rowmap(int kind, int off, int n) {
;     if (kind == 0) return off + n;
;     if (kind == 1) return off + ((n >> 7) << 8) + (n & 127);
; __device__ __forceinline__ void transpose_item_f8(const float* W, int N, unsigned char* WT, int ldt, int kind, int off, int item, int lane, float scale) {
;     ...
; #pragma unroll
;     for (int hh = 0; hh < 2; ++hh)
; #pragma unroll
;         for (int i = 0; i < 4; ++i) { v4u o; o.x = pg8::pk4_fp8(v[hh][0][i] * scale, v[hh][1][i] * scale, v[hh][2][i] * scale, v[hh][3][i] * scale); o.y = pg8::pk4_fp8(v[hh][4][i] * scale, v[hh][5][i] * scale, v[hh][6][i] * scale, v[hh][7][i] * scale);
;             o.z = pg8::pk4_fp8(v[hh][8][i] * scale, v[hh][9][i] * scale, v[hh][10][i] * scale, v[hh][11][i] * scale); o.w = pg8::pk4_fp8(v[hh][12][i] * scale, v[hh][13][i] * scale, v[hh][14][i] * scale, v[hh][15][i] * scale);
;             __builtin_nontemporal_store(o, (v4u*)(WT + (size_t)rowmap(kind, off, n + 32 * hh + i) * ldt + k0)); }
	v_mul_f32_e32 v10, s31, v10
	s_waitcnt vmcnt(9)
	v_mul_f32_e32 v14, s31, v14
	global_store_dwordx4 v[70:71], v[66:69], off nt
	v_med3_f32 v10, v10, s19, v135
	v_med3_f32 v14, v14, s19, v135
	v_mov_b32_e32 v68, 0
	v_cvt_pk_fp8_f32 v68, v10, v14
	s_waitcnt vmcnt(9)
	v_mul_f32_e32 v18, s31, v18
	s_waitcnt vmcnt(8)
	v_mul_f32_e32 v6, s31, v6
	v_med3_f32 v10, v18, s19, v135
	v_med3_f32 v6, v6, s19, v135
	v_cvt_pk_fp8_f32 v68, v10, v6 op_sel:[0,0,1]
	s_waitcnt vmcnt(7)
	v_mul_f32_e32 v2, s31, v2
	s_waitcnt vmcnt(6)
	v_mul_f32_e32 v6, s31, v54
	v_med3_f32 v2, v2, s19, v135
	v_med3_f32 v6, v6, s19, v135
	v_mov_b32_e32 v69, 0
	v_mul_f32_e32 v42, s31, v42
	v_mul_f32_e32 v46, s31, v46
	v_mul_f32_e32 v30, s31, v30
	v_mul_f32_e32 v34, s31, v34
	v_cvt_pk_fp8_f32 v69, v2, v6
	v_med3_f32 v42, v42, s19, v135
	v_med3_f32 v46, v46, s19, v135
	v_mov_b32_e32 v66, 0
	v_med3_f32 v30, v30, s19, v135
	v_med3_f32 v34, v34, s19, v135
	v_mov_b32_e32 v67, 0
	v_cvt_pk_fp8_f32 v66, v42, v46
	v_cvt_pk_fp8_f32 v67, v30, v34
	s_waitcnt vmcnt(5)
	v_mul_f32_e32 v10, s31, v62
	s_waitcnt vmcnt(4)
	v_mul_f32_e32 v2, s31, v58
	v_med3_f32 v6, v10, s19, v135
	v_med3_f32 v2, v2, s19, v135
	v_or_b32_e32 v70, 32, v130
	v_mul_f32_e32 v50, s31, v50
	v_mul_f32_e32 v38, s31, v38
	v_mul_f32_e32 v26, s31, v26
	v_mul_f32_e32 v22, s31, v22
	v_cvt_pk_fp8_f32 v69, v6, v2 op_sel:[0,0,1]
	v_bitop3_b32 v6, v130, s23, 32 bitop3:0xc8
	v_med3_f32 v42, v50, s19, v135
	v_med3_f32 v38, v38, s19, v135
	v_med3_f32 v26, v26, s19, v135
	v_med3_f32 v22, v22, s19, v135
	v_add_u32_e32 v2, s30, v70
	v_or_b32_e32 v6, s2, v6
	v_cvt_pk_fp8_f32 v66, v42, v38 op_sel:[0,0,1]
	v_cvt_pk_fp8_f32 v67, v26, v22 op_sel:[0,0,1]
	v_cndmask_b32_e64 v2, v6, v2, s[4:5]
	v_ashrrev_i32_e32 v6, 31, v2
	v_mul_lo_u32 v6, s6, v6
	v_mad_u64_u32 v[70:71], s[8:9], s6, v2, v[132:133]
	v_mul_lo_u32 v2, s7, v2
	v_add3_u32 v71, v2, v71, v6
	v_mul_f32_e32 v2, s31, v43
	v_mul_f32_e32 v6, s31, v47
	global_store_dwordx4 v[70:71], v[66:69], off nt
	v_med3_f32 v2, v2, s19, v135
	v_med3_f32 v6, v6, s19, v135
	v_mov_b32_e32 v66, 0
	v_cvt_pk_fp8_f32 v66, v2, v6
	v_mul_f32_e32 v10, s31, v51
	v_mul_f32_e32 v2, s31, v39
	v_med3_f32 v6, v10, s19, v135
	v_med3_f32 v2, v2, s19, v135
	v_cvt_pk_fp8_f32 v66, v6, v2 op_sel:[0,0,1]
	v_mul_f32_e32 v2, s31, v31
	v_mul_f32_e32 v6, s31, v35
	v_med3_f32 v2, v2, s19, v135
	v_med3_f32 v6, v6, s19, v135
	v_mov_b32_e32 v67, 0
	v_cvt_pk_fp8_f32 v67, v2, v6
	v_mul_f32_e32 v10, s31, v27
	v_mul_f32_e32 v2, s31, v23
	v_med3_f32 v6, v10, s19, v135
	v_med3_f32 v2, v2, s19, v135
	v_cvt_pk_fp8_f32 v67, v6, v2 op_sel:[0,0,1]
	v_mul_f32_e32 v2, s31, v11
	v_mul_f32_e32 v6, s31, v15
	v_med3_f32 v2, v2, s19, v135
	v_med3_f32 v6, v6, s19, v135
	v_mov_b32_e32 v68, 0
	v_cvt_pk_fp8_f32 v68, v2, v6
	v_mul_f32_e32 v10, s31, v19
	v_mul_f32_e32 v2, s31, v7
	v_med3_f32 v6, v10, s19, v135
	v_med3_f32 v2, v2, s19, v135
	v_cvt_pk_fp8_f32 v68, v6, v2 op_sel:[0,0,1]
	v_mul_f32_e32 v2, s31, v3
	v_mul_f32_e32 v3, s31, v55
	v_med3_f32 v2, v2, s19, v135
	v_med3_f32 v3, v3, s19, v135
	v_mov_b32_e32 v69, 0
	v_cvt_pk_fp8_f32 v69, v2, v3
	v_mul_f32_e32 v6, s31, v63
	v_mul_f32_e32 v2, s31, v59
	v_med3_f32 v3, v6, s19, v135
	v_med3_f32 v2, v2, s19, v135
	v_cvt_pk_fp8_f32 v69, v3, v2 op_sel:[0,0,1]
	v_or_b32_e32 v2, 33, v130
	v_bitop3_b32 v3, v130, s26, 33 bitop3:0xc8
	v_add_u32_e32 v2, s30, v2
	v_or_b32_e32 v3, s2, v3
	v_cndmask_b32_e64 v6, v3, v2, s[4:5]
	v_ashrrev_i32_e32 v2, 31, v6
	v_mul_lo_u32 v7, s6, v2
	v_mad_u64_u32 v[2:3], s[8:9], s6, v6, v[132:133]
	v_mul_lo_u32 v6, s7, v6
	v_add3_u32 v3, v6, v3, v7
	global_store_dwordx4 v[2:3], v[66:69], off nt
	v_mul_f32_e32 v2, s31, v44
	v_mul_f32_e32 v3, s31, v48
	v_med3_f32 v2, v2, s19, v135
	v_med3_f32 v3, v3, s19, v135
	v_mov_b32_e32 v66, 0
	v_cvt_pk_fp8_f32 v66, v2, v3
	v_mul_f32_e32 v6, s31, v52
	v_mul_f32_e32 v2, s31, v40
	v_med3_f32 v3, v6, s19, v135
	v_med3_f32 v2, v2, s19, v135
	v_cvt_pk_fp8_f32 v66, v3, v2 op_sel:[0,0,1]
	v_mul_f32_e32 v2, s31, v32
	v_mul_f32_e32 v3, s31, v36
	v_med3_f32 v2, v2, s19, v135
	v_med3_f32 v3, v3, s19, v135
	v_mov_b32_e32 v67, 0
	v_cvt_pk_fp8_f32 v67, v2, v3
	v_mul_f32_e32 v6, s31, v28
	v_mul_f32_e32 v2, s31, v24
	v_med3_f32 v3, v6, s19, v135
	v_med3_f32 v2, v2, s19, v135
	v_cvt_pk_fp8_f32 v67, v3, v2 op_sel:[0,0,1]
	v_mul_f32_e32 v2, s31, v12
	v_mul_f32_e32 v3, s31, v16
	v_med3_f32 v2, v2, s19, v135
	v_med3_f32 v3, v3, s19, v135
	v_mov_b32_e32 v68, 0
	v_cvt_pk_fp8_f32 v68, v2, v3
	v_mul_f32_e32 v6, s31, v20
	v_mul_f32_e32 v2, s31, v8
	v_med3_f32 v3, v6, s19, v135
	v_med3_f32 v2, v2, s19, v135
	v_cvt_pk_fp8_f32 v68, v3, v2 op_sel:[0,0,1]
	v_mul_f32_e32 v2, s31, v4
	v_mul_f32_e32 v3, s31, v56
	v_med3_f32 v2, v2, s19, v135
	v_med3_f32 v3, v3, s19, v135
	v_mov_b32_e32 v69, 0
	v_cvt_pk_fp8_f32 v69, v2, v3
	v_mul_f32_e32 v4, s31, v64
	v_mul_f32_e32 v2, s31, v60
	v_med3_f32 v3, v4, s19, v135
	v_med3_f32 v2, v2, s19, v135
	v_cvt_pk_fp8_f32 v69, v3, v2 op_sel:[0,0,1]
	v_or_b32_e32 v2, 34, v130
	v_bitop3_b32 v3, v130, s27, 34 bitop3:0xc8
	v_add_u32_e32 v2, s30, v2
	v_or_b32_e32 v3, s2, v3
	v_cndmask_b32_e64 v4, v3, v2, s[4:5]
	v_ashrrev_i32_e32 v2, 31, v4
	v_mul_lo_u32 v6, s6, v2
	v_mad_u64_u32 v[2:3], s[8:9], s6, v4, v[132:133]
	v_mul_lo_u32 v4, s7, v4
	v_add3_u32 v3, v4, v3, v6
	global_store_dwordx4 v[2:3], v[66:69], off nt
	v_mul_f32_e32 v2, s31, v45
	v_mul_f32_e32 v3, s31, v49
	v_med3_f32 v6, v2, s19, v135
	v_med3_f32 v3, v3, s19, v135
	v_mov_b32_e32 v2, 0
	v_cvt_pk_fp8_f32 v2, v6, v3
	v_mul_f32_e32 v4, s31, v53
	v_mul_f32_e32 v3, s31, v41
	v_med3_f32 v4, v4, s19, v135
	v_med3_f32 v3, v3, s19, v135
	v_cvt_pk_fp8_f32 v2, v4, v3 op_sel:[0,0,1]
	v_mul_f32_e32 v3, s31, v33
	v_mul_f32_e32 v4, s31, v37
	v_med3_f32 v7, v3, s19, v135
	v_med3_f32 v4, v4, s19, v135
	v_mov_b32_e32 v3, 0
	v_cvt_pk_fp8_f32 v3, v7, v4
	v_mul_f32_e32 v6, s31, v29
	v_mul_f32_e32 v4, s31, v25
	v_med3_f32 v6, v6, s19, v135
	v_med3_f32 v4, v4, s19, v135
	v_cvt_pk_fp8_f32 v3, v6, v4 op_sel:[0,0,1]
	v_mul_f32_e32 v4, s31, v13
	v_mul_f32_e32 v6, s31, v17
	v_med3_f32 v8, v4, s19, v135
	v_med3_f32 v6, v6, s19, v135
	v_mov_b32_e32 v4, 0
	v_cvt_pk_fp8_f32 v4, v8, v6
	v_mul_f32_e32 v7, s31, v21
	v_mul_f32_e32 v6, s31, v9
	v_med3_f32 v7, v7, s19, v135
	v_med3_f32 v6, v6, s19, v135
	v_cvt_pk_fp8_f32 v4, v7, v6 op_sel:[0,0,1]
	v_mul_f32_e32 v5, s31, v5
	v_mul_f32_e32 v6, s31, v57
	v_med3_f32 v8, v5, s19, v135
	v_med3_f32 v6, v6, s19, v135
	v_mov_b32_e32 v5, 0
	v_cvt_pk_fp8_f32 v5, v8, v6
	v_mul_f32_e32 v7, s31, v65
	v_mul_f32_e32 v6, s31, v61
	v_med3_f32 v7, v7, s19, v135
	v_med3_f32 v6, v6, s19, v135
	v_cvt_pk_fp8_f32 v5, v7, v6 op_sel:[0,0,1]
	v_or_b32_e32 v6, 35, v130
	v_bitop3_b32 v7, v130, s28, 35 bitop3:0xc8
	v_add_u32_e32 v6, s30, v6
	v_or_b32_e32 v7, s2, v7
	v_cndmask_b32_e64 v8, v7, v6, s[4:5]
	v_ashrrev_i32_e32 v6, 31, v8
	v_mul_lo_u32 v9, s6, v6
	v_mad_u64_u32 v[6:7], s[4:5], s6, v8, v[132:133]
	v_mul_lo_u32 v8, s7, v8
	v_add3_u32 v7, v8, v7, v9
	global_store_dwordx4 v[6:7], v[2:5], off nt
	s_cbranch_scc0 .LBB0_246

; __device__ __forceinline__ void transpose_item_f8(const float* W, int N, unsigned char* WT, int ldt, int kind, int off, int item, int lane, float scale) {
;     const int nblk = N >> 6, kb = item / nblk, nb = item - kb * nblk, k0 = 128 * kb + 16 * (lane & 7), n = 64 * nb + 4 * (lane >> 3);
;     const f32x4* src = (const f32x4*)(W + (size_t)k0 * N + n);
;     f32x4 v[2][16];
; #pragma unroll
;     for (int hh = 0; hh < 2; ++hh)
; #pragma unroll
;         for (int j = 0; j < 16; ++j) v[hh][j] = __builtin_nontemporal_load(src + (size_t)j * (N >> 2) + 8 * hh);
; __device__ __forceinline__ void moe_convert(Frame& F, int lo, int hi, int rank, int nrank) {
;     if (MOE_DMA) { moe_convert_dma(F, lo, hi, rank, nrank); return; }
;     for (int it = lo + rank; it < hi; it += nrank) {
;         int r = it; const float* W; unsigned char* WT; int N, ldt, kind, off; float f8s;
;         if (r < 14336) { const int e = r / 1792; r -= e * 1792; W = F.in[IN_WMG] + (size_t)e * 2048 * DFFE; N = DFFE; WT = F.ws + WS_WGU1 + (size_t)e * 14336 * 2048; ldt = 2048; kind = 1; off = 0; f8s = 32.f; }
;         else if ((r -= 14336) < 14336) { const int e = r / 1792; r -= e * 1792; W = F.in[IN_WMU] + (size_t)e * 2048 * DFFE; N = DFFE; WT = F.ws + WS_WGU1 + (size_t)e * 14336 * 2048; ldt = 2048; kind = 1; off = 128; f8s = 256.f; }
;         else { r -= 14336; const int e = r / 1792; r -= e * 1792; W = F.in[IN_WMD] + (size_t)e * DFFE * 2048; N = 2048; WT = F.ws + WS_WDN1 + (size_t)e * 2048 * DFFE; ldt = DFFE; kind = 0; off = 0; f8s = 64.f; }
;         transpose_item_f8(W, N, WT, ldt, kind, off, r, F.lane, f8s);
.LBB0_298:
	s_or_b64 exec, exec, s[0:1]
	v_readfirstlane_b32 s4, v0
	s_lshr_b32 s4, s4, 6
	s_cmp_lg_u32 s4, 0
	s_cbranch_scc1 .Lsf0_notw0
	v_mov_b32_e32 v2, 0x20020
	v_mov_b32_e32 v4, 1
	ds_write_b32 v2, v4
	s_branch .Lsf0_skip
.Lsf0_notw0:
	s_cmp_gt_u32 s4, 3
	s_cbranch_scc1 .Lsf0_skip
	v_mov_b32_e32 v8, 0x20020
	ds_read_b32 v9, v8 offset:4
	v_mbcnt_lo_u32_b32 v2, -1, 0
	v_mbcnt_hi_u32_b32 v2, -1, v2
	s_waitcnt lgkmcnt(0)
	v_readfirstlane_b32 s5, v9
	s_cmp_ge_u32 s5, 96
	s_cbranch_scc1 .Lsf0_skip
	s_add_i32 s5, s4, -1
	s_lshl_b32 s5, s5, 14
	v_lshl_add_u32 v7, v2, 4, s5
	ds_write_b128 v7, v[160:163] offset:0
	ds_write_b128 v7, v[164:167] offset:1024
	ds_write_b128 v7, v[168:171] offset:2048
	ds_write_b128 v7, v[172:175] offset:3072
	ds_write_b128 v7, v[176:179] offset:4096
	ds_write_b128 v7, v[180:183] offset:5120
	ds_write_b128 v7, v[184:187] offset:6144
	ds_write_b128 v7, v[188:191] offset:7168
	ds_write_b128 v7, v[192:195] offset:8192
	ds_write_b128 v7, v[196:199] offset:9216
	ds_write_b128 v7, v[200:203] offset:10240
	ds_write_b128 v7, v[204:207] offset:11264
	ds_write_b128 v7, v[208:211] offset:12288
	ds_write_b128 v7, v[212:215] offset:13312
	ds_write_b128 v7, v[216:219] offset:14336
	ds_write_b128 v7, v[220:223] offset:15360
	v_readlane_b32 s6, v247, 0
	v_readlane_b32 s7, v247, 1
	s_load_dwordx2 s[10:11], s[6:7], 0xc0
	s_load_dwordx2 s[12:13], s[6:7], 0xc8
	v_readlane_b32 s33, v247, 6
	v_mov_b32_e32 v3, 0x43e00000
	v_cmp_eq_u32_e32 vcc, 0, v2
	s_mul_i32 s33, s33, 96
	s_nop 1
	v_cndmask_b32_e64 v18, 0, 1, vcc
	s_waitcnt lgkmcnt(0)
.Lsf0_loop:
	ds_read_b32 v9, v8
	s_waitcnt lgkmcnt(0)
	v_readfirstlane_b32 s5, v9
	s_cmp_eq_u32 s5, 1
	s_cbranch_scc1 .Lsf0_done
	ds_add_rtn_u32 v9, v8, v18 offset:4
	s_waitcnt lgkmcnt(0)
	v_readfirstlane_b32 s18, v9
	s_cmp_ge_u32 s18, 96
	s_cbranch_scc1 .Lsf0_done
	s_add_i32 s18, s18, s33
	s_and_b32 s27, s18, 1
	s_lshr_b32 s19, s18, 1
	s_add_i32 s19, s19, 0x5800
	s_cmp_lt_u32 s19, 0x7000
	s_cbranch_scc0 .Lsf0_down
	s_add_i32 s20, s19, 0xffffc800
	s_lshr_b32 s21, s20, 8
	s_mul_i32 s21, s21, 37
	s_lshr_b32 s21, s21, 8
	s_mul_i32 s28, s21, 0x700
	s_sub_i32 s20, s20, s28
	s_mul_i32 s28, s21, 0x3800000
	s_add_u32 s14, s10, s28
	s_addc_u32 s15, s11, 0
	s_mul_i32 s28, s21, 0x1c00000
	s_add_u32 s28, s28, 0x7800000
	s_add_u32 s16, s86, s28
	s_addc_u32 s17, s87, 0
	s_movk_i32 s24, 0x7000
	s_movk_i32 s25, 0x800
	s_mov_b32 s26, 0x43800000
	s_lshr_b32 s22, s20, 4
	s_mul_i32 s22, s22, 0x2493
	s_lshr_b32 s22, s22, 16
	s_mul_i32 s28, s22, 0x70
	s_sub_i32 s23, s20, s28
	s_mov_b32 s29, 1
	s_branch .Lsf0_dec
.Lsf0_down:
	s_add_i32 s20, s19, 0xffff9000
	s_lshr_b32 s21, s20, 8
	s_mul_i32 s21, s21, 37
	s_lshr_b32 s21, s21, 8
	s_mul_i32 s28, s21, 0x700
	s_sub_i32 s20, s20, s28
	s_mul_i32 s28, s21, 0x3800000
	s_add_u32 s14, s12, s28
	s_addc_u32 s15, s13, 0
	s_mul_i32 s28, s21, 0xe00000
	s_add_u32 s28, s28, 0x23800000
	s_add_u32 s16, s86, s28
	s_addc_u32 s17, s87, 0
	s_movk_i32 s24, 0x2000
	s_movk_i32 s25, 0x1c00
	s_mov_b32 s26, 0x42800000
	s_lshr_b32 s22, s20, 5
	s_and_b32 s23, s20, 31
	s_mov_b32 s29, 0
.Lsf0_dec:
	v_and_b32_e32 v4, 7, v2
	v_lshrrev_b32_e32 v5, 3, v2
	s_lshl_b32 s28, s24, 4
	v_mul_lo_u32 v6, s28, v4
	v_lshl_add_u32 v5, v5, 4, v6
	s_lshl_b32 s28, s24, 7
	s_mul_i32 s28, s28, s22
	s_lshl_b32 s30, s23, 8
	s_add_i32 s28, s28, s30
	s_lshl_b32 s30, s27, 7
	s_add_i32 s28, s28, s30
	s_add_u32 s14, s14, s28
	s_addc_u32 s15, s15, 0
	s_lshl_b32 s30, s23, 6
	s_lshl_b32 s31, s27, 5
	s_add_i32 s30, s30, s31
	s_cmp_eq_u32 s29, 0
	s_cbranch_scc1 .Lsf0_k0
	s_lshr_b32 s31, s30, 7
	s_lshl_b32 s31, s31, 8
	s_and_b32 s30, s30, 0x7f
	s_add_i32 s30, s30, s31
	s_add_i32 s30, s30, 0x80
.Lsf0_k0:
	s_mul_i32 s30, s30, s25
	s_lshl_b32 s31, s22, 7
	s_add_i32 s30, s30, s31
	s_add_u32 s16, s16, s30
	s_addc_u32 s17, s17, 0
	v_lshrrev_b32_e32 v6, 3, v2
	v_lshlrev_b32_e32 v6, 2, v6
	v_mul_lo_u32 v6, s25, v6
	v_lshl_add_u32 v6, v4, 4, v6
	global_load_dwordx4 v[160:163], v5, s[14:15] nt
	s_add_u32 s14, s14, s24
	s_addc_u32 s15, s15, 0
	global_load_dwordx4 v[164:167], v5, s[14:15] nt
	s_add_u32 s14, s14, s24
	s_addc_u32 s15, s15, 0
	global_load_dwordx4 v[168:171], v5, s[14:15] nt
	s_add_u32 s14, s14, s24
	s_addc_u32 s15, s15, 0
	global_load_dwordx4 v[172:175], v5, s[14:15] nt
	s_add_u32 s14, s14, s24
	s_addc_u32 s15, s15, 0
	global_load_dwordx4 v[176:179], v5, s[14:15] nt
	s_add_u32 s14, s14, s24
	s_addc_u32 s15, s15, 0
	global_load_dwordx4 v[180:183], v5, s[14:15] nt
	s_add_u32 s14, s14, s24
	s_addc_u32 s15, s15, 0
	global_load_dwordx4 v[184:187], v5, s[14:15] nt
	s_add_u32 s14, s14, s24
	s_addc_u32 s15, s15, 0
	global_load_dwordx4 v[188:191], v5, s[14:15] nt
	s_add_u32 s14, s14, s24
	s_addc_u32 s15, s15, 0
	global_load_dwordx4 v[192:195], v5, s[14:15] nt
	s_add_u32 s14, s14, s24
	s_addc_u32 s15, s15, 0
	global_load_dwordx4 v[196:199], v5, s[14:15] nt
	s_add_u32 s14, s14, s24
	s_addc_u32 s15, s15, 0
	global_load_dwordx4 v[200:203], v5, s[14:15] nt
	s_add_u32 s14, s14, s24
	s_addc_u32 s15, s15, 0
	global_load_dwordx4 v[204:207], v5, s[14:15] nt
	s_add_u32 s14, s14, s24
	s_addc_u32 s15, s15, 0
	global_load_dwordx4 v[208:211], v5, s[14:15] nt
	s_add_u32 s14, s14, s24
	s_addc_u32 s15, s15, 0
	global_load_dwordx4 v[212:215], v5, s[14:15] nt
	s_add_u32 s14, s14, s24
	s_addc_u32 s15, s15, 0
	global_load_dwordx4 v[216:219], v5, s[14:15] nt
	s_add_u32 s14, s14, s24
	s_addc_u32 s15, s15, 0
	global_load_dwordx4 v[220:223], v5, s[14:15] nt
	s_mov_b32 s28, 0xc3e00000
	s_waitcnt vmcnt(0)
; __device__ __forceinline__ unsigned pk4_fp8(float a, float b, float c, float d) { int w = 0; w = __builtin_amdgcn_cvt_pk_fp8_f32(clamp448(a), clamp448(b), w, false); w = __builtin_amdgcn_cvt_pk_fp8_f32(clamp448(c), clamp448(d), w, true); return (unsigned)w; }
; __device__ __forceinline__ float clamp448(float x) { return __builtin_amdgcn_fmed3f(x, -448.f, 448.f); }
; __device__ __forceinline__ void transpose_item_f8(const float* W, int N, unsigned char* WT, int ldt, int kind, int off, int item, int lane, float scale) {
;     ...
; #pragma unroll
;     for (int hh = 0; hh < 2; ++hh)
; #pragma unroll
;         for (int i = 0; i < 4; ++i) { v4u o; o.x = pg8::pk4_fp8(v[hh][0][i] * scale, v[hh][1][i] * scale, v[hh][2][i] * scale, v[hh][3][i] * scale); o.y = pg8::pk4_fp8(v[hh][4][i] * scale, v[hh][5][i] * scale, v[hh][6][i] * scale, v[hh][7][i] * scale);
;             o.z = pg8::pk4_fp8(v[hh][8][i] * scale, v[hh][9][i] * scale, v[hh][10][i] * scale, v[hh][11][i] * scale); o.w = pg8::pk4_fp8(v[hh][12][i] * scale, v[hh][13][i] * scale, v[hh][14][i] * scale, v[hh][15][i] * scale);
;             __builtin_nontemporal_store(o, (v4u*)(WT + (size_t)rowmap(kind, off, n + 32 * hh + i) * ldt + k0)); }
	v_mul_f32_e32 v160, s26, v160
	v_mul_f32_e32 v161, s26, v161
	v_mul_f32_e32 v162, s26, v162
	v_mul_f32_e32 v163, s26, v163
	v_mul_f32_e32 v164, s26, v164
	v_mul_f32_e32 v165, s26, v165
	v_mul_f32_e32 v166, s26, v166
	v_mul_f32_e32 v167, s26, v167
	v_mul_f32_e32 v168, s26, v168
	v_mul_f32_e32 v169, s26, v169
	v_mul_f32_e32 v170, s26, v170
	v_mul_f32_e32 v171, s26, v171
	v_mul_f32_e32 v172, s26, v172
	v_mul_f32_e32 v173, s26, v173
	v_mul_f32_e32 v174, s26, v174
	v_mul_f32_e32 v175, s26, v175
	v_mul_f32_e32 v176, s26, v176
	v_mul_f32_e32 v177, s26, v177
	v_mul_f32_e32 v178, s26, v178
	v_mul_f32_e32 v179, s26, v179
	v_mul_f32_e32 v180, s26, v180
	v_mul_f32_e32 v181, s26, v181
	v_mul_f32_e32 v182, s26, v182
	v_mul_f32_e32 v183, s26, v183
	v_mul_f32_e32 v184, s26, v184
	v_mul_f32_e32 v185, s26, v185
	v_mul_f32_e32 v186, s26, v186
	v_mul_f32_e32 v187, s26, v187
	v_mul_f32_e32 v188, s26, v188
	v_mul_f32_e32 v189, s26, v189
	v_mul_f32_e32 v190, s26, v190
	v_mul_f32_e32 v191, s26, v191
	v_mul_f32_e32 v192, s26, v192
	v_mul_f32_e32 v193, s26, v193
	v_mul_f32_e32 v194, s26, v194
	v_mul_f32_e32 v195, s26, v195
	v_mul_f32_e32 v196, s26, v196
	v_mul_f32_e32 v197, s26, v197
	v_mul_f32_e32 v198, s26, v198
	v_mul_f32_e32 v199, s26, v199
	v_mul_f32_e32 v200, s26, v200
	v_mul_f32_e32 v201, s26, v201
	v_mul_f32_e32 v202, s26, v202
	v_mul_f32_e32 v203, s26, v203
	v_mul_f32_e32 v204, s26, v204
	v_mul_f32_e32 v205, s26, v205
	v_mul_f32_e32 v206, s26, v206
	v_mul_f32_e32 v207, s26, v207
	v_mul_f32_e32 v208, s26, v208
	v_mul_f32_e32 v209, s26, v209
	v_mul_f32_e32 v210, s26, v210
	v_mul_f32_e32 v211, s26, v211
	v_mul_f32_e32 v212, s26, v212
	v_mul_f32_e32 v213, s26, v213
	v_mul_f32_e32 v214, s26, v214
	v_mul_f32_e32 v215, s26, v215
	v_mul_f32_e32 v216, s26, v216
	v_mul_f32_e32 v217, s26, v217
	v_mul_f32_e32 v218, s26, v218
	v_mul_f32_e32 v219, s26, v219
	v_mul_f32_e32 v220, s26, v220
	v_mul_f32_e32 v221, s26, v221
	v_mul_f32_e32 v222, s26, v222
	v_mul_f32_e32 v223, s26, v223
	v_med3_f32 v160, v160, s28, v3
	v_med3_f32 v161, v161, s28, v3
	v_med3_f32 v162, v162, s28, v3
	v_med3_f32 v163, v163, s28, v3
	v_med3_f32 v164, v164, s28, v3
	v_med3_f32 v165, v165, s28, v3
	v_med3_f32 v166, v166, s28, v3
	v_med3_f32 v167, v167, s28, v3
	v_med3_f32 v168, v168, s28, v3
	v_med3_f32 v169, v169, s28, v3
	v_med3_f32 v170, v170, s28, v3
	v_med3_f32 v171, v171, s28, v3
	v_med3_f32 v172, v172, s28, v3
	v_med3_f32 v173, v173, s28, v3
	v_med3_f32 v174, v174, s28, v3
	v_med3_f32 v175, v175, s28, v3
	v_med3_f32 v176, v176, s28, v3
	v_med3_f32 v177, v177, s28, v3
	v_med3_f32 v178, v178, s28, v3
	v_med3_f32 v179, v179, s28, v3
	v_med3_f32 v180, v180, s28, v3
	v_med3_f32 v181, v181, s28, v3
	v_med3_f32 v182, v182, s28, v3
	v_med3_f32 v183, v183, s28, v3
	v_med3_f32 v184, v184, s28, v3
	v_med3_f32 v185, v185, s28, v3
	v_med3_f32 v186, v186, s28, v3
	v_med3_f32 v187, v187, s28, v3
	v_med3_f32 v188, v188, s28, v3
	v_med3_f32 v189, v189, s28, v3
	v_med3_f32 v190, v190, s28, v3
	v_med3_f32 v191, v191, s28, v3
	v_med3_f32 v192, v192, s28, v3
	v_med3_f32 v193, v193, s28, v3
	v_med3_f32 v194, v194, s28, v3
	v_med3_f32 v195, v195, s28, v3
	v_med3_f32 v196, v196, s28, v3
	v_med3_f32 v197, v197, s28, v3
	v_med3_f32 v198, v198, s28, v3
	v_med3_f32 v199, v199, s28, v3
	v_med3_f32 v200, v200, s28, v3
	v_med3_f32 v201, v201, s28, v3
	v_med3_f32 v202, v202, s28, v3
	v_med3_f32 v203, v203, s28, v3
	v_med3_f32 v204, v204, s28, v3
	v_med3_f32 v205, v205, s28, v3
	v_med3_f32 v206, v206, s28, v3
	v_med3_f32 v207, v207, s28, v3
	v_med3_f32 v208, v208, s28, v3
	v_med3_f32 v209, v209, s28, v3
	v_med3_f32 v210, v210, s28, v3
	v_med3_f32 v211, v211, s28, v3
	v_med3_f32 v212, v212, s28, v3
	v_med3_f32 v213, v213, s28, v3
	v_med3_f32 v214, v214, s28, v3
	v_med3_f32 v215, v215, s28, v3
	v_med3_f32 v216, v216, s28, v3
	v_med3_f32 v217, v217, s28, v3
	v_med3_f32 v218, v218, s28, v3
	v_med3_f32 v219, v219, s28, v3
	v_med3_f32 v220, v220, s28, v3
	v_med3_f32 v221, v221, s28, v3
	v_med3_f32 v222, v222, s28, v3
	v_med3_f32 v223, v223, s28, v3
	v_mov_b32_e32 v10, 0
	v_mov_b32_e32 v11, 0
	v_mov_b32_e32 v12, 0
	v_mov_b32_e32 v13, 0
	v_cvt_pk_fp8_f32 v10, v160, v164
	v_cvt_pk_fp8_f32 v11, v176, v180
	v_cvt_pk_fp8_f32 v12, v192, v196
	v_cvt_pk_fp8_f32 v13, v208, v212
	v_cvt_pk_fp8_f32 v10, v168, v172 op_sel:[0,0,1]
	v_cvt_pk_fp8_f32 v11, v184, v188 op_sel:[0,0,1]
	v_cvt_pk_fp8_f32 v12, v200, v204 op_sel:[0,0,1]
	v_cvt_pk_fp8_f32 v13, v216, v220 op_sel:[0,0,1]
	s_nop 1
	global_store_dwordx4 v6, v[10:13], s[16:17] nt
	s_add_u32 s16, s16, s25
	s_addc_u32 s17, s17, 0
	v_mov_b32_e32 v14, 0
	v_mov_b32_e32 v15, 0
	v_mov_b32_e32 v16, 0
	v_mov_b32_e32 v17, 0
	v_cvt_pk_fp8_f32 v14, v161, v165
	v_cvt_pk_fp8_f32 v15, v177, v181
	v_cvt_pk_fp8_f32 v16, v193, v197
	v_cvt_pk_fp8_f32 v17, v209, v213
	v_cvt_pk_fp8_f32 v14, v169, v173 op_sel:[0,0,1]
	v_cvt_pk_fp8_f32 v15, v185, v189 op_sel:[0,0,1]
	v_cvt_pk_fp8_f32 v16, v201, v205 op_sel:[0,0,1]
	v_cvt_pk_fp8_f32 v17, v217, v221 op_sel:[0,0,1]
	s_nop 1
	global_store_dwordx4 v6, v[14:17], s[16:17] nt
	s_add_u32 s16, s16, s25
	s_addc_u32 s17, s17, 0
	v_mov_b32_e32 v248, 0
	v_mov_b32_e32 v249, 0
	v_mov_b32_e32 v250, 0
	v_mov_b32_e32 v251, 0
	v_cvt_pk_fp8_f32 v248, v162, v166
	v_cvt_pk_fp8_f32 v249, v178, v182
	v_cvt_pk_fp8_f32 v250, v194, v198
	v_cvt_pk_fp8_f32 v251, v210, v214
	v_cvt_pk_fp8_f32 v248, v170, v174 op_sel:[0,0,1]
	v_cvt_pk_fp8_f32 v249, v186, v190 op_sel:[0,0,1]
	v_cvt_pk_fp8_f32 v250, v202, v206 op_sel:[0,0,1]
	v_cvt_pk_fp8_f32 v251, v218, v222 op_sel:[0,0,1]
	s_nop 1
	global_store_dwordx4 v6, v[248:251], s[16:17] nt
	s_add_u32 s16, s16, s25
	s_addc_u32 s17, s17, 0
	v_mov_b32_e32 v252, 0
	v_mov_b32_e32 v253, 0
	v_mov_b32_e32 v254, 0
	v_mov_b32_e32 v255, 0
	v_cvt_pk_fp8_f32 v252, v163, v167
	v_cvt_pk_fp8_f32 v253, v179, v183
	v_cvt_pk_fp8_f32 v254, v195, v199
	v_cvt_pk_fp8_f32 v255, v211, v215
	v_cvt_pk_fp8_f32 v252, v171, v175 op_sel:[0,0,1]
	v_cvt_pk_fp8_f32 v253, v187, v191 op_sel:[0,0,1]
	v_cvt_pk_fp8_f32 v254, v203, v207 op_sel:[0,0,1]
	v_cvt_pk_fp8_f32 v255, v219, v223 op_sel:[0,0,1]
	s_nop 1
	global_store_dwordx4 v6, v[252:255], s[16:17] nt
	s_branch .Lsf0_loop
; template <bool ROUTER, bool XBF>
; __device__ __forceinline__ void norm_phase(Frame& F, const void* xin_, const float* g, const float* modl, int sh_off, int sc_off) {
;     ...
;     const int PER = (M + NGW - 1) / NGW, m0 = gw * PER, m1 = (m0 + PER < M) ? m0 + PER : M;
;     f32x4 gs[8], shv[8];
;     if (m0 < M) { const int b = m0 >> 11;
;         const f32x4* gp = (const f32x4*)g + F.lane; const f32x4* scp = (const f32x4*)(modl + (size_t)b * 12288 + sc_off) + F.lane; const f32x4* shp = (const f32x4*)(modl + (size_t)b * 12288 + sh_off) + F.lane;
; #pragma unroll
;         for (int j = 0; j < 8; ++j) { gs[j] = gp[64 * j] * (scp[64 * j] + 1.0f); shv[j] = shp[64 * j]; } }
;     f32x4 vn[8]; v2u vb[8];
;     if (m0 < M) {
;         if (XBF) { const v2u* xr = (const v2u*)((const bf16*)xin_ + (size_t)m0 * DM) + F.lane;
; #pragma unroll
;             for (int j = 0; j < 8; ++j) vb[j] = xr[64 * j]; }
;         else { const f32x4* xr = (const f32x4*)((const float*)xin_ + (size_t)m0 * DM) + F.lane;
; #pragma unroll
;             for (int j = 0; j < 8; ++j) vn[j] = xr[64 * j]; } }
.Lsf0_done:
	s_waitcnt vmcnt(0)
	ds_read_b128 v[160:163], v7 offset:0
	ds_read_b128 v[164:167], v7 offset:1024
	ds_read_b128 v[168:171], v7 offset:2048
	ds_read_b128 v[172:175], v7 offset:3072
	ds_read_b128 v[176:179], v7 offset:4096
	ds_read_b128 v[180:183], v7 offset:5120
	ds_read_b128 v[184:187], v7 offset:6144
	ds_read_b128 v[188:191], v7 offset:7168
	ds_read_b128 v[192:195], v7 offset:8192
	ds_read_b128 v[196:199], v7 offset:9216
	ds_read_b128 v[200:203], v7 offset:10240
	ds_read_b128 v[204:207], v7 offset:11264
	ds_read_b128 v[208:211], v7 offset:12288
	ds_read_b128 v[212:215], v7 offset:13312
	ds_read_b128 v[216:219], v7 offset:14336
	ds_read_b128 v[220:223], v7 offset:15360
.Lsf0_skip:
	s_waitcnt lgkmcnt(0)
	s_barrier
.LBB0_299:
	s_cmp_lt_i32 s68, 2
	s_cselect_b64 s[0:1], -1, 0
	s_add_u32 s47, s86, 0x100000
	s_addc_u32 s4, s87, 0
	v_writelane_b32 v247, s4, 9
	s_and_b64 s[0:1], s[0:1], s[2:3]
	v_readlane_b32 s4, v247, 0
	v_readlane_b32 s5, v247, 1
	s_load_dwordx2 s[4:5], s[4:5], 0x0
	s_andn2_b64 vcc, exec, s[0:1]
	s_waitcnt lgkmcnt(0)
	v_writelane_b32 v247, s4, 10
	s_nop 1
	v_writelane_b32 v247, s5, 11
	s_cbranch_vccnz .LBB0_307
	s_lshl_b32 s2, s82, 3
	s_abs_i32 s3, s2
	v_cvt_f32_u32_e32 v1, s3
	s_sub_i32 s6, 0, s3
	s_add_i32 s5, s2, 0x3fff
	s_xor_b32 s2, s5, s2
	v_rcp_iflag_f32_e32 v1, v1
	s_abs_i32 s5, s5
	s_lshl_b32 s4, s94, 3
	s_add_i32 s4, s4, s77
	v_mul_f32_e32 v1, 0x4f7ffffe, v1
	v_cvt_u32_f32_e32 v1, v1
	s_ashr_i32 s2, s2, 31
	v_readfirstlane_b32 s7, v1
	s_mul_i32 s6, s6, s7
	s_mul_hi_u32 s6, s7, s6
	s_add_i32 s7, s7, s6
	s_mul_hi_u32 s6, s5, s7
	s_mul_i32 s7, s6, s3
	s_sub_i32 s5, s5, s7
	s_add_i32 s8, s6, 1
	s_sub_i32 s7, s5, s3
	s_cmp_ge_u32 s5, s3
	s_cselect_b32 s6, s8, s6
	s_cselect_b32 s5, s7, s5
	s_add_i32 s7, s6, 1
	s_cmp_ge_u32 s5, s3
	s_cselect_b32 s3, s7, s6
	s_xor_b32 s3, s3, s2
	s_sub_i32 s2, s3, s2
	s_mul_i32 s4, s2, s4
	s_cmpk_gt_i32 s4, 0x3fff
	s_cbranch_scc1 .LBB0_302
	v_readlane_b32 s6, v247, 0
	v_readlane_b32 s7, v247, 1
	s_ashr_i32 s3, s4, 11
	s_load_dwordx2 s[6:7], s[6:7], 0x20
	s_mul_hi_i32 s5, s3, 0xc000
	s_mul_i32 s3, s3, 0xc000
	s_add_u32 s8, s47, s3
	v_readlane_b32 s3, v247, 9
	s_waitcnt vmcnt(2)
	v_lshlrev_b32_e32 v34, 4, v186
	v_mov_b32_e32 v35, 0
	s_addc_u32 s9, s3, s5
	v_lshl_add_u64 v[20:21], s[8:9], 0, v[34:35]
	v_add_co_u32_e32 v24, vcc, 0x2000, v20
	s_waitcnt lgkmcnt(0)
	v_lshl_add_u64 v[18:19], s[6:7], 0, v[34:35]
	v_addc_co_u32_e32 v25, vcc, 0, v21, vcc
	s_movk_i32 s3, 0x1000
	v_add_co_u32_e32 v36, vcc, s3, v18
	s_movk_i32 s5, 0x3000
	s_nop 0
	v_addc_co_u32_e32 v37, vcc, 0, v19, vcc
	s_mov_b64 s[10:11], 0x2000
	s_waitcnt vmcnt(0)
	v_add_co_u32_e32 v38, vcc, s5, v20
	s_ashr_i32 s5, s4, 31
	v_lshl_add_u64 v[22:23], v[20:21], 0, s[10:11]
	global_load_dwordx4 v[66:69], v34, s[6:7]
	global_load_dwordx4 v[70:73], v34, s[6:7] offset:1024
	global_load_dwordx4 v[2:5], v34, s[8:9]
	global_load_dwordx4 v[6:9], v34, s[8:9] offset:1024
	global_load_dwordx4 v[74:77], v[22:23], off offset:1024
	global_load_dwordx4 v[78:81], v[22:23], off offset:2048
	global_load_dwordx4 v[82:85], v34, s[6:7] offset:2048
	global_load_dwordx4 v[86:89], v34, s[6:7] offset:3072
	global_load_dwordx4 v[90:93], v[24:25], off
	global_load_dwordx4 v[94:97], v[22:23], off offset:3072
	global_load_dwordx4 v[10:13], v34, s[8:9] offset:2048
	global_load_dwordx4 v[14:17], v34, s[8:9] offset:3072
	s_lshl_b64 s[6:7], s[4:5], 13
	v_readlane_b32 s8, v247, 10
	v_addc_co_u32_e32 v39, vcc, 0, v21, vcc
	v_readlane_b32 s9, v247, 11
	s_add_u32 s6, s8, s6
	v_add_co_u32_e32 v40, vcc, s3, v20
	s_addc_u32 s7, s9, s7
	s_nop 0
	v_addc_co_u32_e32 v41, vcc, 0, v21, vcc
	global_load_dwordx4 v[100:103], v[36:37], off
	global_load_dwordx4 v[126:129], v[36:37], off offset:1024
	global_load_dwordx4 v[104:107], v[38:39], off
	global_load_dwordx4 v[130:133], v[38:39], off offset:1024
	global_load_dwordx4 v[18:21], v[40:41], off
	global_load_dwordx4 v[22:25], v[40:41], off offset:1024
	global_load_dwordx4 v[134:137], v[36:37], off offset:2048
	global_load_dwordx4 v[138:141], v[36:37], off offset:3072
	global_load_dwordx4 v[142:145], v[38:39], off offset:2048
	global_load_dwordx4 v[146:149], v[38:39], off offset:3072
	global_load_dwordx4 v[26:29], v[40:41], off offset:2048
	global_load_dwordx4 v[30:33], v[40:41], off offset:3072
	v_lshl_add_u64 v[36:37], s[6:7], 0, v[34:35]
	global_load_dwordx4 v[62:65], v34, s[6:7]
	global_load_dwordx4 v[58:61], v34, s[6:7] offset:1024
	global_load_dwordx4 v[54:57], v34, s[6:7] offset:2048
	global_load_dwordx4 v[50:53], v34, s[6:7] offset:3072
	v_add_co_u32_e32 v34, vcc, s3, v36
	s_waitcnt vmcnt(23)
	v_pk_add_f32 v[76:77], v[76:77], 1.0 op_sel_hi:[1,0]
	v_addc_co_u32_e32 v35, vcc, 0, v37, vcc
	global_load_dwordx4 v[46:49], v[34:35], off
	global_load_dwordx4 v[42:45], v[34:35], off offset:1024
	global_load_dwordx4 v[38:41], v[34:35], off offset:2048
	s_nop 0
	global_load_dwordx4 v[34:37], v[34:35], off offset:3072
	s_waitcnt vmcnt(23)
	v_pk_add_f32 v[92:93], v[92:93], 1.0 op_sel_hi:[1,0]
	v_pk_add_f32 v[90:91], v[90:91], 1.0 op_sel_hi:[1,0]
	v_pk_mul_f32 v[120:121], v[68:69], v[92:93]
	v_pk_mul_f32 v[112:113], v[66:67], v[90:91]
	v_pk_add_f32 v[74:75], v[74:75], 1.0 op_sel_hi:[1,0]
	v_pk_add_f32 v[80:81], v[80:81], 1.0 op_sel_hi:[1,0]
	s_waitcnt vmcnt(17)
	v_pk_add_f32 v[66:67], v[106:107], 1.0 op_sel_hi:[1,0]
	v_pk_add_f32 v[68:69], v[104:105], 1.0 op_sel_hi:[1,0]
	v_pk_mul_f32 v[122:123], v[102:103], v[66:67]
	v_pk_mul_f32 v[106:107], v[100:101], v[68:69]
	s_waitcnt vmcnt(16)
	v_pk_add_f32 v[66:67], v[132:133], 1.0 op_sel_hi:[1,0]
	v_pk_add_f32 v[68:69], v[130:131], 1.0 op_sel_hi:[1,0]
	v_pk_mul_f32 v[124:125], v[128:129], v[66:67]
	v_pk_mul_f32 v[104:105], v[126:127], v[68:69]
	s_waitcnt vmcnt(11)
	v_pk_add_f32 v[66:67], v[144:145], 1.0 op_sel_hi:[1,0]
	v_pk_add_f32 v[68:69], v[142:143], 1.0 op_sel_hi:[1,0]
	v_pk_add_f32 v[78:79], v[78:79], 1.0 op_sel_hi:[1,0]
	v_pk_mul_f32 v[114:115], v[72:73], v[76:77]
	v_pk_mul_f32 v[110:111], v[70:71], v[74:75]
	v_pk_add_f32 v[70:71], v[96:97], 1.0 op_sel_hi:[1,0]
	v_pk_add_f32 v[72:73], v[94:95], 1.0 op_sel_hi:[1,0]
	v_pk_mul_f32 v[126:127], v[136:137], v[66:67]
	v_pk_mul_f32 v[102:103], v[134:135], v[68:69]
	s_waitcnt vmcnt(10)
	v_pk_add_f32 v[66:67], v[148:149], 1.0 op_sel_hi:[1,0]
	v_pk_add_f32 v[68:69], v[146:147], 1.0 op_sel_hi:[1,0]
	v_pk_mul_f32 v[116:117], v[84:85], v[80:81]
	v_pk_mul_f32 v[98:99], v[82:83], v[78:79]
	v_pk_mul_f32 v[118:119], v[88:89], v[70:71]
	v_pk_mul_f32 v[108:109], v[86:87], v[72:73]
	v_pk_mul_f32 v[128:129], v[140:141], v[66:67]
	v_pk_mul_f32 v[100:101], v[138:139], v[68:69]
	s_add_i32 s2, s4, s2
	s_min_i32 s12, s2, 0x4000
	s_cmp_ge_i32 s4, s12
	s_cbranch_scc0 .LBB0_303
	s_branch .LBB0_307

; __device__ __forceinline__ void xcd_barrier(const XcdBarrier& b) {
;     ...
;     }
;     __syncthreads();
.LBB0_356:
	s_or_b64 exec, exec, s[0:1]
	v_readfirstlane_b32 s4, v0
	s_lshr_b32 s4, s4, 6
	s_cmp_lg_u32 s4, 0
	s_cbranch_scc1 .Lsf1_notw0
	v_mov_b32_e32 v2, 0x20020
	v_mov_b32_e32 v4, 2
	ds_write_b32 v2, v4
	s_branch .Lsf1_skip

; __device__ __forceinline__ void transpose_item_f8(const float* W, int N, unsigned char* WT, int ldt, int kind, int off, int item, int lane, float scale) {
;     const int nblk = N >> 6, kb = item / nblk, nb = item - kb * nblk, k0 = 128 * kb + 16 * (lane & 7), n = 64 * nb + 4 * (lane >> 3);
; __device__ __forceinline__ void moe_convert(Frame& F, int lo, int hi, int rank, int nrank) {
;     ...
;     for (int it = lo + rank; it < hi; it += nrank) {
;         int r = it; const float* W; unsigned char* WT; int N, ldt, kind, off; float f8s;
;         if (r < 14336) { const int e = r / 1792; r -= e * 1792; W = F.in[IN_WMG] + (size_t)e * 2048 * DFFE; N = DFFE; WT = F.ws + WS_WGU1 + (size_t)e * 14336 * 2048; ldt = 2048; kind = 1; off = 0; f8s = 32.f; }
;         else if ((r -= 14336) < 14336) { const int e = r / 1792; r -= e * 1792; W = F.in[IN_WMU] + (size_t)e * 2048 * DFFE; N = DFFE; WT = F.ws + WS_WGU1 + (size_t)e * 14336 * 2048; ldt = 2048; kind = 1; off = 128; f8s = 256.f; }
;         else { r -= 14336; const int e = r / 1792; r -= e * 1792; W = F.in[IN_WMD] + (size_t)e * DFFE * 2048; N = 2048; WT = F.ws + WS_WDN1 + (size_t)e * 2048 * DFFE; ldt = DFFE; kind = 0; off = 0; f8s = 64.f; }
;         transpose_item_f8(W, N, WT, ldt, kind, off, r, F.lane, f8s);
.Lsf1_loop:
	ds_read_b32 v9, v8
	s_waitcnt lgkmcnt(0)
	v_readfirstlane_b32 s5, v9
	s_cmp_eq_u32 s5, 2
	s_cbranch_scc1 .Lsf1_done
	ds_add_rtn_u32 v9, v8, v18 offset:4
	s_waitcnt lgkmcnt(0)
	v_readfirstlane_b32 s18, v9
	s_cmp_ge_u32 s18, 96
	s_cbranch_scc1 .Lsf1_done
	s_add_i32 s18, s18, s33
	s_and_b32 s27, s18, 1
	s_lshr_b32 s19, s18, 1
	s_add_i32 s19, s19, 0x5800
	s_cmp_lt_u32 s19, 0x7000
	s_cbranch_scc0 .Lsf1_down
	s_add_i32 s20, s19, 0xffffc800
	s_lshr_b32 s21, s20, 8
	s_mul_i32 s21, s21, 37
	s_lshr_b32 s21, s21, 8
	s_mul_i32 s28, s21, 0x700
	s_sub_i32 s20, s20, s28
	s_mul_i32 s28, s21, 0x3800000
	s_add_u32 s14, s10, s28
	s_addc_u32 s15, s11, 0
	s_mul_i32 s28, s21, 0x1c00000
	s_add_u32 s28, s28, 0x7800000
	s_add_u32 s16, s86, s28
	s_addc_u32 s17, s87, 0
	s_movk_i32 s24, 0x7000
	s_movk_i32 s25, 0x800
	s_mov_b32 s26, 0x43800000
	s_lshr_b32 s22, s20, 4
	s_mul_i32 s22, s22, 0x2493
	s_lshr_b32 s22, s22, 16
	s_mul_i32 s28, s22, 0x70
	s_sub_i32 s23, s20, s28
	s_mov_b32 s29, 1
	s_branch .Lsf1_dec

; #define PG8_STAGE(bufoff, gbase, voff) do { _Pragma("unroll") for (int _i = 0; _i < 2; ++_i) \
;         __builtin_amdgcn_global_load_lds((const unsigned*)((const char*)(gbase) + (voff)[_i]), (PG8_LAS unsigned*)(lds + (bufoff) + ldsw + _i * 8192), 16, 0, 0); } while (0)
; #define PG8_BAR __builtin_amdgcn_s_barrier()
; template <class Epi, class Sched, bool ALIGN_EPI = false, bool SP2 = false>
; __device__ __forceinline__ void gemm_phase(PG8_LAS unsigned char* lds, const Gemm g, const Sched& S, const Epi& E) {
;     const int tid = threadIdx.x, wid = __builtin_amdgcn_readfirstlane(tid >> 6), lane = tid & 63, wr = wid >> 2, wc = wid & 3, fr = lane & 15, fq = lane >> 4;
;     const int K = g.K, nt = K / BK;
;     unsigned voffA[2], voffB[2];
; #pragma unroll
;     for (int i = 0; i < 2; ++i) { int R, C; stage_rc(tid * 16 + i * 8192, R, C); const int Rb = Epi::PERM ? ((R & ~31) + perm32(R & 31)) : R;
;         voffA[i] = (unsigned)(R * K + C) * 2u; voffB[i] = (unsigned)(Rb * K + C) * 2u; }
;     const size_t kstep = (size_t)(BK * 2);
;     const size_t hstep = (size_t)HALF * K * 2;
;     const size_t tstep = 2 * hstep;
;     const unsigned ldsw = (unsigned)wid * 1024u;
;     const int aoff = lds_byte(wr * 64 + fr, fq * 8), boff = lds_byte(wc * 32 + fr, fq * 8);
;     ...
;     Unit cur, nxt; int ui = 0;
;     if (!S.next(0, cur)) return;
;     int f8_sw = Epi::SCALE_W, f8_sx = Epi::SCALE_X;
;     if constexpr (Epi::FP8) asm volatile("" : "+v"(f8_sw), "+v"(f8_sx));
;     f32x4 acc[2][2][4][2];
; #pragma unroll
;     for (int a = 0; a < 2; ++a)
; #pragma unroll
;         for (int b = 0; b < 2; ++b)
; #pragma unroll
;             for (int m = 0; m < 4; ++m)
; #pragma unroll
;                 for (int n = 0; n < 2; ++n) acc[a][b][m][n] = (f32x4){0.f, 0.f, 0.f, 0.f};
;     bf16x8 At[4][2], B0[2][2], B1[2][2];
;     const char* cA = (const char*)g.A + (size_t)cur.pm * tstep; const char* cB = (const char*)g.Bt + (size_t)cur.pn * tstep;
;     S.a_ready(cur);
;     if constexpr (SP2) {
;         PG8_STAGE(PG8_SB(0, 0), cB, voffB); PG8_STAGE(PG8_SB(0, 1), cB + hstep, voffB); PG8_STAGE(PG8_SA(0, 0), cA, voffA); PG8_STAGE(PG8_SA(0, 1), cA + hstep, voffA);
;         if (wr == 1) PG8_BAR;
.Lsf1_skip:
	s_waitcnt lgkmcnt(0)
	s_barrier
.LBB0_357:
	s_cmp_lt_i32 s68, 3
	s_cselect_b64 s[0:1], -1, 0
	s_add_u32 s70, s86, 0x39800000
	s_addc_u32 s71, s87, 0
	s_add_u32 s4, s86, 0x41c00000
	v_writelane_b32 v247, s47, 12
	s_addc_u32 s5, s87, 0
	v_writelane_b32 v247, s4, 13
	v_lshlrev_b32_e32 v211, 4, v0
	v_lshrrev_b32_e32 v210, 1, v0
	v_writelane_b32 v247, s5, 14
	s_add_u32 s4, s86, 0x41800000
	s_addc_u32 s5, s87, 0
	s_and_b64 s[0:1], s[0:1], s[2:3]
	v_writelane_b32 v247, s4, 15
	s_andn2_b64 vcc, exec, s[0:1]
	s_nop 0
	v_writelane_b32 v247, s5, 16
	s_cbranch_vccnz .LBB0_406
	v_readlane_b32 s5, v247, 6
	s_cmpk_gt_i32 s5, 0x47f
	v_readfirstlane_b32 s3, v0
	s_cbranch_scc1 .LBB0_380
	v_lshrrev_b32_e32 v1, 5, v0
	v_and_b32_e32 v1, 4, v1
	s_waitcnt vmcnt(2)
	v_bfe_u32 v2, v0, 2, 2
	v_and_b32_e32 v13, 24, v210
	v_or_b32_e32 v10, 0x2000, v211
	s_add_u32 s33, s86, 0x200000
	v_or3_b32 v1, v1, v2, v13
	v_lshrrev_b32_e32 v2, 7, v10
	s_movk_i32 s2, 0x60
	s_addc_u32 s38, s87, 0
	v_and_or_b32 v3, v2, s2, v1
	v_bfe_u32 v14, v0, 2, 4
	s_movk_i32 s2, 0x70
	s_ashr_i32 s40, s5, 31
	v_and_or_b32 v2, v2, s2, v14
	s_lshr_b32 s2, s40, 29
	s_add_i32 s2, s5, s2
	s_lshr_b32 s6, s3, 6
	s_ashr_i32 s4, s2, 3
	s_and_b32 s2, s2, -8
	s_lshr_b32 s8, s3, 8
	s_lshl_b32 s39, s6, 10
	s_sub_i32 s2, s5, s2
	s_cmp_lt_i32 s2, 0
	s_movk_i32 s41, 0x91
	s_cselect_b32 s5, s41, 0x90
	s_mul_i32 s2, s2, s5
	s_add_i32 s2, s2, s4
	s_mul_hi_i32 s4, s2, 0x38e38e39
	s_lshr_b32 s5, s4, 31
	s_ashr_i32 s4, s4, 5
	s_add_i32 s4, s4, s5
	s_lshl_b32 s5, s4, 3
	s_mulk_i32 s4, 0x90
	s_sub_i32 s4, s2, s4
	s_sext_i32_i16 s2, s4
	s_bfe_u32 s2, s2, 0x3001c
	s_add_i32 s7, s4, s2
	s_sext_i32_i16 s2, s7
	s_and_b32 s7, s7, 0xfff8
	s_sub_i32 s4, s4, s7
	s_sext_i32_i16 s4, s4
	v_and_b32_e32 v4, 32, v0
	s_lshr_b32 s2, s2, 3
	s_add_i32 s28, s5, s4
	v_bitop3_b32 v11, v211, v4, 48 bitop3:0x6c
	v_and_b32_e32 v12, 64, v0
	s_ashr_i32 s29, s28, 31
	s_bfe_i64 s[10:11], s[2:3], 0x100000
	v_or_b32_e32 v4, v11, v12
	s_lshl_b64 s[4:5], s[28:29], 20
	s_lshl_b64 s[10:11], s[10:11], 20
	v_lshl_or_b32 v132, v2, 12, v4
	v_lshrrev_b32_e32 v2, 3, v0
	s_add_u32 s34, s33, s10
	v_and_or_b32 v1, v2, 32, v1
	s_addc_u32 s35, s38, s11
	s_add_i32 s42, s39, 0
	v_lshl_or_b32 v134, v1, 12, v4
	s_add_i32 m0, s42, 0x10000
	v_lshl_or_b32 v130, v3, 12, v4
	global_load_lds_dwordx4 v134, s[34:35]
	s_add_i32 m0, s42, 0x12000
	s_add_u32 s10, s34, 0x80000
	global_load_lds_dwordx4 v130, s[34:35]
	s_addc_u32 s11, s35, 0
	s_add_i32 m0, s42, 0x14000
	v_and_or_b32 v1, v2, 48, v14
	global_load_lds_dwordx4 v134, s[10:11]
	s_add_i32 m0, s42, 0x16000
	s_add_u32 s30, s70, s4
	s_addc_u32 s31, s71, s5
	s_add_i32 s43, s42, 0x2000
	v_lshl_or_b32 v136, v1, 12, v4
	global_load_lds_dwordx4 v130, s[10:11]
	s_mov_b32 m0, s42
	s_add_u32 s4, s30, 0x80000
	global_load_lds_dwordx4 v136, s[30:31]
	s_mov_b32 m0, s43
	s_addc_u32 s5, s31, 0
	s_add_i32 s44, s42, 0x4000
	global_load_lds_dwordx4 v132, s[30:31]
	s_mov_b32 m0, s44
	s_add_i32 s45, s42, 0x6000
	global_load_lds_dwordx4 v136, s[4:5]
	s_mov_b32 m0, s45
	v_mov_b32_e32 v135, 0
	global_load_lds_dwordx4 v132, s[4:5]
	v_mov_b32_e32 v131, v135
	v_mov_b32_e32 v137, v135
	v_mov_b32_e32 v133, v135
	s_cmp_eq_u32 s8, 1
	s_mov_b32 s46, 0
	s_waitcnt vmcnt(0)
	v_lshl_add_u64 v[8:9], s[34:35], 0, v[134:135]
	v_lshl_add_u64 v[6:7], s[34:35], 0, v[130:131]
	v_lshl_add_u64 v[4:5], s[30:31], 0, v[136:137]
	v_lshl_add_u64 v[2:3], s[30:31], 0, v[132:133]
	s_cselect_b64 s[4:5], -1, 0
	s_cmp_lg_u32 s8, 1
	s_movk_i32 s47, 0x4000
	s_cbranch_scc1 .LBB0_361
	s_barrier

; __device__ __forceinline__ void xcd_barrier(const XcdBarrier& b) {
;     ...
;     }
;     __syncthreads();
.LBB0_455:
	s_or_b64 exec, exec, s[0:1]
	v_readfirstlane_b32 s4, v0
	s_lshr_b32 s4, s4, 6
	s_cmp_lg_u32 s4, 0
	s_cbranch_scc1 .Lsf2_notw0
	v_mov_b32_e32 v2, 0x20020
	v_mov_b32_e32 v4, 3
	ds_write_b32 v2, v4
	s_branch .Lsf2_skip

; __device__ __forceinline__ void transpose_item_f8(const float* W, int N, unsigned char* WT, int ldt, int kind, int off, int item, int lane, float scale) {
;     const int nblk = N >> 6, kb = item / nblk, nb = item - kb * nblk, k0 = 128 * kb + 16 * (lane & 7), n = 64 * nb + 4 * (lane >> 3);
; __device__ __forceinline__ void moe_convert(Frame& F, int lo, int hi, int rank, int nrank) {
;     ...
;     for (int it = lo + rank; it < hi; it += nrank) {
;         int r = it; const float* W; unsigned char* WT; int N, ldt, kind, off; float f8s;
;         if (r < 14336) { const int e = r / 1792; r -= e * 1792; W = F.in[IN_WMG] + (size_t)e * 2048 * DFFE; N = DFFE; WT = F.ws + WS_WGU1 + (size_t)e * 14336 * 2048; ldt = 2048; kind = 1; off = 0; f8s = 32.f; }
;         else if ((r -= 14336) < 14336) { const int e = r / 1792; r -= e * 1792; W = F.in[IN_WMU] + (size_t)e * 2048 * DFFE; N = DFFE; WT = F.ws + WS_WGU1 + (size_t)e * 14336 * 2048; ldt = 2048; kind = 1; off = 128; f8s = 256.f; }
;         else { r -= 14336; const int e = r / 1792; r -= e * 1792; W = F.in[IN_WMD] + (size_t)e * DFFE * 2048; N = 2048; WT = F.ws + WS_WDN1 + (size_t)e * 2048 * DFFE; ldt = DFFE; kind = 0; off = 0; f8s = 64.f; }
;         transpose_item_f8(W, N, WT, ldt, kind, off, r, F.lane, f8s);
.Lsf2_loop:
	ds_read_b32 v9, v8
	s_waitcnt lgkmcnt(0)
	v_readfirstlane_b32 s5, v9
	s_cmp_eq_u32 s5, 3
	s_cbranch_scc1 .Lsf2_done
	ds_add_rtn_u32 v9, v8, v18 offset:4
	s_waitcnt lgkmcnt(0)
	v_readfirstlane_b32 s18, v9
	s_cmp_ge_u32 s18, 96
	s_cbranch_scc1 .Lsf2_done
	s_add_i32 s18, s18, s33
	s_and_b32 s27, s18, 1
	s_lshr_b32 s19, s18, 1
	s_add_i32 s19, s19, 0x5800
	s_cmp_lt_u32 s19, 0x7000
	s_cbranch_scc0 .Lsf2_down
	s_add_i32 s20, s19, 0xffffc800
	s_lshr_b32 s21, s20, 8
	s_mul_i32 s21, s21, 37
	s_lshr_b32 s21, s21, 8
	s_mul_i32 s28, s21, 0x700
	s_sub_i32 s20, s20, s28
	s_mul_i32 s28, s21, 0x3800000
	s_add_u32 s14, s10, s28
	s_addc_u32 s15, s11, 0
	s_mul_i32 s28, s21, 0x1c00000
	s_add_u32 s28, s28, 0x7800000
	s_add_u32 s16, s86, s28
	s_addc_u32 s17, s87, 0
	s_movk_i32 s24, 0x7000
	s_movk_i32 s25, 0x800
	s_mov_b32 s26, 0x43800000
	s_lshr_b32 s22, s20, 4
	s_mul_i32 s22, s22, 0x2493
	s_lshr_b32 s22, s22, 16
	s_mul_i32 s28, s22, 0x70
	s_sub_i32 s23, s20, s28
	s_mov_b32 s29, 1
	s_branch .Lsf2_dec

; #define LAS __attribute__((address_space(3)))
; __device__ __forceinline__ void swa_unit(Frame& F, int l, int unit) {
;     const int b = unit >> 5, kvh = (unit >> 4) & 1, nb = unit & 15;
;     const int tid = F.tid, lane = F.lane, w = F.wave, g = lane >> 4, n = lane & 15;
;     const bf16* proj = (const bf16*)(F.ws + WS_PROJ); bf16* Y = (bf16*)(F.ws + WS_Y);
;     LAS unsigned char* Kt = F.lds + RING_OFF; LAS unsigned char* Vt = Kt + 36864; LAS float* bias = (LAS float*)(Kt + 73728);
;     constexpr int LDB = 144;
;     const int hq = kvh * 8 + w;
;     v4u qn[2][2];
;     const bf16* qbase = proj + (size_t)(b * SEQ + nb * 128 + n) * PROJ_LD + C_AQ + hq * 64 + 8 * g;
; #pragma unroll
;     for (int jt = 0; jt < 2; ++jt) { qn[jt][0] = *(const v4u*)(qbase + (size_t)(jt * 16) * PROJ_LD); qn[jt][1] = *(const v4u*)(qbase + (size_t)(jt * 16) * PROJ_LD + 32); }
;     __syncthreads();
;     {
;         const int r = tid >> 1, hf = tid & 1, pos = nb * 128 - 128 + r;
;         v4u kx[4], vx[4];
;         if (pos >= 0) { const bf16* kp = proj + (size_t)(b * SEQ + pos) * PROJ_LD + C_AK + kvh * 64 + hf * 32; const bf16* vp = proj + (size_t)(b * SEQ + pos) * PROJ_LD + C_AV + kvh * 64 + hf * 32;
; #pragma unroll
;             for (int j = 0; j < 4; ++j) { kx[j] = *(const v4u*)(kp + 8 * j); vx[j] = *(const v4u*)(vp + 8 * j); } }
;         else {
; #pragma unroll
;             for (int j = 0; j < 4; ++j) { kx[j] = (v4u){0u, 0u, 0u, 0u}; vx[j] = (v4u){0u, 0u, 0u, 0u}; } }
;         float kf[32]; float ss = 0.f;
; #pragma unroll
;         for (int j = 0; j < 4; ++j) { kf[8 * j + 0] = bflo(kx[j].x); kf[8 * j + 1] = bfhi(kx[j].x); kf[8 * j + 2] = bflo(kx[j].y); kf[8 * j + 3] = bfhi(kx[j].y); kf[8 * j + 4] = bflo(kx[j].z); kf[8 * j + 5] = bfhi(kx[j].z); kf[8 * j + 6] = bflo(kx[j].w); kf[8 * j + 7] = bfhi(kx[j].w); }
; #pragma unroll
;         for (int i = 0; i < 32; ++i) ss += kf[i] * kf[i];
;         ss += __shfl_xor(ss, 1);
;         const float rstd = 1.0f / sqrtf(ss * (1.0f / 64.0f) + EPS);
;         const float* gk = F.in[IN_GKN] + l * 64 + hf * 32;
; #pragma unroll
;         for (int j = 0; j < 4; ++j) { const f32x4 g0 = *(const f32x4*)(gk + 8 * j), g1 = *(const f32x4*)(gk + 8 * j + 4);
;             v4u o; o.x = pk2(kf[8 * j] * rstd * g0.x, kf[8 * j + 1] * rstd * g0.y); o.y = pk2(kf[8 * j + 2] * rstd * g0.z, kf[8 * j + 3] * rstd * g0.w);
.Lsf2_skip:
	s_waitcnt lgkmcnt(0)
	s_barrier
.LBB0_456:
	s_cmp_lt_i32 s68, 4
	s_cselect_b64 s[0:1], -1, 0
	s_and_b64 s[62:63], s[0:1], s[2:3]
	s_andn2_b64 vcc, exec, s[62:63]
	s_cbranch_vccnz .LBB0_526
	s_cmpk_lt_i32 s94, 0x100
	s_cbranch_scc0 .LBB0_474
	s_waitcnt vmcnt(0)
	v_and_b32_e32 v6, 0x7f, v0
	s_getpc_b64 s[2:3]
	s_add_u32 s2, s2, _ZL9T5_BUCKET@rel32@lo+4
	s_addc_u32 s3, s3, _ZL9T5_BUCKET@rel32@hi+12
	global_load_ubyte v9, v6, s[2:3]
	v_mbcnt_lo_u32_b32 v1, -1, 0
	v_mbcnt_hi_u32_b32 v2, -1, v1
	v_and_b32_e32 v3, 64, v2
	v_xor_b32_e32 v1, 1, v2
	v_add_u32_e32 v3, 64, v3
	v_cmp_lt_i32_e32 vcc, v1, v3
	v_xor_b32_e32 v4, 2, v2
	v_readlane_b32 s2, v247, 0
	v_cndmask_b32_e32 v1, v2, v1, vcc
	v_cmp_lt_i32_e32 vcc, v4, v3
	v_readlane_b32 s3, v247, 1
	s_load_dwordx8 s[36:43], s[2:3], 0x70
	v_cndmask_b32_e32 v4, v2, v4, vcc
	v_lshlrev_b32_e32 v134, 2, v4
	v_xor_b32_e32 v4, 4, v2
	v_cmp_lt_i32_e32 vcc, v4, v3
	s_movk_i32 s0, 0x90
	v_mad_u32_u24 v11, v210, s0, 0
	v_cndmask_b32_e32 v4, v2, v4, vcc
	v_lshlrev_b32_e32 v135, 2, v4
	v_xor_b32_e32 v4, 8, v2
	v_cmp_lt_i32_e32 vcc, v4, v3
	s_lshl_b32 s0, s77, 9
	s_add_i32 s18, 0, 0x12000
	v_cndmask_b32_e32 v4, v2, v4, vcc
	v_lshlrev_b32_e32 v136, 2, v4
	v_xor_b32_e32 v4, 16, v2
	v_cmp_lt_i32_e32 vcc, v4, v3
	s_add_i32 s0, s18, s0
	v_lshlrev_b32_e32 v6, 2, v186
	v_cndmask_b32_e32 v4, v2, v4, vcc
	v_lshlrev_b32_e32 v137, 2, v4
	v_xor_b32_e32 v4, 32, v2
	v_cmp_lt_i32_e32 vcc, v4, v3
	v_and_b32_e32 v139, 15, v0
	v_add_u32_e32 v141, s0, v6
	v_cndmask_b32_e32 v2, v2, v4, vcc
	v_lshlrev_b32_e32 v138, 2, v2
	v_mov_b32_e32 v2, 0
	v_mov_b32_e32 v7, v2
	s_waitcnt lgkmcnt(0)
	v_lshl_add_u64 v[114:115], s[36:37], 0, v[6:7]
	v_lshl_add_u64 v[116:117], s[38:39], 0, v[6:7]
	v_lshrrev_b32_e32 v6, 4, v0
	v_bfe_u32 v7, v0, 4, 3
	v_lshrrev_b32_e32 v15, 7, v0
	s_add_i32 s33, 0, 0x18000
	v_lshl_add_u32 v142, v7, 2, s33
	v_mul_u32_u24_e32 v6, 0x280, v6
	s_add_i32 s10, 0, 0x13000
	v_lshlrev_b32_e32 v12, 7, v7
	v_add_u32_e32 v7, v139, v15
	v_lshlrev_b32_e32 v8, 2, v139
	v_add3_u32 v143, s10, v6, v8
	v_or_b32_e32 v6, 32, v7
	v_sub_u32_e32 v6, v12, v6
	v_lshl_add_u32 v144, v6, 2, s18
	v_or_b32_e32 v6, 64, v7
	v_sub_u32_e32 v6, v12, v6
	v_lshl_add_u32 v145, v6, 2, s18
	v_sub_u32_e32 v6, v12, v7
	v_lshl_add_u32 v146, v6, 2, s18
	v_or_b32_e32 v6, 0x60, v7
	v_lshrrev_b32_e32 v3, 4, v186
	v_sub_u32_e32 v6, v12, v6
	v_cmp_lt_u32_e64 s[4:5], 15, v7
	v_lshl_add_u32 v148, v6, 2, s18
	v_or_b32_e32 v13, 0x80, v7
	v_add_u32_e32 v16, 0x70, v7
	v_lshlrev_b32_e32 v6, 5, v3
	v_mov_b32_e32 v7, v2
	s_lshl_b32 s8, s77, 2
	v_lshl_add_u64 v[118:119], s[36:37], 0, v[6:7]
	v_lshlrev_b32_e32 v6, 2, v3
	v_lshlrev_b32_e32 v4, 3, v3
	s_add_i32 s33, s33, s8
	v_sub_co_u32_e64 v3, s[8:9], v6, v139
	v_add_u32_e32 v3, 15, v3
	v_lshlrev_b32_e32 v7, 3, v3
	v_and_b32_e32 v7, 24, v7
	s_movk_i32 s0, 0x280
	v_add_u32_e32 v7, s77, v7
	v_lshlrev_b32_e32 v3, 2, v3
	s_movk_i32 s6, 0x80
	v_mul_lo_u32 v7, v7, s0
	v_and_b32_e32 v3, -16, v3
	v_and_b32_e32 v5, 1, v0
	v_cmp_gt_u32_e64 s[6:7], s6, v16
	v_add3_u32 v149, s10, v7, v3
	v_bfe_u32 v3, v0, 2, 4
	v_lshlrev_b32_e32 v7, 3, v0
	v_or_b32_e32 v10, 2, v6
	v_sub_u32_e32 v16, v12, v16
	v_sub_u32_e32 v12, v12, v13
	v_and_b32_e32 v8, 48, v0
	v_and_b32_e32 v7, 24, v7
	v_cmp_gt_u32_e64 s[14:15], v10, v139
	v_or_b32_e32 v10, 3, v6
	v_lshl_add_u32 v153, v12, 2, s18
	v_lshlrev_b32_e32 v12, 7, v5
	v_mov_b32_e32 v13, v2
	s_waitcnt vmcnt(0)
	v_lshl_or_b32 v154, v9, 4, v15
	v_mov_b32_e32 v9, v2
	v_mul_u32_u24_e32 v3, 0x90, v3
	v_lshlrev_b32_e32 v14, 6, v5
	v_cmp_gt_u32_e64 s[16:17], v10, v139
	v_lshlrev_b32_e32 v10, 5, v5
	v_lshl_add_u32 v152, v16, 2, s18
	v_lshl_add_u64 v[120:121], s[38:39], 0, v[12:13]
	v_lshl_add_u32 v156, v0, 2, s18
	v_lshl_add_u64 v[12:13], s[86:87], 0, v[8:9]
	s_mov_b64 s[18:19], 0x41c45800
	v_add3_u32 v157, v3, v7, 0
	v_mul_u32_u24_e32 v3, 0x90, v139
	s_mov_b32 s1, 0
	v_lshlrev_b32_e32 v1, 2, v1
	v_add_u32_e32 v140, 0xffffff80, v210
	v_cmp_eq_u32_e64 s[2:3], 0, v186
	v_add_u32_e32 v147, 0xfffffec0, v146
	v_cmp_gt_u32_e64 s[10:11], v6, v139
	v_cmp_ge_u32_e64 s[12:13], v6, v139
	v_subrev_u32_e32 v150, 64, v146
	v_add_u32_e32 v151, 0xffffff40, v146
	v_or_b32_e32 v155, 0xfffffe00, v0
	v_lshl_add_u64 v[122:123], v[12:13], 0, s[18:19]
	s_lshl_b32 s48, s94, 6
	s_lshl_b32 s49, s82, 6
	s_lshl_b32 s50, s77, 6
	v_add3_u32 v158, v3, v8, 0
	s_movk_i32 s51, 0x2200
	v_lshlrev_b32_e32 v124, 1, v4
	s_mov_b64 s[30:31], 0x1800
	s_movk_i32 s52, 0x1000
	v_lshlrev_b32_e32 v126, 1, v10
	s_mov_b64 s[34:35], 0x2000
	s_mov_b64 s[36:37], 0x2100
	v_add_u32_e32 v159, v11, v14
	v_mov_b32_e32 v160, 0x358637bd
	s_mov_b32 s53, 0xf800000
	v_mov_b32_e32 v161, 0x260
	s_mov_b32 s54, 0x3e38aa3b
	v_lshlrev_b32_e32 v128, 1, v6
	s_mov_b64 s[38:39], 0x3d800800
	s_mov_b32 s55, 0x3d800000
	s_mov_b64 s[44:45], 0x44000
	s_mov_b32 s56, s94
	s_mov_b32 s57, s94
	s_branch .LBB0_460

; __device__ __forceinline__ void xcd_barrier(const XcdBarrier& b) {
;     ...
;     }
;     __syncthreads();
.LBB0_575:
	s_or_b64 exec, exec, s[2:3]
	v_readfirstlane_b32 s4, v0
	s_lshr_b32 s4, s4, 6
	s_cmp_lg_u32 s4, 0
	s_cbranch_scc1 .Lsf3_notw0
	v_mov_b32_e32 v2, 0x20020
	v_mov_b32_e32 v4, 4
	ds_write_b32 v2, v4
	s_branch .Lsf3_skip

; __device__ __forceinline__ void transpose_item_f8(const float* W, int N, unsigned char* WT, int ldt, int kind, int off, int item, int lane, float scale) {
;     const int nblk = N >> 6, kb = item / nblk, nb = item - kb * nblk, k0 = 128 * kb + 16 * (lane & 7), n = 64 * nb + 4 * (lane >> 3);
; __device__ __forceinline__ void moe_convert(Frame& F, int lo, int hi, int rank, int nrank) {
;     ...
;     for (int it = lo + rank; it < hi; it += nrank) {
;         int r = it; const float* W; unsigned char* WT; int N, ldt, kind, off; float f8s;
;         if (r < 14336) { const int e = r / 1792; r -= e * 1792; W = F.in[IN_WMG] + (size_t)e * 2048 * DFFE; N = DFFE; WT = F.ws + WS_WGU1 + (size_t)e * 14336 * 2048; ldt = 2048; kind = 1; off = 0; f8s = 32.f; }
;         else if ((r -= 14336) < 14336) { const int e = r / 1792; r -= e * 1792; W = F.in[IN_WMU] + (size_t)e * 2048 * DFFE; N = DFFE; WT = F.ws + WS_WGU1 + (size_t)e * 14336 * 2048; ldt = 2048; kind = 1; off = 128; f8s = 256.f; }
;         else { r -= 14336; const int e = r / 1792; r -= e * 1792; W = F.in[IN_WMD] + (size_t)e * DFFE * 2048; N = 2048; WT = F.ws + WS_WDN1 + (size_t)e * 2048 * DFFE; ldt = DFFE; kind = 0; off = 0; f8s = 64.f; }
;         transpose_item_f8(W, N, WT, ldt, kind, off, r, F.lane, f8s);
.Lsf3_loop:
	ds_read_b32 v9, v8
	s_waitcnt lgkmcnt(0)
	v_readfirstlane_b32 s5, v9
	s_cmp_eq_u32 s5, 4
	s_cbranch_scc1 .Lsf3_done
	ds_add_rtn_u32 v9, v8, v18 offset:4
	s_waitcnt lgkmcnt(0)
	v_readfirstlane_b32 s18, v9
	s_cmp_ge_u32 s18, 96
	s_cbranch_scc1 .Lsf3_done
	s_add_i32 s18, s18, s33
	s_and_b32 s27, s18, 1
	s_lshr_b32 s19, s18, 1
	s_add_i32 s19, s19, 0x5800
	s_cmp_lt_u32 s19, 0x7000
	s_cbranch_scc0 .Lsf3_down
	s_add_i32 s20, s19, 0xffffc800
	s_lshr_b32 s21, s20, 8
	s_mul_i32 s21, s21, 37
	s_lshr_b32 s21, s21, 8
	s_mul_i32 s28, s21, 0x700
	s_sub_i32 s20, s20, s28
	s_mul_i32 s28, s21, 0x3800000
	s_add_u32 s14, s10, s28
	s_addc_u32 s15, s11, 0
	s_mul_i32 s28, s21, 0x1c00000
	s_add_u32 s28, s28, 0x7800000
	s_add_u32 s16, s86, s28
	s_addc_u32 s17, s87, 0
	s_movk_i32 s24, 0x7000
	s_movk_i32 s25, 0x800
	s_mov_b32 s26, 0x43800000
	s_lshr_b32 s22, s20, 4
	s_mul_i32 s22, s22, 0x2493
	s_lshr_b32 s22, s22, 16
	s_mul_i32 s28, s22, 0x70
	s_sub_i32 s23, s20, s28
	s_mov_b32 s29, 1
	s_branch .Lsf3_dec

; #define LAS __attribute__((address_space(3)))
; __device__ __forceinline__ void mlstm_out_group(Frame& F, int l, int ug) {
;     const int bh = ug >> 3, jj = ug & 7, b = bh >> 2, h = bh & 3;
;     const int tid = F.tid, lane = F.lane, w = F.wave, g = lane >> 4, n = lane & 15;
;     const bf16* proj = (const bf16*)(F.ws + WS_PROJ); const float* side = (const float*)(F.ws + WS_SIDE); const bf16* qkc = (const bf16*)(F.ws + WS_QKC); bf16* Y = (bf16*)(F.ws + WS_Y);
;     const float* UM = (const float*)(F.ws + WS_UM); const float* MS = UM + (size_t)512 * 136 * 64;
;     LAS unsigned char* QC = F.lds + RING_OFF; LAS unsigned char* KC = QC + 18432; LAS unsigned char* VT = QC + 36864; LAS unsigned char* CS = QC + 71680;
;     LAS float* GF = (LAS float*)(QC + 92416);
;     float C[16], nn = 0.f, mst = 0.f;
; #pragma unroll
;     for (int i = 0; i < 16; ++i) C[i] = 0.f;
;     const int cv = tid >> 2, ck = (tid & 3) * 16;
;     int cdone = 0;
;     const float* gout = F.in[IN_GOUTM] + l * 512 + h * 128;
; #pragma clang loop unroll(disable)
;     for (int oi = 0; oi < 2; ++oi) {
;         asm volatile("" : "+s"(proj), "+s"(side), "+s"(qkc), "+s"(Y), "+s"(UM), "+s"(MS), "+s"(gout));
.Lsf3_skip:
	s_waitcnt lgkmcnt(0)
	s_barrier
.LBB0_576:
	s_cmp_lt_i32 s68, 5
	s_cselect_b64 s[2:3], -1, 0
	s_add_u32 s4, s86, 0x3d800000
	s_addc_u32 s5, s87, 0
	s_and_b64 s[2:3], s[2:3], s[0:1]
	v_writelane_b32 v247, s4, 17
	s_cmpk_lt_i32 s94, 0x100
	s_cselect_b64 s[0:1], -1, 0
	v_writelane_b32 v247, s5, 18
	v_writelane_b32 v247, s0, 19
	v_and_b32_e32 v212, 15, v0
	v_lshrrev_b32_e32 v1, 2, v0
	v_writelane_b32 v247, s1, 20
	v_writelane_b32 v247, s2, 21
	s_and_b64 s[0:1], s[2:3], s[0:1]
	s_andn2_b64 vcc, exec, s[0:1]
	v_writelane_b32 v247, s3, 22
	v_writelane_b32 v247, s77, 23
	v_writelane_b32 v247, s72, 24
	v_and_b32_e32 v215, 3, v0
	v_cmp_gt_u32_e64 s[4:5], 64, v0
	v_lshlrev_b32_e32 v213, 1, v0
	v_cmp_gt_u32_e64 s[6:7], 2, v186
	v_cmp_gt_u32_e64 s[8:9], 4, v186
	v_cmp_gt_u32_e64 s[10:11], 8, v186
	v_cmp_gt_u32_e64 s[2:3], 16, v186
	v_cmp_gt_u32_e64 s[12:13], 32, v186
	v_lshrrev_b32_e32 v214, 2, v186
	v_and_b32_e32 v188, 48, v0
	v_writelane_b32 v247, s73, 25
	v_writelane_b32 v247, s80, 26
	s_cbranch_vccnz .LBB0_679
; #define LAS __attribute__((address_space(3)))
; #define MFMA16(a, b, c) __builtin_amdgcn_mfma_f32_16x16x32_bf16((a), (b), (c), 0, 0, 0)
; __device__ __forceinline__ void mlstm_out_group(Frame& F, int l, int ug) {
;     ...
;         for (int prep = 0; prep < PROBE_SUBREP(210); ++prep) {
;             const int j = 16 * w + n; const float Mj = GF[128 + j], bj = GF[256 + j];
;             const size_t row = (size_t)(t0 + j);
;             v2u mx8[8];
; #pragma unroll
;             for (int mt = 0; mt < 8; ++mt) { const int v = 16 * mt + 4 * g; mx8[mt] = *(const v2u*)(proj + row * PROJ_LD + C_MO + h * 128 + v); }
;             bf16x8 qf[2];
; #pragma unroll
;             for (int ks = 0; ks < 2; ++ks) qf[ks] = frag_row(QC, 144, 16 * w, 32 * ks, lane);
;             f32x4 p[8];
; #pragma unroll
;             for (int st = 0; st < 8; ++st) { p[st] = (f32x4){0.f, 0.f, 0.f, 0.f};
;                 if (st <= w) {
; #pragma unroll
;                     for (int ks = 0; ks < 2; ++ks) p[st] = MFMA16(frag_row(KC, 144, 16 * st, 32 * ks, lane), qf[ks], p[st]);
;                     const f32x4 as = *(const LAS f32x4*)(GF + 16 * st + 4 * g);
; #pragma unroll
;                     for (int r = 0; r < 4; ++r) { const float e = __expf(as[r] - Mj); p[st][r] = (st < w || 4 * g + r <= n) ? p[st][r] * e : 0.f; } } }
;             f32x4 o[9];
;             const float wi = __expf(mst - Mj);
; #pragma unroll
;             for (int mt = 0; mt < 9; ++mt) { o[mt] = (f32x4){0.f, 0.f, 0.f, 0.f};
; #pragma unroll
;                 for (int ks = 0; ks < 2; ++ks) o[mt] = MFMA16(frag_row(CS, 144, 16 * mt, 32 * ks, lane), qf[ks], o[mt]);
;                 o[mt] = o[mt] * wi; }
;             const bf16x8 ones = (n == 0) ? pack8(1.f, 1.f, 1.f, 1.f, 1.f, 1.f, 1.f, 1.f) : pack8(0.f, 0.f, 0.f, 0.f, 0.f, 0.f, 0.f, 0.f);
; #pragma unroll
;             for (int kk = 0; kk < 4; ++kk) { if (2 * kk <= w) {
;                 const bf16x8 pf = pack8(p[2 * kk][0], p[2 * kk][1], p[2 * kk][2], p[2 * kk][3], p[2 * kk + 1][0], p[2 * kk + 1][1], p[2 * kk + 1][2], p[2 * kk + 1][3]);
; #pragma unroll
;                 for (int mt = 0; mt < 8; ++mt) o[mt] = MFMA16(frag_tr2(VT, 272, 32 * kk, 32 * kk + 16, 16 * mt, lane), pf, o[mt]);
;                 o[8] = MFMA16(ones, pf, o[8]); } }
	v_writelane_b32 v247, s71, 27
	s_add_u32 s0, s86, 0x4ac00000
	v_writelane_b32 v247, s70, 28
	s_addc_u32 s1, s87, 0
	v_writelane_b32 v247, s0, 30
	v_and_b32_e32 v124, 12, v214
	v_lshl_or_b32 v125, s77, 4, v212
	v_writelane_b32 v247, s1, 31
	s_add_u32 s0, s86, 0x4dc00000
	s_addc_u32 s1, s87, 0
	v_writelane_b32 v247, s0, 32
	s_waitcnt vmcnt(0)
	v_or_b32_e32 v12, 2, v124
	s_movk_i32 s19, 0x90
	v_writelane_b32 v247, s1, 33
	s_add_u32 s0, s86, 0x4ed00000
	s_addc_u32 s1, s87, 0
	v_writelane_b32 v247, s0, 34
	s_add_i32 s18, 0, 0x11800
	s_add_i32 s20, 0, 0x16900
	v_writelane_b32 v247, s1, 35
	s_cmp_gt_u32 s80, 63
	v_readlane_b32 s0, v247, 0
	v_readlane_b32 s1, v247, 1
	s_load_dwordx2 s[0:1], s[0:1], 0x50
	v_mov_b32_e32 v3, s18
	v_lshl_add_u32 v155, v0, 2, s20
	s_cselect_b64 s[72:73], -1, 0
	s_cmp_lt_u32 s80, 64
	s_waitcnt lgkmcnt(0)
	v_writelane_b32 v247, s0, 36
	v_lshl_add_u32 v157, v125, 2, s20
	v_lshl_add_u32 v158, v124, 2, s20
	v_writelane_b32 v247, s1, 37
	s_movk_i32 s0, 0x80
	v_cmp_eq_u32_e32 vcc, 0, v212
	v_mov_b32_e32 v11, 0x3f803f80
	v_cmp_gt_u32_e64 s[20:21], v12, v212
	v_or_b32_e32 v12, 3, v214
	v_cmp_gt_u32_e64 s[14:15], s0, v0
	v_mad_u32_u24 v3, v1, s19, v3
	v_mad_u32_u24 v154, v1, s19, 0
	s_cselect_b64 s[0:1], -1, 0
	v_mul_lo_u32 v6, v125, s19
	v_add_u32_e32 v8, s18, v188
	v_cndmask_b32_e32 v50, 0, v11, vcc
	v_cmp_gt_u32_e32 vcc, v124, v212
	v_cmp_ge_u32_e64 s[18:19], v124, v212
	v_cmp_gt_u32_e64 s[22:23], v12, v212
	s_and_b64 s[74:75], s[0:1], vcc
	s_mov_b32 s25, s77
	s_and_b64 s[76:77], s[0:1], s[18:19]
	s_and_b64 s[56:57], s[0:1], s[20:21]
	s_and_b64 s[54:55], s[0:1], s[22:23]
	s_cmp_eq_u32 s25, 1
	s_cselect_b64 s[0:1], -1, 0
	s_and_b64 s[26:27], s[0:1], vcc
	v_writelane_b32 v247, s26, 38
	s_mov_b32 s24, s94
	v_lshlrev_b32_e32 v156, 3, v186
	v_writelane_b32 v247, s27, 39
	s_and_b64 s[26:27], s[0:1], s[18:19]
	v_writelane_b32 v247, s26, 40
	v_and_or_b32 v9, v1, 3, v124
	v_and_b32_e32 v10, 24, v156
	v_writelane_b32 v247, s27, 41
	s_and_b64 s[26:27], s[0:1], s[20:21]
	v_writelane_b32 v247, s26, 42
	s_and_b64 s[0:1], s[0:1], s[22:23]
	s_cmpk_gt_u32 s80, 0x7f
	v_writelane_b32 v247, s27, 43
	v_writelane_b32 v247, s0, 44
	s_mov_b32 s26, s80
	s_cselect_b64 s[80:81], -1, 0
	s_cmp_eq_u32 s25, 2
	v_writelane_b32 v247, s1, 45
	s_cselect_b64 s[0:1], -1, 0
	s_and_b64 s[28:29], s[0:1], vcc
	v_writelane_b32 v247, s28, 46
	v_lshlrev_b32_e32 v2, 4, v215
	v_or_b32_e32 v13, 0x800, v213
	v_writelane_b32 v247, s29, 47
	s_and_b64 s[28:29], s[0:1], s[18:19]
	v_writelane_b32 v247, s28, 48
	v_lshlrev_b32_e32 v126, 1, v2
	v_or_b32_e32 v14, 0xc00, v213
	v_writelane_b32 v247, s29, 49
	s_and_b64 s[28:29], s[0:1], s[20:21]
	v_writelane_b32 v247, s28, 50
	s_and_b64 s[0:1], s[0:1], s[22:23]
	s_cmpk_gt_u32 s26, 0xbf
	v_writelane_b32 v247, s29, 51
	v_writelane_b32 v247, s0, 52
	s_cselect_b64 s[58:59], -1, 0
	s_cmp_eq_u32 s25, 3
	v_writelane_b32 v247, s1, 53
	s_cselect_b64 s[0:1], -1, 0
	s_and_b64 s[28:29], s[0:1], vcc
	v_writelane_b32 v247, s28, 54
	v_mov_b32_e32 v119, 0
	v_lshlrev_b32_e32 v120, 5, v215
	v_writelane_b32 v247, s29, 55
	s_and_b64 s[28:29], s[0:1], s[18:19]
	v_writelane_b32 v247, s28, 56
	s_mov_b32 s83, 0
	v_lshl_add_u32 v4, v1, 7, v154
	v_writelane_b32 v247, s29, 57
	s_and_b64 s[28:29], s[0:1], s[20:21]
	v_writelane_b32 v247, s28, 58
	s_and_b64 s[0:1], s[0:1], s[22:23]
	s_cmpk_gt_u32 s26, 0xff
	v_writelane_b32 v247, s29, 59
	v_writelane_b32 v247, s0, 60
	s_cselect_b64 s[44:45], -1, 0
	s_cmp_eq_u32 s25, 4
	v_writelane_b32 v247, s1, 61
	s_cselect_b64 s[0:1], -1, 0
	s_and_b64 s[28:29], s[0:1], vcc
	v_writelane_b32 v247, s28, 62
	v_lshlrev_b32_e32 v5, 6, v215
	v_add_u32_e32 v6, 0, v6
	v_writelane_b32 v247, s29, 63
	s_and_b64 s[28:29], s[0:1], s[18:19]
	v_writelane_b32 v246, s28, 0
	v_add_u32_e32 v7, 0, v188
	v_mul_u32_u24_e32 v11, 0x90, v212
	v_writelane_b32 v246, s29, 1
	s_and_b64 s[28:29], s[0:1], s[20:21]
	v_writelane_b32 v246, s28, 2
	s_and_b64 s[0:1], s[0:1], s[22:23]
	s_cmpk_gt_u32 s26, 0x13f
	v_writelane_b32 v246, s29, 3
	v_writelane_b32 v246, s0, 4
	s_cselect_b64 s[94:95], -1, 0
	s_cmp_eq_u32 s25, 5
	v_writelane_b32 v246, s1, 5
	s_cselect_b64 s[0:1], -1, 0
	s_and_b64 s[28:29], s[0:1], vcc
	v_writelane_b32 v246, s28, 6
	v_add_u32_e32 v161, 0, v213
	v_lshlrev_b32_e32 v122, 6, v1
	v_writelane_b32 v246, s29, 7
	s_and_b64 s[28:29], s[0:1], s[18:19]
	v_writelane_b32 v246, s28, 8
	v_cmp_eq_u32_e64 s[16:17], 0, v186
	v_mov_b32_e32 v51, v50
	v_writelane_b32 v246, s29, 9
	s_and_b64 s[28:29], s[0:1], s[20:21]
	v_writelane_b32 v246, s28, 10
	s_and_b64 s[0:1], s[0:1], s[22:23]
	s_cmpk_gt_u32 s26, 0x17f
	v_writelane_b32 v246, s29, 11
	v_writelane_b32 v246, s0, 12
	s_cselect_b64 s[64:65], -1, 0
	s_cmp_eq_u32 s25, 6
	v_writelane_b32 v246, s1, 13
	s_cselect_b64 s[0:1], -1, 0
	s_and_b64 s[28:29], s[0:1], vcc
	s_and_b64 s[40:41], s[0:1], s[18:19]
	s_and_b64 s[42:43], s[0:1], s[20:21]
	s_and_b64 s[48:49], s[0:1], s[22:23]
	s_cmpk_gt_u32 s26, 0x1bf
	s_cselect_b64 s[52:53], -1, 0
	s_cmp_eq_u32 s25, 7
	s_cselect_b64 s[0:1], -1, 0
	s_and_b64 s[50:51], s[0:1], vcc
	s_and_b64 s[78:79], s[0:1], s[18:19]
	s_and_b64 s[30:31], s[0:1], s[20:21]
	s_and_b64 s[60:61], s[0:1], s[22:23]
	s_movk_i32 s0, 0x110
	v_mad_u32_u24 v9, v9, s0, 0
	v_add_u32_e32 v12, 0x9000, v9
	v_add_u32_e32 v159, v9, v10
	v_sub_u32_e32 v9, 0x437, v0
	v_lshrrev_b32_e32 v9, 9, v9
	v_writelane_b32 v246, s28, 14
	v_cmp_ne_u32_e64 s[18:19], 0, v9
	v_cmp_lt_u32_e64 s[20:21], 1, v9
	v_cmp_lt_u32_e64 s[22:23], 2, v9
	v_or_b32_e32 v9, 0x400, v213
	v_writelane_b32 v246, s29, 15
	v_add_u32_e32 v2, 0, v9
	s_mov_b32 s0, s24
	v_add_u32_e32 v163, 0x16090, v2
	v_add_u32_e32 v2, 0, v13
	v_writelane_b32 v246, s0, 16
	v_add_u32_e32 v164, 0x16090, v2
	v_add_u32_e32 v2, 0, v14
	v_writelane_b32 v246, s1, 17
	v_mov_b32_e32 v52, v50
	v_mov_b32_e32 v53, v50
	v_mov_b32_e32 v128, v126
	v_mov_b32_e32 v129, v119
	s_movk_i32 s33, 0x2200
	v_lshlrev_b32_e32 v130, 1, v120
	v_mov_b32_e32 v131, v119
	v_add_u32_e32 v160, v3, v120
	v_add_u32_e32 v162, 0x16000, v161
	v_add_u32_e32 v165, 0x16090, v2
	v_add_u32_e32 v166, v4, v5
	v_lshlrev_b32_e32 v132, 1, v124
	v_add_u32_e32 v167, v6, v188
	v_add_u32_e32 v168, v8, v11
	v_add_u32_e32 v169, v12, v10
	v_mov_b32_e32 v170, 0x358637bd
	v_mov_b32_e32 v171, 0x260
	v_mov_b32_e32 v172, 0x41b17218
	v_mbcnt_lo_u32_b32 v173, -1, 0
	v_mov_b32_e32 v174, 0xff800000
	v_add_u32_e32 v121, v7, v11
	s_mov_b32 s25, s24
	v_writelane_b32 v246, s82, 18
	s_nop 1
	v_writelane_b32 v246, s83, 19
	s_branch .LBB0_579

; __device__ __forceinline__ void xcd_barrier(const XcdBarrier& b) {
;     ...
;     }
;     __syncthreads();
.LBB0_728:
	s_or_b64 exec, exec, s[2:3]
	v_readfirstlane_b32 s4, v0
	s_lshr_b32 s4, s4, 6
	s_cmp_lg_u32 s4, 0
	s_cbranch_scc1 .Lsf4_notw0
	v_mov_b32_e32 v2, 0x20020
	v_mov_b32_e32 v4, 5
	ds_write_b32 v2, v4
	s_branch .Lsf4_skip

; __device__ __forceinline__ void transpose_item_f8(const float* W, int N, unsigned char* WT, int ldt, int kind, int off, int item, int lane, float scale) {
;     const int nblk = N >> 6, kb = item / nblk, nb = item - kb * nblk, k0 = 128 * kb + 16 * (lane & 7), n = 64 * nb + 4 * (lane >> 3);
; __device__ __forceinline__ void moe_convert(Frame& F, int lo, int hi, int rank, int nrank) {
;     ...
;     for (int it = lo + rank; it < hi; it += nrank) {
;         int r = it; const float* W; unsigned char* WT; int N, ldt, kind, off; float f8s;
;         if (r < 14336) { const int e = r / 1792; r -= e * 1792; W = F.in[IN_WMG] + (size_t)e * 2048 * DFFE; N = DFFE; WT = F.ws + WS_WGU1 + (size_t)e * 14336 * 2048; ldt = 2048; kind = 1; off = 0; f8s = 32.f; }
;         else if ((r -= 14336) < 14336) { const int e = r / 1792; r -= e * 1792; W = F.in[IN_WMU] + (size_t)e * 2048 * DFFE; N = DFFE; WT = F.ws + WS_WGU1 + (size_t)e * 14336 * 2048; ldt = 2048; kind = 1; off = 128; f8s = 256.f; }
;         else { r -= 14336; const int e = r / 1792; r -= e * 1792; W = F.in[IN_WMD] + (size_t)e * DFFE * 2048; N = 2048; WT = F.ws + WS_WDN1 + (size_t)e * 2048 * DFFE; ldt = DFFE; kind = 0; off = 0; f8s = 64.f; }
;         transpose_item_f8(W, N, WT, ldt, kind, off, r, F.lane, f8s);
.Lsf4_loop:
	ds_read_b32 v9, v8
	s_waitcnt lgkmcnt(0)
	v_readfirstlane_b32 s5, v9
	s_cmp_eq_u32 s5, 5
	s_cbranch_scc1 .Lsf4_done
	ds_add_rtn_u32 v9, v8, v18 offset:4
	s_waitcnt lgkmcnt(0)
	v_readfirstlane_b32 s18, v9
	s_cmp_ge_u32 s18, 96
	s_cbranch_scc1 .Lsf4_done
	s_add_i32 s18, s18, s33
	s_and_b32 s27, s18, 1
	s_lshr_b32 s19, s18, 1
	s_add_i32 s19, s19, 0x5800
	s_cmp_lt_u32 s19, 0x7000
	s_cbranch_scc0 .Lsf4_down
	s_add_i32 s20, s19, 0xffffc800
	s_lshr_b32 s21, s20, 8
	s_mul_i32 s21, s21, 37
	s_lshr_b32 s21, s21, 8
	s_mul_i32 s28, s21, 0x700
	s_sub_i32 s20, s20, s28
	s_mul_i32 s28, s21, 0x3800000
	s_add_u32 s14, s10, s28
	s_addc_u32 s15, s11, 0
	s_mul_i32 s28, s21, 0x1c00000
	s_add_u32 s28, s28, 0x7800000
	s_add_u32 s16, s86, s28
	s_addc_u32 s17, s87, 0
	s_movk_i32 s24, 0x7000
	s_movk_i32 s25, 0x800
	s_mov_b32 s26, 0x43800000
	s_lshr_b32 s22, s20, 4
	s_mul_i32 s22, s22, 0x2493
	s_lshr_b32 s22, s22, 16
	s_mul_i32 s28, s22, 0x70
	s_sub_i32 s23, s20, s28
	s_mov_b32 s29, 1
	s_branch .Lsf4_dec

;     __host__ __device__ bool next(int i, Unit& u) const {
;         const long L = (long)i * G + c; if (L >= nwg) return false;
;         int wgid = (int)L; { const int q = nwg / NXCD, r = nwg % NXCD, xcd = wgid % NXCD, off = wgid / NXCD; wgid = (xcd < r ? xcd * (q + 1) : r * (q + 1) + (xcd - r) * q) + off; }
;         const int nig = WGM * nN, gid = wgid / nig, fm = gid * WGM, gsz = (nM - fm) < WGM ? (nM - fm) : WGM;
;         u.pm = fm + ((wgid % nig) % gsz); u.pn = (wgid % nig) / gsz; return true;
.Lsf4_skip:
	s_waitcnt lgkmcnt(0)
	s_barrier
.LBB0_729:
	s_cmp_lt_i32 s68, 6
	s_cselect_b64 s[2:3], -1, 0
	s_add_u32 s66, s86, 0x31800000
	s_addc_u32 s67, s87, 0
	s_and_b64 s[0:1], s[2:3], s[0:1]
	s_andn2_b64 vcc, exec, s[0:1]
	s_cbranch_vccnz .LBB0_754
	v_readlane_b32 s2, v247, 6
	s_cmpk_gt_i32 s2, 0x1ff
	v_readfirstlane_b32 s8, v0
	s_cbranch_scc1 .LBB0_754
	v_readlane_b32 s3, v247, 6
	s_ashr_i32 s33, s3, 31
	s_lshr_b32 s2, s33, 29
	s_add_i32 s5, s3, s2
	s_and_b32 s2, s5, -8
	s_sub_i32 s6, s3, s2
	s_cmp_gt_i32 s6, -1
	s_cbranch_scc0 .LBB0_733
	s_lshl_b32 s4, s6, 6
	s_cbranch_execz .LBB0_734
	s_branch .LBB0_735

; __device__ __forceinline__ void xcd_barrier(const XcdBarrier& b) {
;     ...
;     }
;     __syncthreads();
.LBB0_803:
	s_or_b64 exec, exec, s[0:1]
	v_readfirstlane_b32 s4, v0
	s_lshr_b32 s4, s4, 6
	s_cmp_lg_u32 s4, 0
	s_cbranch_scc1 .Lsf5_notw0
	v_mov_b32_e32 v2, 0x20020
	v_mov_b32_e32 v4, 6
	ds_write_b32 v2, v4
	s_branch .Lsf5_skip

; __device__ __forceinline__ void transpose_item_f8(const float* W, int N, unsigned char* WT, int ldt, int kind, int off, int item, int lane, float scale) {
;     const int nblk = N >> 6, kb = item / nblk, nb = item - kb * nblk, k0 = 128 * kb + 16 * (lane & 7), n = 64 * nb + 4 * (lane >> 3);
; __device__ __forceinline__ void moe_convert(Frame& F, int lo, int hi, int rank, int nrank) {
;     ...
;     for (int it = lo + rank; it < hi; it += nrank) {
;         int r = it; const float* W; unsigned char* WT; int N, ldt, kind, off; float f8s;
;         if (r < 14336) { const int e = r / 1792; r -= e * 1792; W = F.in[IN_WMG] + (size_t)e * 2048 * DFFE; N = DFFE; WT = F.ws + WS_WGU1 + (size_t)e * 14336 * 2048; ldt = 2048; kind = 1; off = 0; f8s = 32.f; }
;         else if ((r -= 14336) < 14336) { const int e = r / 1792; r -= e * 1792; W = F.in[IN_WMU] + (size_t)e * 2048 * DFFE; N = DFFE; WT = F.ws + WS_WGU1 + (size_t)e * 14336 * 2048; ldt = 2048; kind = 1; off = 128; f8s = 256.f; }
;         else { r -= 14336; const int e = r / 1792; r -= e * 1792; W = F.in[IN_WMD] + (size_t)e * DFFE * 2048; N = 2048; WT = F.ws + WS_WDN1 + (size_t)e * 2048 * DFFE; ldt = DFFE; kind = 0; off = 0; f8s = 64.f; }
;         transpose_item_f8(W, N, WT, ldt, kind, off, r, F.lane, f8s);
.Lsf5_loop:
	ds_read_b32 v9, v8
	s_waitcnt lgkmcnt(0)
	v_readfirstlane_b32 s5, v9
	s_cmp_eq_u32 s5, 6
	s_cbranch_scc1 .Lsf5_done
	ds_add_rtn_u32 v9, v8, v18 offset:4
	s_waitcnt lgkmcnt(0)
	v_readfirstlane_b32 s18, v9
	s_cmp_ge_u32 s18, 96
	s_cbranch_scc1 .Lsf5_done
	s_add_i32 s18, s18, s33
	s_and_b32 s27, s18, 1
	s_lshr_b32 s19, s18, 1
	s_add_i32 s19, s19, 0x5800
	s_cmp_lt_u32 s19, 0x7000
	s_cbranch_scc0 .Lsf5_down
	s_add_i32 s20, s19, 0xffffc800
	s_lshr_b32 s21, s20, 8
	s_mul_i32 s21, s21, 37
	s_lshr_b32 s21, s21, 8
	s_mul_i32 s28, s21, 0x700
	s_sub_i32 s20, s20, s28
	s_mul_i32 s28, s21, 0x3800000
	s_add_u32 s14, s10, s28
	s_addc_u32 s15, s11, 0
	s_mul_i32 s28, s21, 0x1c00000
	s_add_u32 s28, s28, 0x7800000
	s_add_u32 s16, s86, s28
	s_addc_u32 s17, s87, 0
	s_movk_i32 s24, 0x7000
	s_movk_i32 s25, 0x800
	s_mov_b32 s26, 0x43800000
	s_lshr_b32 s22, s20, 4
	s_mul_i32 s22, s22, 0x2493
	s_lshr_b32 s22, s22, 16
	s_mul_i32 s28, s22, 0x70
	s_sub_i32 s23, s20, s28
	s_mov_b32 s29, 1
	s_branch .Lsf5_dec

; template <bool ROUTER, bool XBF>
; __device__ __forceinline__ void norm_phase(Frame& F, const void* xin_, const float* g, const float* modl, int sh_off, int sc_off) {
;     ...
;     const int PER = (M + NGW - 1) / NGW, m0 = gw * PER, m1 = (m0 + PER < M) ? m0 + PER : M;
;     f32x4 gs[8], shv[8];
;     if (m0 < M) { const int b = m0 >> 11;
;         const f32x4* gp = (const f32x4*)g + F.lane; const f32x4* scp = (const f32x4*)(modl + (size_t)b * 12288 + sc_off) + F.lane; const f32x4* shp = (const f32x4*)(modl + (size_t)b * 12288 + sh_off) + F.lane;
; #pragma unroll
;         for (int j = 0; j < 8; ++j) { gs[j] = gp[64 * j] * (scp[64 * j] + 1.0f); shv[j] = shp[64 * j]; } }
;     f32x4 vn[8]; v2u vb[8];
;     if (m0 < M) {
;         if (XBF) { const v2u* xr = (const v2u*)((const bf16*)xin_ + (size_t)m0 * DM) + F.lane;
; #pragma unroll
;             for (int j = 0; j < 8; ++j) vb[j] = xr[64 * j]; }
;         else { const f32x4* xr = (const f32x4*)((const float*)xin_ + (size_t)m0 * DM) + F.lane;
; #pragma unroll
;             for (int j = 0; j < 8; ++j) vn[j] = xr[64 * j]; } }
.Lsf5_skip:
	s_waitcnt lgkmcnt(0)
	s_barrier
.LBB0_804:
	s_cmp_lt_i32 s68, 7
	s_cselect_b64 s[0:1], -1, 0
	s_and_b64 s[0:1], s[0:1], s[2:3]
	s_andn2_b64 vcc, exec, s[0:1]
	s_cbranch_vccnz .LBB0_812
	s_lshl_b32 s2, s82, 3
	s_abs_i32 s3, s2
	s_waitcnt vmcnt(0)
	v_cvt_f32_u32_e32 v2, s3
	s_sub_i32 s6, 0, s3
	s_add_i32 s5, s2, 0x3fff
	s_xor_b32 s2, s5, s2
	v_rcp_iflag_f32_e32 v2, v2
	s_abs_i32 s5, s5
	s_lshl_b32 s4, s94, 3
	s_add_i32 s4, s4, s77
	v_mul_f32_e32 v2, 0x4f7ffffe, v2
	v_cvt_u32_f32_e32 v2, v2
	s_ashr_i32 s2, s2, 31
	v_readfirstlane_b32 s7, v2
	s_mul_i32 s6, s6, s7
	s_mul_hi_u32 s6, s7, s6
	s_add_i32 s7, s7, s6
	s_mul_hi_u32 s6, s5, s7
	s_mul_i32 s7, s6, s3
	s_sub_i32 s5, s5, s7
	s_add_i32 s8, s6, 1
	s_sub_i32 s7, s5, s3
	s_cmp_ge_u32 s5, s3
	s_cselect_b32 s6, s8, s6
	s_cselect_b32 s5, s7, s5
	s_add_i32 s7, s6, 1
	s_cmp_ge_u32 s5, s3
	s_cselect_b32 s3, s7, s6
	s_xor_b32 s3, s3, s2
	s_sub_i32 s2, s3, s2
	s_mul_i32 s4, s2, s4
	s_cmpk_gt_i32 s4, 0x3fff
	s_cbranch_scc1 .LBB0_807
	s_ashr_i32 s3, s4, 11
	v_readlane_b32 s6, v247, 0
	s_mul_hi_i32 s5, s3, 0xc000
	s_mul_i32 s3, s3, 0xc000
	v_readlane_b32 s8, v247, 12
	v_readlane_b32 s7, v247, 1
	s_add_u32 s8, s8, s3
	v_readlane_b32 s3, v247, 9
	s_load_dwordx2 s[6:7], s[6:7], 0x28
	v_lshlrev_b32_e32 v14, 4, v186
	v_mov_b32_e32 v15, 0
	s_addc_u32 s9, s3, s5
	v_lshl_add_u64 v[2:3], s[8:9], 0, v[14:15]
	s_mov_b32 s3, 0x9000
	v_add_co_u32_e32 v54, vcc, s3, v2
	s_mov_b64 s[8:9], 0x8000
	s_nop 0
	v_addc_co_u32_e32 v55, vcc, 0, v3, vcc
	s_movk_i32 s3, 0x7000
	v_lshl_add_u64 v[18:19], v[2:3], 0, s[8:9]
	s_mov_b64 s[8:9], 0x6000
	v_add_co_u32_e32 v64, vcc, s3, v2
	s_ashr_i32 s5, s4, 31
	s_waitcnt lgkmcnt(0)
	v_lshl_add_u64 v[16:17], s[6:7], 0, v[14:15]
	v_lshl_add_u64 v[20:21], v[2:3], 0, s[8:9]
	global_load_dwordx4 v[34:37], v[54:55], off offset:-4096
	v_addc_co_u32_e32 v65, vcc, 0, v3, vcc
	global_load_dwordx4 v[38:41], v14, s[6:7]
	global_load_dwordx4 v[42:45], v14, s[6:7] offset:1024
	global_load_dwordx4 v[46:49], v[18:19], off offset:1024
	global_load_dwordx4 v[50:53], v[18:19], off offset:2048
	global_load_dwordx4 v[56:59], v14, s[6:7] offset:2048
	global_load_dwordx4 v[60:63], v14, s[6:7] offset:3072
	global_load_dwordx4 v[6:9], v[20:21], off offset:1024
	global_load_dwordx4 v[82:85], v[18:19], off offset:3072
	global_load_dwordx4 v[2:5], v[20:21], off offset:2048
	global_load_dwordx4 v[10:13], v[20:21], off offset:3072
	s_movk_i32 s3, 0x1000
	s_lshl_b64 s[6:7], s[4:5], 12
	v_add_co_u32_e32 v66, vcc, s3, v16
	s_add_u32 s6, s66, s6
	s_nop 0
	v_addc_co_u32_e32 v67, vcc, 0, v17, vcc
	global_load_dwordx4 v[86:89], v[54:55], off
	global_load_dwordx4 v[90:93], v[66:67], off
	global_load_dwordx4 v[94:97], v[66:67], off offset:1024
	global_load_dwordx4 v[14:17], v[64:65], off
	global_load_dwordx4 v[18:21], v[64:65], off offset:1024
	global_load_dwordx4 v[98:101], v[54:55], off offset:1024
	global_load_dwordx4 v[102:105], v[54:55], off offset:2048
	global_load_dwordx4 v[106:109], v[66:67], off offset:2048
	global_load_dwordx4 v[110:113], v[66:67], off offset:3072
	global_load_dwordx4 v[30:33], v[64:65], off offset:-4096
	global_load_dwordx4 v[114:117], v[54:55], off offset:3072
	global_load_dwordx4 v[22:25], v[64:65], off offset:2048
	global_load_dwordx4 v[26:29], v[64:65], off offset:3072
	s_addc_u32 s7, s67, s7
	v_lshlrev_b32_e32 v54, 3, v186
	global_load_dwordx2 v[80:81], v54, s[6:7]
	global_load_dwordx2 v[78:79], v54, s[6:7] offset:512
	global_load_dwordx2 v[76:77], v54, s[6:7] offset:1024
	global_load_dwordx2 v[74:75], v54, s[6:7] offset:1536
	global_load_dwordx2 v[72:73], v54, s[6:7] offset:2048
	global_load_dwordx2 v[70:71], v54, s[6:7] offset:2560
	global_load_dwordx2 v[68:69], v54, s[6:7] offset:3072
	global_load_dwordx2 v[66:67], v54, s[6:7] offset:3584
	s_waitcnt vmcnt(28)
	v_pk_add_f32 v[54:55], v[48:49], 1.0 op_sel_hi:[1,0]
	v_pk_add_f32 v[46:47], v[46:47], 1.0 op_sel_hi:[1,0]
	s_waitcnt vmcnt(27)
	v_pk_add_f32 v[118:119], v[50:51], 1.0 op_sel_hi:[1,0]
	v_pk_mul_f32 v[46:47], v[42:43], v[46:47]
	v_pk_add_f32 v[34:35], v[34:35], 1.0 op_sel_hi:[1,0]
	v_pk_add_f32 v[36:37], v[36:37], 1.0 op_sel_hi:[1,0]
	s_waitcnt vmcnt(23)
	v_pk_add_f32 v[82:83], v[82:83], 1.0 op_sel_hi:[1,0]
	v_pk_mul_f32 v[48:49], v[38:39], v[34:35]
	s_waitcnt vmcnt(15)
	v_pk_add_f32 v[34:35], v[100:101], 1.0 op_sel_hi:[1,0]
	v_pk_add_f32 v[84:85], v[84:85], 1.0 op_sel_hi:[1,0]
	v_pk_mul_f32 v[50:51], v[40:41], v[36:37]
	v_pk_mul_f32 v[42:43], v[60:61], v[82:83]
	v_pk_add_f32 v[36:37], v[98:99], 1.0 op_sel_hi:[1,0]
	v_pk_mul_f32 v[60:61], v[96:97], v[34:35]
	s_waitcnt vmcnt(14)
	v_pk_add_f32 v[34:35], v[104:105], 1.0 op_sel_hi:[1,0]
	v_pk_add_f32 v[64:65], v[52:53], 1.0 op_sel_hi:[1,0]
	v_pk_add_f32 v[88:89], v[88:89], 1.0 op_sel_hi:[1,0]
	v_pk_add_f32 v[86:87], v[86:87], 1.0 op_sel_hi:[1,0]
	v_pk_mul_f32 v[52:53], v[44:45], v[54:55]
	v_pk_mul_f32 v[44:45], v[56:57], v[118:119]
	v_pk_mul_f32 v[56:57], v[62:63], v[84:85]
	v_pk_mul_f32 v[38:39], v[94:95], v[36:37]
	v_pk_add_f32 v[36:37], v[102:103], 1.0 op_sel_hi:[1,0]
	s_waitcnt vmcnt(13)
	v_pk_mul_f32 v[62:63], v[108:109], v[34:35]
	s_waitcnt vmcnt(10)
	v_pk_add_f32 v[34:35], v[116:117], 1.0 op_sel_hi:[1,0]
	v_pk_add_f32 v[82:83], v[114:115], 1.0 op_sel_hi:[1,0]
	v_pk_mul_f32 v[54:55], v[58:59], v[64:65]
	v_pk_mul_f32 v[58:59], v[92:93], v[88:89]
	v_pk_mul_f32 v[40:41], v[90:91], v[86:87]
	v_pk_mul_f32 v[36:37], v[106:107], v[36:37]
	v_pk_mul_f32 v[64:65], v[112:113], v[34:35]
	v_pk_mul_f32 v[34:35], v[110:111], v[82:83]
	s_add_i32 s2, s4, s2
	s_min_i32 s10, s2, 0x4000
	s_cmp_ge_i32 s4, s10
	s_cbranch_scc0 .LBB0_808
	s_branch .LBB0_812

; __device__ __forceinline__ void xcd_barrier(const XcdBarrier& b) {
;     ...
;     }
;     __syncthreads();
.LBB0_861:
	s_or_b64 exec, exec, s[0:1]
	v_readfirstlane_b32 s4, v0
	s_lshr_b32 s4, s4, 6
	s_cmp_lg_u32 s4, 0
	s_cbranch_scc1 .Lsf6_notw0
	v_mov_b32_e32 v2, 0x20020
	v_mov_b32_e32 v4, 7
	ds_write_b32 v2, v4
	s_branch .Lsf6_skip

; __device__ __forceinline__ void transpose_item_f8(const float* W, int N, unsigned char* WT, int ldt, int kind, int off, int item, int lane, float scale) {
;     const int nblk = N >> 6, kb = item / nblk, nb = item - kb * nblk, k0 = 128 * kb + 16 * (lane & 7), n = 64 * nb + 4 * (lane >> 3);
; __device__ __forceinline__ void moe_convert(Frame& F, int lo, int hi, int rank, int nrank) {
;     ...
;     for (int it = lo + rank; it < hi; it += nrank) {
;         int r = it; const float* W; unsigned char* WT; int N, ldt, kind, off; float f8s;
;         if (r < 14336) { const int e = r / 1792; r -= e * 1792; W = F.in[IN_WMG] + (size_t)e * 2048 * DFFE; N = DFFE; WT = F.ws + WS_WGU1 + (size_t)e * 14336 * 2048; ldt = 2048; kind = 1; off = 0; f8s = 32.f; }
;         else if ((r -= 14336) < 14336) { const int e = r / 1792; r -= e * 1792; W = F.in[IN_WMU] + (size_t)e * 2048 * DFFE; N = DFFE; WT = F.ws + WS_WGU1 + (size_t)e * 14336 * 2048; ldt = 2048; kind = 1; off = 128; f8s = 256.f; }
;         else { r -= 14336; const int e = r / 1792; r -= e * 1792; W = F.in[IN_WMD] + (size_t)e * DFFE * 2048; N = 2048; WT = F.ws + WS_WDN1 + (size_t)e * 2048 * DFFE; ldt = DFFE; kind = 0; off = 0; f8s = 64.f; }
;         transpose_item_f8(W, N, WT, ldt, kind, off, r, F.lane, f8s);
.Lsf6_loop:
	ds_read_b32 v9, v8
	s_waitcnt lgkmcnt(0)
	v_readfirstlane_b32 s5, v9
	s_cmp_eq_u32 s5, 7
	s_cbranch_scc1 .Lsf6_done
	ds_add_rtn_u32 v9, v8, v18 offset:4
	s_waitcnt lgkmcnt(0)
	v_readfirstlane_b32 s18, v9
	s_cmp_ge_u32 s18, 96
	s_cbranch_scc1 .Lsf6_done
	s_add_i32 s18, s18, s33
	s_and_b32 s27, s18, 1
	s_lshr_b32 s19, s18, 1
	s_add_i32 s19, s19, 0x5800
	s_cmp_lt_u32 s19, 0x7000
	s_cbranch_scc0 .Lsf6_down
	s_add_i32 s20, s19, 0xffffc800
	s_lshr_b32 s21, s20, 8
	s_mul_i32 s21, s21, 37
	s_lshr_b32 s21, s21, 8
	s_mul_i32 s28, s21, 0x700
	s_sub_i32 s20, s20, s28
	s_mul_i32 s28, s21, 0x3800000
	s_add_u32 s14, s10, s28
	s_addc_u32 s15, s11, 0
	s_mul_i32 s28, s21, 0x1c00000
	s_add_u32 s28, s28, 0x7800000
	s_add_u32 s16, s86, s28
	s_addc_u32 s17, s87, 0
	s_movk_i32 s24, 0x7000
	s_movk_i32 s25, 0x800
	s_mov_b32 s26, 0x43800000
	s_lshr_b32 s22, s20, 4
	s_mul_i32 s22, s22, 0x2493
	s_lshr_b32 s22, s22, 16
	s_mul_i32 s28, s22, 0x70
	s_sub_i32 s23, s20, s28
	s_mov_b32 s29, 1
	s_branch .Lsf6_dec

; #define PG8_STAGE(bufoff, gbase, voff) do { _Pragma("unroll") for (int _i = 0; _i < 2; ++_i) \
;         __builtin_amdgcn_global_load_lds((const unsigned*)((const char*)(gbase) + (voff)[_i]), (PG8_LAS unsigned*)(lds + (bufoff) + ldsw + _i * 8192), 16, 0, 0); } while (0)
; #define PG8_BAR __builtin_amdgcn_s_barrier()
; template <class Epi, class Sched, bool ALIGN_EPI = false, bool SP2 = false>
; __device__ __forceinline__ void gemm_phase(PG8_LAS unsigned char* lds, const Gemm g, const Sched& S, const Epi& E) {
;     const int tid = threadIdx.x, wid = __builtin_amdgcn_readfirstlane(tid >> 6), lane = tid & 63, wr = wid >> 2, wc = wid & 3, fr = lane & 15, fq = lane >> 4;
;     const int K = g.K, nt = K / BK;
;     unsigned voffA[2], voffB[2];
; #pragma unroll
;     for (int i = 0; i < 2; ++i) { int R, C; stage_rc(tid * 16 + i * 8192, R, C); const int Rb = Epi::PERM ? ((R & ~31) + perm32(R & 31)) : R;
;         voffA[i] = (unsigned)(R * K + C) * 2u; voffB[i] = (unsigned)(Rb * K + C) * 2u; }
;     const size_t kstep = (size_t)(BK * 2);
;     const size_t hstep = (size_t)HALF * K * 2;
;     const size_t tstep = 2 * hstep;
;     const unsigned ldsw = (unsigned)wid * 1024u;
;     const int aoff = lds_byte(wr * 64 + fr, fq * 8), boff = lds_byte(wc * 32 + fr, fq * 8);
;     ...
;     Unit cur, nxt; int ui = 0;
;     if (!S.next(0, cur)) return;
;     int f8_sw = Epi::SCALE_W, f8_sx = Epi::SCALE_X;
;     if constexpr (Epi::FP8) asm volatile("" : "+v"(f8_sw), "+v"(f8_sx));
;     f32x4 acc[2][2][4][2];
; #pragma unroll
;     for (int a = 0; a < 2; ++a)
; #pragma unroll
;         for (int b = 0; b < 2; ++b)
; #pragma unroll
;             for (int m = 0; m < 4; ++m)
; #pragma unroll
;                 for (int n = 0; n < 2; ++n) acc[a][b][m][n] = (f32x4){0.f, 0.f, 0.f, 0.f};
;     bf16x8 At[4][2], B0[2][2], B1[2][2];
;     const char* cA = (const char*)g.A + (size_t)cur.pm * tstep; const char* cB = (const char*)g.Bt + (size_t)cur.pn * tstep;
;     S.a_ready(cur);
;     if constexpr (SP2) {
;         PG8_STAGE(PG8_SB(0, 0), cB, voffB); PG8_STAGE(PG8_SB(0, 1), cB + hstep, voffB); PG8_STAGE(PG8_SA(0, 0), cA, voffA); PG8_STAGE(PG8_SA(0, 1), cA + hstep, voffA);
;         if (wr == 1) PG8_BAR;
.Lsf6_skip:
	s_waitcnt lgkmcnt(0)
	s_barrier
.LBB0_862:
	s_cmp_lt_i32 s68, 8
	s_cselect_b64 s[0:1], -1, 0
	s_and_b64 s[0:1], s[0:1], s[2:3]
	s_andn2_b64 vcc, exec, s[0:1]
	s_cbranch_vccnz .LBB0_879
	v_readlane_b32 s2, v247, 6
	s_cmpk_gt_i32 s2, 0xaff
	v_readfirstlane_b32 s3, v0
	s_cbranch_scc1 .LBB0_879
	s_waitcnt vmcnt(0)
	v_lshrrev_b32_e32 v2, 5, v0
	v_and_b32_e32 v2, 4, v2
	v_bfe_u32 v3, v0, 2, 2
	v_and_b32_e32 v13, 24, v210
	v_or_b32_e32 v10, 0x2000, v211
	s_add_u32 s11, s86, 0x3600000
	v_or3_b32 v2, v2, v3, v13
	v_lshrrev_b32_e32 v3, 7, v10
	s_movk_i32 s2, 0x60
	v_readlane_b32 s5, v247, 6
	s_addc_u32 s28, s87, 0
	v_and_or_b32 v4, v3, s2, v2
	v_bfe_u32 v14, v0, 2, 4
	s_movk_i32 s2, 0x70
	s_ashr_i32 s30, s5, 31
	v_and_or_b32 v3, v3, s2, v14
	s_lshr_b32 s2, s30, 29
	s_add_i32 s2, s5, s2
	s_lshr_b32 s6, s3, 6
	s_ashr_i32 s4, s2, 3
	s_and_b32 s2, s2, -8
	s_lshr_b32 s8, s3, 8
	s_lshl_b32 s29, s6, 10
	s_sub_i32 s2, s5, s2
	s_cmp_lt_i32 s2, 0
	s_movk_i32 s31, 0x161
	s_cselect_b32 s5, s31, 0x160
	s_mul_i32 s2, s2, s5
	s_add_i32 s2, s2, s4
	s_mul_hi_i32 s4, s2, 0x2e8ba2e9
	s_lshr_b32 s5, s4, 31
	s_ashr_i32 s4, s4, 6
	s_add_i32 s4, s4, s5
	s_lshl_b32 s5, s4, 3
	s_mulk_i32 s4, 0x160
	s_sub_i32 s4, s2, s4
	s_sext_i32_i16 s2, s4
	s_bfe_u32 s2, s2, 0x3001c
	s_add_i32 s7, s4, s2
	s_sext_i32_i16 s2, s7
	s_and_b32 s7, s7, 0xfff8
	s_sub_i32 s4, s4, s7
	s_sext_i32_i16 s4, s4
	v_and_b32_e32 v5, 32, v0
	s_lshr_b32 s2, s2, 3
	s_add_i32 s20, s5, s4
	v_bitop3_b32 v11, v211, v5, 48 bitop3:0x6c
	v_and_b32_e32 v12, 64, v0
	s_ashr_i32 s21, s20, 31
	s_bfe_i64 s[12:13], s[2:3], 0x100000
	v_or_b32_e32 v5, v11, v12
	s_lshl_b64 s[4:5], s[20:21], 20
	s_lshl_b64 s[12:13], s[12:13], 20
	v_lshl_or_b32 v132, v3, 12, v5
	v_lshrrev_b32_e32 v3, 3, v0
	s_add_u32 s24, s11, s12
	v_and_or_b32 v2, v3, 32, v2
	s_addc_u32 s25, s28, s13
	s_add_i32 s21, s29, 0
	v_lshl_or_b32 v134, v2, 12, v5
	s_add_i32 m0, s21, 0x10000
	v_lshl_or_b32 v130, v4, 12, v5
	global_load_lds_dwordx4 v134, s[24:25]
	s_add_i32 m0, s21, 0x12000
	s_add_u32 s12, s24, 0x80000
	global_load_lds_dwordx4 v130, s[24:25]
	s_addc_u32 s13, s25, 0
	s_add_i32 m0, s21, 0x14000
	v_and_or_b32 v2, v3, 48, v14
	global_load_lds_dwordx4 v134, s[12:13]
	s_add_i32 m0, s21, 0x16000
	s_add_u32 s22, s70, s4
	s_addc_u32 s23, s71, s5
	s_add_i32 s33, s21, 0x2000
	v_lshl_or_b32 v136, v2, 12, v5
	global_load_lds_dwordx4 v130, s[12:13]
	s_mov_b32 m0, s21
	s_add_u32 s4, s22, 0x80000
	global_load_lds_dwordx4 v136, s[22:23]
	s_mov_b32 m0, s33
	s_addc_u32 s5, s23, 0
	s_add_i32 s34, s21, 0x4000
	global_load_lds_dwordx4 v132, s[22:23]
	s_mov_b32 m0, s34
	s_add_i32 s35, s21, 0x6000
	global_load_lds_dwordx4 v136, s[4:5]
	s_mov_b32 m0, s35
	v_mov_b32_e32 v135, 0
	global_load_lds_dwordx4 v132, s[4:5]
	v_mov_b32_e32 v131, v135
	v_mov_b32_e32 v137, v135
	v_mov_b32_e32 v133, v135
	s_cmp_eq_u32 s8, 1
	s_mov_b32 s36, 0
	v_lshl_add_u64 v[8:9], s[24:25], 0, v[134:135]
	v_lshl_add_u64 v[6:7], s[24:25], 0, v[130:131]
	v_lshl_add_u64 v[2:3], s[22:23], 0, v[136:137]
	s_cselect_b64 s[4:5], -1, 0
	s_cmp_lg_u32 s8, 1
	v_lshl_add_u64 v[4:5], s[22:23], 0, v[132:133]
	s_cbranch_scc1 .LBB0_866
	s_barrier

; __device__ __forceinline__ void xcd_barrier(const XcdBarrier& b) {
;     ...
;     }
;     __syncthreads();
.LBB0_928:
	s_or_b64 exec, exec, s[0:1]
	v_readfirstlane_b32 s4, v0
	s_lshr_b32 s4, s4, 6
	s_cmp_lg_u32 s4, 0
	s_cbranch_scc1 .Lsf7_notw0
	v_mov_b32_e32 v2, 0x20020
	v_mov_b32_e32 v4, 8
	ds_write_b32 v2, v4
	s_branch .Lsf7_skip

; __device__ __forceinline__ void transpose_item_f8(const float* W, int N, unsigned char* WT, int ldt, int kind, int off, int item, int lane, float scale) {
;     const int nblk = N >> 6, kb = item / nblk, nb = item - kb * nblk, k0 = 128 * kb + 16 * (lane & 7), n = 64 * nb + 4 * (lane >> 3);
; __device__ __forceinline__ void moe_convert(Frame& F, int lo, int hi, int rank, int nrank) {
;     ...
;     for (int it = lo + rank; it < hi; it += nrank) {
;         int r = it; const float* W; unsigned char* WT; int N, ldt, kind, off; float f8s;
;         if (r < 14336) { const int e = r / 1792; r -= e * 1792; W = F.in[IN_WMG] + (size_t)e * 2048 * DFFE; N = DFFE; WT = F.ws + WS_WGU1 + (size_t)e * 14336 * 2048; ldt = 2048; kind = 1; off = 0; f8s = 32.f; }
;         else if ((r -= 14336) < 14336) { const int e = r / 1792; r -= e * 1792; W = F.in[IN_WMU] + (size_t)e * 2048 * DFFE; N = DFFE; WT = F.ws + WS_WGU1 + (size_t)e * 14336 * 2048; ldt = 2048; kind = 1; off = 128; f8s = 256.f; }
;         else { r -= 14336; const int e = r / 1792; r -= e * 1792; W = F.in[IN_WMD] + (size_t)e * DFFE * 2048; N = 2048; WT = F.ws + WS_WDN1 + (size_t)e * 2048 * DFFE; ldt = DFFE; kind = 0; off = 0; f8s = 64.f; }
;         transpose_item_f8(W, N, WT, ldt, kind, off, r, F.lane, f8s);
.Lsf7_loop:
	ds_read_b32 v9, v8
	s_waitcnt lgkmcnt(0)
	v_readfirstlane_b32 s5, v9
	s_cmp_eq_u32 s5, 8
	s_cbranch_scc1 .Lsf7_done
	ds_add_rtn_u32 v9, v8, v18 offset:4
	s_waitcnt lgkmcnt(0)
	v_readfirstlane_b32 s18, v9
	s_cmp_ge_u32 s18, 96
	s_cbranch_scc1 .Lsf7_done
	s_add_i32 s18, s18, s33
	s_and_b32 s27, s18, 1
	s_lshr_b32 s19, s18, 1
	s_add_i32 s19, s19, 0x5800
	s_cmp_lt_u32 s19, 0x7000
	s_cbranch_scc0 .Lsf7_down
	s_add_i32 s20, s19, 0xffffc800
	s_lshr_b32 s21, s20, 8
	s_mul_i32 s21, s21, 37
	s_lshr_b32 s21, s21, 8
	s_mul_i32 s28, s21, 0x700
	s_sub_i32 s20, s20, s28
	s_mul_i32 s28, s21, 0x3800000
	s_add_u32 s14, s10, s28
	s_addc_u32 s15, s11, 0
	s_mul_i32 s28, s21, 0x1c00000
	s_add_u32 s28, s28, 0x7800000
	s_add_u32 s16, s86, s28
	s_addc_u32 s17, s87, 0
	s_movk_i32 s24, 0x7000
	s_movk_i32 s25, 0x800
	s_mov_b32 s26, 0x43800000
	s_lshr_b32 s22, s20, 4
	s_mul_i32 s22, s22, 0x2493
	s_lshr_b32 s22, s22, 16
	s_mul_i32 s28, s22, 0x70
	s_sub_i32 s23, s20, s28
	s_mov_b32 s29, 1
	s_branch .Lsf7_dec

;     __host__ __device__ bool next(int i, Unit& u) const {
;         const long L = (long)i * G + c; if (L >= nwg) return false;
;         int wgid = (int)L; { const int q = nwg / NXCD, r = nwg % NXCD, xcd = wgid % NXCD, off = wgid / NXCD; wgid = (xcd < r ? xcd * (q + 1) : r * (q + 1) + (xcd - r) * q) + off; }
;         const int nig = WGM * nN, gid = wgid / nig, fm = gid * WGM, gsz = (nM - fm) < WGM ? (nM - fm) : WGM;
;         u.pm = fm + ((wgid % nig) % gsz); u.pn = (wgid % nig) / gsz; return true;
.Lsf7_skip:
	s_waitcnt lgkmcnt(0)
	s_barrier
.LBB0_929:
	s_cmp_lt_i32 s68, 9
	s_cselect_b64 s[0:1], -1, 0
	s_add_u32 s4, s86, 0x35800000
	s_addc_u32 s5, s87, 0
	s_and_b64 s[0:1], s[0:1], s[2:3]
	v_writelane_b32 v247, s4, 30
	s_andn2_b64 vcc, exec, s[0:1]
	s_nop 0
	v_writelane_b32 v247, s5, 31
	s_cbranch_vccnz .LBB0_958
	v_readlane_b32 s2, v247, 6
	s_cmpk_gt_i32 s2, 0x1ff
	v_readfirstlane_b32 s4, v0
	s_cbranch_scc1 .LBB0_958
	v_readlane_b32 s3, v247, 6
	s_ashr_i32 s20, s3, 31
	s_lshr_b32 s2, s20, 29
	s_add_i32 s6, s3, s2
	s_and_b32 s2, s6, -8
	s_sub_i32 s7, s3, s2
	s_cmp_gt_i32 s7, -1
	s_cbranch_scc0 .LBB0_933
	s_lshl_b32 s5, s7, 6
	s_cbranch_execz .LBB0_934
	s_branch .LBB0_935

; __device__ __forceinline__ void xcd_barrier(const XcdBarrier& b) {
;     ...
;     }
;     __syncthreads();
.LBB0_1007:
	s_or_b64 exec, exec, s[0:1]
	v_readfirstlane_b32 s4, v0
	s_lshr_b32 s4, s4, 6
	s_cmp_lg_u32 s4, 0
	s_cbranch_scc1 .Lsf8_notw0
	v_mov_b32_e32 v2, 0x20020
	v_mov_b32_e32 v4, 9
	ds_write_b32 v2, v4
	s_branch .Lsf8_skip

; __device__ __forceinline__ void transpose_item_f8(const float* W, int N, unsigned char* WT, int ldt, int kind, int off, int item, int lane, float scale) {
;     const int nblk = N >> 6, kb = item / nblk, nb = item - kb * nblk, k0 = 128 * kb + 16 * (lane & 7), n = 64 * nb + 4 * (lane >> 3);
; __device__ __forceinline__ void moe_convert(Frame& F, int lo, int hi, int rank, int nrank) {
;     ...
;     for (int it = lo + rank; it < hi; it += nrank) {
;         int r = it; const float* W; unsigned char* WT; int N, ldt, kind, off; float f8s;
;         if (r < 14336) { const int e = r / 1792; r -= e * 1792; W = F.in[IN_WMG] + (size_t)e * 2048 * DFFE; N = DFFE; WT = F.ws + WS_WGU1 + (size_t)e * 14336 * 2048; ldt = 2048; kind = 1; off = 0; f8s = 32.f; }
;         else if ((r -= 14336) < 14336) { const int e = r / 1792; r -= e * 1792; W = F.in[IN_WMU] + (size_t)e * 2048 * DFFE; N = DFFE; WT = F.ws + WS_WGU1 + (size_t)e * 14336 * 2048; ldt = 2048; kind = 1; off = 128; f8s = 256.f; }
;         else { r -= 14336; const int e = r / 1792; r -= e * 1792; W = F.in[IN_WMD] + (size_t)e * DFFE * 2048; N = 2048; WT = F.ws + WS_WDN1 + (size_t)e * 2048 * DFFE; ldt = DFFE; kind = 0; off = 0; f8s = 64.f; }
;         transpose_item_f8(W, N, WT, ldt, kind, off, r, F.lane, f8s);
.Lsf8_loop:
	ds_read_b32 v9, v8
	s_waitcnt lgkmcnt(0)
	v_readfirstlane_b32 s5, v9
	s_cmp_eq_u32 s5, 9
	s_cbranch_scc1 .Lsf8_done
	ds_add_rtn_u32 v9, v8, v18 offset:4
	s_waitcnt lgkmcnt(0)
	v_readfirstlane_b32 s18, v9
	s_cmp_ge_u32 s18, 96
	s_cbranch_scc1 .Lsf8_done
	s_add_i32 s18, s18, s33
	s_and_b32 s27, s18, 1
	s_lshr_b32 s19, s18, 1
	s_add_i32 s19, s19, 0x5800
	s_cmp_lt_u32 s19, 0x7000
	s_cbranch_scc0 .Lsf8_down
	s_add_i32 s20, s19, 0xffffc800
	s_lshr_b32 s21, s20, 8
	s_mul_i32 s21, s21, 37
	s_lshr_b32 s21, s21, 8
	s_mul_i32 s28, s21, 0x700
	s_sub_i32 s20, s20, s28
	s_mul_i32 s28, s21, 0x3800000
	s_add_u32 s14, s10, s28
	s_addc_u32 s15, s11, 0
	s_mul_i32 s28, s21, 0x1c00000
	s_add_u32 s28, s28, 0x7800000
	s_add_u32 s16, s86, s28
	s_addc_u32 s17, s87, 0
	s_movk_i32 s24, 0x7000
	s_movk_i32 s25, 0x800
	s_mov_b32 s26, 0x43800000
	s_lshr_b32 s22, s20, 4
	s_mul_i32 s22, s22, 0x2493
	s_lshr_b32 s22, s22, 16
	s_mul_i32 s28, s22, 0x70
	s_sub_i32 s23, s20, s28
	s_mov_b32 s29, 1
	s_branch .Lsf8_dec

; template <bool ROUTER, bool XBF>
; __device__ __forceinline__ void norm_phase(Frame& F, const void* xin_, const float* g, const float* modl, int sh_off, int sc_off) {
;     ...
;     const int PER = (M + NGW - 1) / NGW, m0 = gw * PER, m1 = (m0 + PER < M) ? m0 + PER : M;
;     f32x4 gs[8], shv[8];
;     if (m0 < M) { const int b = m0 >> 11;
;         const f32x4* gp = (const f32x4*)g + F.lane; const f32x4* scp = (const f32x4*)(modl + (size_t)b * 12288 + sc_off) + F.lane; const f32x4* shp = (const f32x4*)(modl + (size_t)b * 12288 + sh_off) + F.lane;
; #pragma unroll
;         for (int j = 0; j < 8; ++j) { gs[j] = gp[64 * j] * (scp[64 * j] + 1.0f); shv[j] = shp[64 * j]; } }
;     f32x4 vn[8]; v2u vb[8];
;     if (m0 < M) {
;         if (XBF) { const v2u* xr = (const v2u*)((const bf16*)xin_ + (size_t)m0 * DM) + F.lane;
; #pragma unroll
;             for (int j = 0; j < 8; ++j) vb[j] = xr[64 * j]; }
;         else { const f32x4* xr = (const f32x4*)((const float*)xin_ + (size_t)m0 * DM) + F.lane;
; #pragma unroll
;             for (int j = 0; j < 8; ++j) vn[j] = xr[64 * j]; } }
.Lsf8_skip:
	s_waitcnt lgkmcnt(0)
	s_barrier
.LBB0_1008:
	s_cmp_lt_i32 s68, 10
	s_cselect_b64 s[0:1], -1, 0
	s_add_u32 s64, s86, 0x160000
	s_addc_u32 s65, s87, 0
	s_and_b64 s[0:1], s[0:1], s[2:3]
	s_andn2_b64 vcc, exec, s[0:1]
	s_cbranch_vccnz .LBB0_1016
	s_lshl_b32 s2, s82, 3
	s_abs_i32 s3, s2
	s_waitcnt vmcnt(0)
	v_cvt_f32_u32_e32 v2, s3
	s_sub_i32 s6, 0, s3
	s_add_i32 s5, s2, 0x3fff
	s_xor_b32 s2, s5, s2
	v_rcp_iflag_f32_e32 v2, v2
	s_abs_i32 s5, s5
	s_lshl_b32 s4, s94, 3
	s_add_i32 s4, s4, s77
	v_mul_f32_e32 v2, 0x4f7ffffe, v2
	v_cvt_u32_f32_e32 v2, v2
	s_ashr_i32 s2, s2, 31
	v_readfirstlane_b32 s7, v2
	s_mul_i32 s6, s6, s7
	s_mul_hi_u32 s6, s7, s6
	s_add_i32 s7, s7, s6
	s_mul_hi_u32 s6, s5, s7
	s_mul_i32 s7, s6, s3
	s_sub_i32 s5, s5, s7
	s_add_i32 s8, s6, 1
	s_sub_i32 s7, s5, s3
	s_cmp_ge_u32 s5, s3
	s_cselect_b32 s6, s8, s6
	s_cselect_b32 s5, s7, s5
	s_add_i32 s7, s6, 1
	s_cmp_ge_u32 s5, s3
	s_cselect_b32 s3, s7, s6
	s_xor_b32 s3, s3, s2
	s_sub_i32 s2, s3, s2
	s_mul_i32 s4, s2, s4
	s_cmpk_gt_i32 s4, 0x3fff
	s_cbranch_scc1 .LBB0_1011
	v_readlane_b32 s6, v247, 0
	v_readlane_b32 s7, v247, 1
	s_load_dwordx2 s[6:7], s[6:7], 0x20
	s_ashr_i32 s3, s4, 11
	v_lshlrev_b32_e32 v18, 4, v186
	v_mov_b32_e32 v19, 0
	s_mul_hi_i32 s5, s3, 0xc000
	s_mul_i32 s3, s3, 0xc000
	s_waitcnt lgkmcnt(0)
	v_lshl_add_u64 v[20:21], s[6:7], 0, v[18:19]
	s_add_u32 s8, s64, s3
	s_addc_u32 s9, s65, s5
	v_add_co_u32_e32 v2, vcc, 0x2000, v20
	v_lshl_add_u64 v[24:25], s[8:9], 0, v[18:19]
	s_nop 0
	v_addc_co_u32_e32 v3, vcc, 0, v21, vcc
	v_add_co_u32_e32 v28, vcc, 0x2000, v24
	s_movk_i32 s3, 0x3000
	s_nop 0
	v_addc_co_u32_e32 v29, vcc, 0, v25, vcc
	v_add_co_u32_e32 v66, vcc, s3, v20
	s_mov_b64 s[6:7], 0x2000
	s_nop 0
	v_addc_co_u32_e32 v67, vcc, 0, v21, vcc
	v_add_co_u32_e32 v68, vcc, s3, v24
	s_ashr_i32 s5, s4, 31
	v_lshl_add_u64 v[22:23], v[20:21], 0, s[6:7]
	v_lshl_add_u64 v[26:27], v[24:25], 0, s[6:7]
	global_load_dwordx4 v[38:41], v[2:3], off
	global_load_dwordx4 v[42:45], v[28:29], off
	s_nop 0
	global_load_dwordx4 v[2:5], v18, s[8:9]
	global_load_dwordx4 v[6:9], v18, s[8:9] offset:1024
	global_load_dwordx4 v[34:37], v[22:23], off offset:1024
	global_load_dwordx4 v[54:57], v[22:23], off offset:2048
	global_load_dwordx4 v[46:49], v[26:27], off offset:1024
	global_load_dwordx4 v[50:53], v[26:27], off offset:2048
	global_load_dwordx4 v[58:61], v[22:23], off offset:3072
	global_load_dwordx4 v[62:65], v[26:27], off offset:3072
	global_load_dwordx4 v[10:13], v18, s[8:9] offset:2048
	global_load_dwordx4 v[14:17], v18, s[8:9] offset:3072
	v_addc_co_u32_e32 v69, vcc, 0, v25, vcc
	s_movk_i32 s3, 0x1000
	s_lshl_b64 s[6:7], s[4:5], 12
	v_readlane_b32 s8, v247, 30
	v_add_co_u32_e32 v70, vcc, s3, v24
	v_readlane_b32 s9, v247, 31
	s_add_u32 s6, s8, s6
	v_addc_co_u32_e32 v71, vcc, 0, v25, vcc
	s_addc_u32 s7, s9, s7
	v_lshlrev_b32_e32 v114, 3, v186
	global_load_dwordx4 v[82:85], v[66:67], off
	global_load_dwordx4 v[86:89], v[66:67], off offset:1024
	global_load_dwordx4 v[90:93], v[68:69], off
	global_load_dwordx4 v[94:97], v[68:69], off offset:1024
	global_load_dwordx4 v[18:21], v[70:71], off
	global_load_dwordx4 v[22:25], v[70:71], off offset:1024
	global_load_dwordx4 v[98:101], v[66:67], off offset:2048
	global_load_dwordx4 v[102:105], v[66:67], off offset:3072
	global_load_dwordx4 v[106:109], v[68:69], off offset:2048
	global_load_dwordx4 v[110:113], v[68:69], off offset:3072
	global_load_dwordx4 v[26:29], v[70:71], off offset:2048
	global_load_dwordx4 v[30:33], v[70:71], off offset:3072
	global_load_dwordx2 v[80:81], v114, s[6:7]
	global_load_dwordx2 v[78:79], v114, s[6:7] offset:512
	global_load_dwordx2 v[76:77], v114, s[6:7] offset:1024
	global_load_dwordx2 v[74:75], v114, s[6:7] offset:1536
	global_load_dwordx2 v[72:73], v114, s[6:7] offset:2048
	global_load_dwordx2 v[70:71], v114, s[6:7] offset:2560
	global_load_dwordx2 v[68:69], v114, s[6:7] offset:3072
	global_load_dwordx2 v[66:67], v114, s[6:7] offset:3584
	s_waitcnt vmcnt(30)
	v_pk_add_f32 v[42:43], v[42:43], 1.0 op_sel_hi:[1,0]
	v_pk_add_f32 v[44:45], v[44:45], 1.0 op_sel_hi:[1,0]
	s_waitcnt vmcnt(25)
	v_pk_add_f32 v[48:49], v[48:49], 1.0 op_sel_hi:[1,0]
	v_pk_add_f32 v[46:47], v[46:47], 1.0 op_sel_hi:[1,0]
	s_waitcnt vmcnt(24)
	v_pk_add_f32 v[52:53], v[52:53], 1.0 op_sel_hi:[1,0]
	v_pk_add_f32 v[114:115], v[50:51], 1.0 op_sel_hi:[1,0]
	s_waitcnt vmcnt(22)
	v_pk_add_f32 v[62:63], v[62:63], 1.0 op_sel_hi:[1,0]
	v_pk_mul_f32 v[50:51], v[36:37], v[48:49]
	v_pk_mul_f32 v[48:49], v[38:39], v[42:43]
	v_pk_add_f32 v[64:65], v[64:65], 1.0 op_sel_hi:[1,0]
	v_pk_mul_f32 v[46:47], v[34:35], v[46:47]
	v_pk_mul_f32 v[52:53], v[56:57], v[52:53]
	s_waitcnt vmcnt(17)
	v_pk_add_f32 v[38:39], v[92:93], 1.0 op_sel_hi:[1,0]
	v_pk_mul_f32 v[34:35], v[58:59], v[62:63]
	v_pk_mul_f32 v[58:59], v[40:41], v[44:45]
	v_pk_add_f32 v[40:41], v[90:91], 1.0 op_sel_hi:[1,0]
	v_pk_mul_f32 v[56:57], v[84:85], v[38:39]
	s_waitcnt vmcnt(16)
	v_pk_add_f32 v[38:39], v[96:97], 1.0 op_sel_hi:[1,0]
	v_pk_mul_f32 v[36:37], v[54:55], v[114:115]
	v_pk_mul_f32 v[54:55], v[60:61], v[64:65]
	v_pk_mul_f32 v[44:45], v[82:83], v[40:41]
	v_pk_add_f32 v[40:41], v[94:95], 1.0 op_sel_hi:[1,0]
	v_pk_mul_f32 v[60:61], v[88:89], v[38:39]
	s_waitcnt vmcnt(11)
	v_pk_add_f32 v[38:39], v[108:109], 1.0 op_sel_hi:[1,0]
	v_pk_mul_f32 v[42:43], v[86:87], v[40:41]
	v_pk_add_f32 v[40:41], v[106:107], 1.0 op_sel_hi:[1,0]
	v_pk_mul_f32 v[62:63], v[100:101], v[38:39]
	s_waitcnt vmcnt(10)
	v_pk_add_f32 v[38:39], v[112:113], 1.0 op_sel_hi:[1,0]
	v_pk_add_f32 v[82:83], v[110:111], 1.0 op_sel_hi:[1,0]
	v_pk_mul_f32 v[40:41], v[98:99], v[40:41]
	v_pk_mul_f32 v[64:65], v[104:105], v[38:39]
	v_pk_mul_f32 v[38:39], v[102:103], v[82:83]
	s_add_i32 s2, s4, s2
	s_min_i32 s10, s2, 0x4000
	s_cmp_ge_i32 s4, s10
	s_cbranch_scc0 .LBB0_1012
	s_branch .LBB0_1016

; __device__ __forceinline__ void xcd_barrier(const XcdBarrier& b) {
;     ...
;     }
;     __syncthreads();
.LBB0_1065:
	s_or_b64 exec, exec, s[0:1]
	v_readfirstlane_b32 s4, v0
	s_lshr_b32 s4, s4, 6
	s_cmp_lg_u32 s4, 0
	s_cbranch_scc1 .Lsf9_notw0
	v_mov_b32_e32 v2, 0x20020
	v_mov_b32_e32 v4, 10
	ds_write_b32 v2, v4
	s_branch .Lsf9_skip

; __device__ __forceinline__ void transpose_item_f8(const float* W, int N, unsigned char* WT, int ldt, int kind, int off, int item, int lane, float scale) {
;     const int nblk = N >> 6, kb = item / nblk, nb = item - kb * nblk, k0 = 128 * kb + 16 * (lane & 7), n = 64 * nb + 4 * (lane >> 3);
; __device__ __forceinline__ void moe_convert(Frame& F, int lo, int hi, int rank, int nrank) {
;     ...
;     for (int it = lo + rank; it < hi; it += nrank) {
;         int r = it; const float* W; unsigned char* WT; int N, ldt, kind, off; float f8s;
;         if (r < 14336) { const int e = r / 1792; r -= e * 1792; W = F.in[IN_WMG] + (size_t)e * 2048 * DFFE; N = DFFE; WT = F.ws + WS_WGU1 + (size_t)e * 14336 * 2048; ldt = 2048; kind = 1; off = 0; f8s = 32.f; }
;         else if ((r -= 14336) < 14336) { const int e = r / 1792; r -= e * 1792; W = F.in[IN_WMU] + (size_t)e * 2048 * DFFE; N = DFFE; WT = F.ws + WS_WGU1 + (size_t)e * 14336 * 2048; ldt = 2048; kind = 1; off = 128; f8s = 256.f; }
;         else { r -= 14336; const int e = r / 1792; r -= e * 1792; W = F.in[IN_WMD] + (size_t)e * DFFE * 2048; N = 2048; WT = F.ws + WS_WDN1 + (size_t)e * 2048 * DFFE; ldt = DFFE; kind = 0; off = 0; f8s = 64.f; }
;         transpose_item_f8(W, N, WT, ldt, kind, off, r, F.lane, f8s);
.Lsf9_loop:
	ds_read_b32 v9, v8
	s_waitcnt lgkmcnt(0)
	v_readfirstlane_b32 s5, v9
	s_cmp_eq_u32 s5, 10
	s_cbranch_scc1 .Lsf9_done
	ds_add_rtn_u32 v9, v8, v18 offset:4
	s_waitcnt lgkmcnt(0)
	v_readfirstlane_b32 s18, v9
	s_cmp_ge_u32 s18, 96
	s_cbranch_scc1 .Lsf9_done
	s_add_i32 s18, s18, s33
	s_and_b32 s27, s18, 1
	s_lshr_b32 s19, s18, 1
	s_add_i32 s19, s19, 0x5800
	s_cmp_lt_u32 s19, 0x7000
	s_cbranch_scc0 .Lsf9_down
	s_add_i32 s20, s19, 0xffffc800
	s_lshr_b32 s21, s20, 8
	s_mul_i32 s21, s21, 37
	s_lshr_b32 s21, s21, 8
	s_mul_i32 s28, s21, 0x700
	s_sub_i32 s20, s20, s28
	s_mul_i32 s28, s21, 0x3800000
	s_add_u32 s14, s10, s28
	s_addc_u32 s15, s11, 0
	s_mul_i32 s28, s21, 0x1c00000
	s_add_u32 s28, s28, 0x7800000
	s_add_u32 s16, s86, s28
	s_addc_u32 s17, s87, 0
	s_movk_i32 s24, 0x7000
	s_movk_i32 s25, 0x800
	s_mov_b32 s26, 0x43800000
	s_lshr_b32 s22, s20, 4
	s_mul_i32 s22, s22, 0x2493
	s_lshr_b32 s22, s22, 16
	s_mul_i32 s28, s22, 0x70
	s_sub_i32 s23, s20, s28
	s_mov_b32 s29, 1
	s_branch .Lsf9_dec

; #define PG8_STAGE(bufoff, gbase, voff) do { _Pragma("unroll") for (int _i = 0; _i < 2; ++_i) \
;         __builtin_amdgcn_global_load_lds((const unsigned*)((const char*)(gbase) + (voff)[_i]), (PG8_LAS unsigned*)(lds + (bufoff) + ldsw + _i * 8192), 16, 0, 0); } while (0)
; #define PG8_BAR __builtin_amdgcn_s_barrier()
; template <class Epi, class Sched, bool ALIGN_EPI = false, bool SP2 = false>
; __device__ __forceinline__ void gemm_phase(PG8_LAS unsigned char* lds, const Gemm g, const Sched& S, const Epi& E) {
;     const int tid = threadIdx.x, wid = __builtin_amdgcn_readfirstlane(tid >> 6), lane = tid & 63, wr = wid >> 2, wc = wid & 3, fr = lane & 15, fq = lane >> 4;
;     const int K = g.K, nt = K / BK;
;     unsigned voffA[2], voffB[2];
; #pragma unroll
;     for (int i = 0; i < 2; ++i) { int R, C; stage_rc(tid * 16 + i * 8192, R, C); const int Rb = Epi::PERM ? ((R & ~31) + perm32(R & 31)) : R;
;         voffA[i] = (unsigned)(R * K + C) * 2u; voffB[i] = (unsigned)(Rb * K + C) * 2u; }
;     const size_t kstep = (size_t)(BK * 2);
;     const size_t hstep = (size_t)HALF * K * 2;
;     const size_t tstep = 2 * hstep;
;     const unsigned ldsw = (unsigned)wid * 1024u;
;     const int aoff = lds_byte(wr * 64 + fr, fq * 8), boff = lds_byte(wc * 32 + fr, fq * 8);
;     ...
;     Unit cur, nxt; int ui = 0;
;     if (!S.next(0, cur)) return;
;     int f8_sw = Epi::SCALE_W, f8_sx = Epi::SCALE_X;
;     if constexpr (Epi::FP8) asm volatile("" : "+v"(f8_sw), "+v"(f8_sx));
;     f32x4 acc[2][2][4][2];
; #pragma unroll
;     for (int a = 0; a < 2; ++a)
; #pragma unroll
;         for (int b = 0; b < 2; ++b)
; #pragma unroll
;             for (int m = 0; m < 4; ++m)
; #pragma unroll
;                 for (int n = 0; n < 2; ++n) acc[a][b][m][n] = (f32x4){0.f, 0.f, 0.f, 0.f};
;     bf16x8 At[4][2], B0[2][2], B1[2][2];
;     const char* cA = (const char*)g.A + (size_t)cur.pm * tstep; const char* cB = (const char*)g.Bt + (size_t)cur.pn * tstep;
;     S.a_ready(cur);
;     if constexpr (SP2) {
;         PG8_STAGE(PG8_SB(0, 0), cB, voffB); PG8_STAGE(PG8_SB(0, 1), cB + hstep, voffB); PG8_STAGE(PG8_SA(0, 0), cA, voffA); PG8_STAGE(PG8_SA(0, 1), cA + hstep, voffA);
;         if (wr == 1) PG8_BAR;
.Lsf9_skip:
	s_waitcnt lgkmcnt(0)
	s_barrier
.LBB0_1066:
	s_cmp_lt_i32 s68, 11
	s_cselect_b64 s[0:1], -1, 0
	s_and_b64 s[0:1], s[0:1], s[2:3]
	s_andn2_b64 vcc, exec, s[0:1]
	s_cbranch_vccnz .LBB0_1115
	v_readlane_b32 s5, v247, 6
	s_cmpk_gt_i32 s5, 0x47f
	v_readfirstlane_b32 s3, v0
	s_cbranch_scc1 .LBB0_1089
	s_waitcnt vmcnt(0)
	v_lshrrev_b32_e32 v2, 5, v0
	v_and_b32_e32 v2, 4, v2
	v_bfe_u32 v3, v0, 2, 2
	v_and_b32_e32 v13, 24, v210
	v_or_b32_e32 v10, 0x2000, v211
	s_add_u32 s33, s86, 0x1400000
	v_or3_b32 v2, v2, v3, v13
	v_lshrrev_b32_e32 v3, 7, v10
	s_movk_i32 s2, 0x60
	s_addc_u32 s38, s87, 0
	v_and_or_b32 v4, v3, s2, v2
	v_bfe_u32 v14, v0, 2, 4
	s_movk_i32 s2, 0x70
	s_ashr_i32 s40, s5, 31
	v_and_or_b32 v3, v3, s2, v14
	s_lshr_b32 s2, s40, 29
	s_add_i32 s2, s5, s2
	s_lshr_b32 s6, s3, 6
	s_ashr_i32 s4, s2, 3
	s_and_b32 s2, s2, -8
	s_lshr_b32 s8, s3, 8
	s_lshl_b32 s39, s6, 10
	s_sub_i32 s2, s5, s2
	s_cmp_lt_i32 s2, 0
	s_movk_i32 s41, 0x91
	s_cselect_b32 s5, s41, 0x90
	s_mul_i32 s2, s2, s5
	s_add_i32 s2, s2, s4
	s_mul_hi_i32 s4, s2, 0x38e38e39
	s_lshr_b32 s5, s4, 31
	s_ashr_i32 s4, s4, 5
	s_add_i32 s4, s4, s5
	s_lshl_b32 s5, s4, 3
	s_mulk_i32 s4, 0x90
	s_sub_i32 s4, s2, s4
	s_sext_i32_i16 s2, s4
	s_bfe_u32 s2, s2, 0x3001c
	s_add_i32 s7, s4, s2
	s_sext_i32_i16 s2, s7
	s_and_b32 s7, s7, 0xfff8
	s_sub_i32 s4, s4, s7
	s_sext_i32_i16 s4, s4
	v_and_b32_e32 v5, 32, v0
	s_lshr_b32 s2, s2, 3
	s_add_i32 s28, s5, s4
	v_bitop3_b32 v11, v211, v5, 48 bitop3:0x6c
	v_and_b32_e32 v12, 64, v0
	s_ashr_i32 s29, s28, 31
	s_bfe_i64 s[10:11], s[2:3], 0x100000
	v_or_b32_e32 v5, v11, v12
	s_lshl_b64 s[4:5], s[28:29], 20
	s_lshl_b64 s[10:11], s[10:11], 20
	v_lshl_or_b32 v132, v3, 12, v5
	v_lshrrev_b32_e32 v3, 3, v0
	s_add_u32 s34, s33, s10
	v_and_or_b32 v2, v3, 32, v2
	s_addc_u32 s35, s38, s11
	s_add_i32 s42, s39, 0
	v_lshl_or_b32 v134, v2, 12, v5
	s_add_i32 m0, s42, 0x10000
	v_lshl_or_b32 v130, v4, 12, v5
	global_load_lds_dwordx4 v134, s[34:35]
	s_add_i32 m0, s42, 0x12000
	s_add_u32 s10, s34, 0x80000
	global_load_lds_dwordx4 v130, s[34:35]
	s_addc_u32 s11, s35, 0
	s_add_i32 m0, s42, 0x14000
	v_and_or_b32 v2, v3, 48, v14
	global_load_lds_dwordx4 v134, s[10:11]
	s_add_i32 m0, s42, 0x16000
	s_add_u32 s30, s70, s4
	s_addc_u32 s31, s71, s5
	s_add_i32 s43, s42, 0x2000
	v_lshl_or_b32 v136, v2, 12, v5
	global_load_lds_dwordx4 v130, s[10:11]
	s_mov_b32 m0, s42
	s_add_u32 s4, s30, 0x80000
	global_load_lds_dwordx4 v136, s[30:31]
	s_mov_b32 m0, s43
	s_addc_u32 s5, s31, 0
	s_add_i32 s44, s42, 0x4000
	global_load_lds_dwordx4 v132, s[30:31]
	s_mov_b32 m0, s44
	s_add_i32 s45, s42, 0x6000
	global_load_lds_dwordx4 v136, s[4:5]
	s_mov_b32 m0, s45
	v_mov_b32_e32 v135, 0
	global_load_lds_dwordx4 v132, s[4:5]
	v_mov_b32_e32 v131, v135
	v_mov_b32_e32 v137, v135
	v_mov_b32_e32 v133, v135
	s_cmp_eq_u32 s8, 1
	s_mov_b32 s46, 0
	v_lshl_add_u64 v[8:9], s[34:35], 0, v[134:135]
	v_lshl_add_u64 v[6:7], s[34:35], 0, v[130:131]
	v_lshl_add_u64 v[4:5], s[30:31], 0, v[136:137]
	v_lshl_add_u64 v[2:3], s[30:31], 0, v[132:133]
	s_cselect_b64 s[4:5], -1, 0
	s_cmp_lg_u32 s8, 1
	s_movk_i32 s47, 0x4000
	s_cbranch_scc1 .LBB0_1070
	s_barrier

; __device__ __forceinline__ void xcd_barrier(const XcdBarrier& b) {
;     ...
;     }
;     __syncthreads();
.LBB0_1164:
	s_or_b64 exec, exec, s[0:1]
	v_readfirstlane_b32 s4, v0
	s_lshr_b32 s4, s4, 6
	s_cmp_lg_u32 s4, 0
	s_cbranch_scc1 .Lsf10_notw0
	v_mov_b32_e32 v2, 0x20020
	v_mov_b32_e32 v4, 11
	ds_write_b32 v2, v4
	s_branch .Lsf10_skip

; __device__ __forceinline__ void transpose_item_f8(const float* W, int N, unsigned char* WT, int ldt, int kind, int off, int item, int lane, float scale) {
;     const int nblk = N >> 6, kb = item / nblk, nb = item - kb * nblk, k0 = 128 * kb + 16 * (lane & 7), n = 64 * nb + 4 * (lane >> 3);
; __device__ __forceinline__ void moe_convert(Frame& F, int lo, int hi, int rank, int nrank) {
;     ...
;     for (int it = lo + rank; it < hi; it += nrank) {
;         int r = it; const float* W; unsigned char* WT; int N, ldt, kind, off; float f8s;
;         if (r < 14336) { const int e = r / 1792; r -= e * 1792; W = F.in[IN_WMG] + (size_t)e * 2048 * DFFE; N = DFFE; WT = F.ws + WS_WGU1 + (size_t)e * 14336 * 2048; ldt = 2048; kind = 1; off = 0; f8s = 32.f; }
;         else if ((r -= 14336) < 14336) { const int e = r / 1792; r -= e * 1792; W = F.in[IN_WMU] + (size_t)e * 2048 * DFFE; N = DFFE; WT = F.ws + WS_WGU1 + (size_t)e * 14336 * 2048; ldt = 2048; kind = 1; off = 128; f8s = 256.f; }
;         else { r -= 14336; const int e = r / 1792; r -= e * 1792; W = F.in[IN_WMD] + (size_t)e * DFFE * 2048; N = 2048; WT = F.ws + WS_WDN1 + (size_t)e * 2048 * DFFE; ldt = DFFE; kind = 0; off = 0; f8s = 64.f; }
;         transpose_item_f8(W, N, WT, ldt, kind, off, r, F.lane, f8s);
.Lsf10_loop:
	ds_read_b32 v9, v8
	s_waitcnt lgkmcnt(0)
	v_readfirstlane_b32 s5, v9
	s_cmp_eq_u32 s5, 11
	s_cbranch_scc1 .Lsf10_done
	ds_add_rtn_u32 v9, v8, v18 offset:4
	s_waitcnt lgkmcnt(0)
	v_readfirstlane_b32 s18, v9
	s_cmp_ge_u32 s18, 96
	s_cbranch_scc1 .Lsf10_done
	s_add_i32 s18, s18, s33
	s_and_b32 s27, s18, 1
	s_lshr_b32 s19, s18, 1
	s_add_i32 s19, s19, 0x5800
	s_cmp_lt_u32 s19, 0x7000
	s_cbranch_scc0 .Lsf10_down
	s_add_i32 s20, s19, 0xffffc800
	s_lshr_b32 s21, s20, 8
	s_mul_i32 s21, s21, 37
	s_lshr_b32 s21, s21, 8
	s_mul_i32 s28, s21, 0x700
	s_sub_i32 s20, s20, s28
	s_mul_i32 s28, s21, 0x3800000
	s_add_u32 s14, s10, s28
	s_addc_u32 s15, s11, 0
	s_mul_i32 s28, s21, 0x1c00000
	s_add_u32 s28, s28, 0x7800000
	s_add_u32 s16, s86, s28
	s_addc_u32 s17, s87, 0
	s_movk_i32 s24, 0x7000
	s_movk_i32 s25, 0x800
	s_mov_b32 s26, 0x43800000
	s_lshr_b32 s22, s20, 4
	s_mul_i32 s22, s22, 0x2493
	s_lshr_b32 s22, s22, 16
	s_mul_i32 s28, s22, 0x70
	s_sub_i32 s23, s20, s28
	s_mov_b32 s29, 1
	s_branch .Lsf10_dec

; #define LAS __attribute__((address_space(3)))
; __device__ __forceinline__ void swa_unit(Frame& F, int l, int unit) {
;     const int b = unit >> 5, kvh = (unit >> 4) & 1, nb = unit & 15;
;     const int tid = F.tid, lane = F.lane, w = F.wave, g = lane >> 4, n = lane & 15;
;     const bf16* proj = (const bf16*)(F.ws + WS_PROJ); bf16* Y = (bf16*)(F.ws + WS_Y);
;     LAS unsigned char* Kt = F.lds + RING_OFF; LAS unsigned char* Vt = Kt + 36864; LAS float* bias = (LAS float*)(Kt + 73728);
;     constexpr int LDB = 144;
;     const int hq = kvh * 8 + w;
;     v4u qn[2][2];
;     const bf16* qbase = proj + (size_t)(b * SEQ + nb * 128 + n) * PROJ_LD + C_AQ + hq * 64 + 8 * g;
; #pragma unroll
;     for (int jt = 0; jt < 2; ++jt) { qn[jt][0] = *(const v4u*)(qbase + (size_t)(jt * 16) * PROJ_LD); qn[jt][1] = *(const v4u*)(qbase + (size_t)(jt * 16) * PROJ_LD + 32); }
;     __syncthreads();
;     {
;         const int r = tid >> 1, hf = tid & 1, pos = nb * 128 - 128 + r;
;         v4u kx[4], vx[4];
;         if (pos >= 0) { const bf16* kp = proj + (size_t)(b * SEQ + pos) * PROJ_LD + C_AK + kvh * 64 + hf * 32; const bf16* vp = proj + (size_t)(b * SEQ + pos) * PROJ_LD + C_AV + kvh * 64 + hf * 32;
; #pragma unroll
;             for (int j = 0; j < 4; ++j) { kx[j] = *(const v4u*)(kp + 8 * j); vx[j] = *(const v4u*)(vp + 8 * j); } }
;         else {
; #pragma unroll
;             for (int j = 0; j < 4; ++j) { kx[j] = (v4u){0u, 0u, 0u, 0u}; vx[j] = (v4u){0u, 0u, 0u, 0u}; } }
;         float kf[32]; float ss = 0.f;
; #pragma unroll
;         for (int j = 0; j < 4; ++j) { kf[8 * j + 0] = bflo(kx[j].x); kf[8 * j + 1] = bfhi(kx[j].x); kf[8 * j + 2] = bflo(kx[j].y); kf[8 * j + 3] = bfhi(kx[j].y); kf[8 * j + 4] = bflo(kx[j].z); kf[8 * j + 5] = bfhi(kx[j].z); kf[8 * j + 6] = bflo(kx[j].w); kf[8 * j + 7] = bfhi(kx[j].w); }
; #pragma unroll
;         for (int i = 0; i < 32; ++i) ss += kf[i] * kf[i];
;         ss += __shfl_xor(ss, 1);
;         const float rstd = 1.0f / sqrtf(ss * (1.0f / 64.0f) + EPS);
;         const float* gk = F.in[IN_GKN] + l * 64 + hf * 32;
; #pragma unroll
;         for (int j = 0; j < 4; ++j) { const f32x4 g0 = *(const f32x4*)(gk + 8 * j), g1 = *(const f32x4*)(gk + 8 * j + 4);
;             v4u o; o.x = pk2(kf[8 * j] * rstd * g0.x, kf[8 * j + 1] * rstd * g0.y); o.y = pk2(kf[8 * j + 2] * rstd * g0.z, kf[8 * j + 3] * rstd * g0.w);
.Lsf10_skip:
	s_waitcnt lgkmcnt(0)
	s_barrier
.LBB0_1165:
	s_cmp_lt_i32 s68, 12
	s_cselect_b64 s[0:1], -1, 0
	s_and_b64 s[70:71], s[0:1], s[2:3]
	s_andn2_b64 vcc, exec, s[70:71]
	s_cbranch_vccnz .LBB0_1235
	v_readlane_b32 s0, v247, 19
	v_readlane_b32 s1, v247, 20
	s_and_b64 vcc, exec, s[0:1]
	s_cbranch_vccz .LBB0_1183
	s_waitcnt vmcnt(0)
	v_and_b32_e32 v5, 0x7f, v0
	s_getpc_b64 s[2:3]
	s_add_u32 s2, s2, _ZL9T5_BUCKET@rel32@lo+4
	s_addc_u32 s3, s3, _ZL9T5_BUCKET@rel32@hi+12
	global_load_ubyte v5, v5, s[2:3]
	v_mbcnt_lo_u32_b32 v2, -1, 0
	v_mbcnt_hi_u32_b32 v2, -1, v2
	v_and_b32_e32 v4, 64, v2
	v_xor_b32_e32 v3, 1, v2
	v_add_u32_e32 v4, 64, v4
	v_cmp_lt_i32_e32 vcc, v3, v4
	v_readlane_b32 s2, v247, 0
	v_readlane_b32 s3, v247, 1
	v_cndmask_b32_e32 v3, v2, v3, vcc
	v_lshlrev_b32_e32 v134, 2, v3
	v_xor_b32_e32 v3, 2, v2
	v_cmp_lt_i32_e32 vcc, v3, v4
	s_load_dwordx8 s[36:43], s[2:3], 0x70
	s_movk_i32 s0, 0x90
	v_cndmask_b32_e32 v3, v2, v3, vcc
	v_lshlrev_b32_e32 v135, 2, v3
	v_xor_b32_e32 v3, 4, v2
	v_cmp_lt_i32_e32 vcc, v3, v4
	v_mad_u32_u24 v12, v210, s0, 0
	s_lshl_b32 s0, s77, 9
	v_cndmask_b32_e32 v3, v2, v3, vcc
	v_lshlrev_b32_e32 v136, 2, v3
	v_xor_b32_e32 v3, 8, v2
	v_cmp_lt_i32_e32 vcc, v3, v4
	s_add_i32 s18, 0, 0x12000
	s_add_i32 s0, s18, s0
	v_cndmask_b32_e32 v3, v2, v3, vcc
	v_lshlrev_b32_e32 v137, 2, v3
	v_xor_b32_e32 v3, 16, v2
	v_cmp_lt_i32_e32 vcc, v3, v4
	v_lshlrev_b32_e32 v6, 2, v186
	v_add_u32_e32 v141, s0, v6
	v_cndmask_b32_e32 v3, v2, v3, vcc
	v_lshlrev_b32_e32 v138, 2, v3
	v_xor_b32_e32 v3, 32, v2
	v_cmp_lt_i32_e32 vcc, v3, v4
	v_lshrrev_b32_e32 v14, 7, v0
	s_add_i32 s33, 0, 0x18000
	v_cndmask_b32_e32 v2, v2, v3, vcc
	v_lshlrev_b32_e32 v139, 2, v2
	v_mov_b32_e32 v2, 0
	v_mov_b32_e32 v7, v2
	s_waitcnt lgkmcnt(0)
	v_lshl_add_u64 v[114:115], s[36:37], 0, v[6:7]
	v_lshl_add_u64 v[116:117], s[38:39], 0, v[6:7]
	v_lshrrev_b32_e32 v6, 4, v0
	v_bfe_u32 v7, v0, 4, 3
	v_lshl_add_u32 v142, v7, 2, s33
	v_mul_u32_u24_e32 v6, 0x280, v6
	s_add_i32 s10, 0, 0x13000
	v_lshlrev_b32_e32 v10, 7, v7
	v_add_u32_e32 v7, v212, v14
	v_lshlrev_b32_e32 v8, 2, v212
	v_add3_u32 v143, s10, v6, v8
	v_or_b32_e32 v6, 32, v7
	v_sub_u32_e32 v6, v10, v6
	v_lshl_add_u32 v144, v6, 2, s18
	v_or_b32_e32 v6, 64, v7
	v_sub_u32_e32 v6, v10, v6
	v_lshl_add_u32 v145, v6, 2, s18
	v_sub_u32_e32 v6, v10, v7
	v_lshl_add_u32 v146, v6, 2, s18
	v_or_b32_e32 v6, 0x60, v7
	v_lshrrev_b32_e32 v3, 4, v186
	v_sub_u32_e32 v6, v10, v6
	v_cmp_lt_u32_e64 s[4:5], 15, v7
	v_lshl_add_u32 v148, v6, 2, s18
	v_or_b32_e32 v11, 0x80, v7
	v_add_u32_e32 v15, 0x70, v7
	v_lshlrev_b32_e32 v6, 5, v3
	v_mov_b32_e32 v7, v2
	s_lshl_b32 s8, s77, 2
	v_lshl_add_u64 v[118:119], s[36:37], 0, v[6:7]
	v_lshlrev_b32_e32 v6, 2, v3
	v_lshlrev_b32_e32 v4, 3, v3
	s_add_i32 s33, s33, s8
	v_sub_co_u32_e64 v3, s[8:9], v6, v212
	v_add_u32_e32 v3, 15, v3
	v_lshlrev_b32_e32 v7, 3, v3
	v_and_b32_e32 v7, 24, v7
	s_movk_i32 s0, 0x280
	v_add_u32_e32 v7, s77, v7
	v_lshlrev_b32_e32 v3, 2, v3
	s_movk_i32 s6, 0x80
	v_mul_lo_u32 v7, v7, s0
	v_and_b32_e32 v3, -16, v3
	v_and_b32_e32 v9, 1, v0
	v_cmp_gt_u32_e64 s[6:7], s6, v15
	v_add3_u32 v149, s10, v7, v3
	v_bfe_u32 v3, v0, 2, 4
	v_lshlrev_b32_e32 v7, 3, v0
	v_or_b32_e32 v8, 2, v6
	v_sub_u32_e32 v15, v10, v15
	v_sub_u32_e32 v10, v10, v11
	v_and_b32_e32 v7, 24, v7
	v_cmp_gt_u32_e64 s[14:15], v8, v212
	v_or_b32_e32 v8, 3, v6
	v_lshl_add_u32 v153, v10, 2, s18
	v_lshlrev_b32_e32 v10, 7, v9
	v_mov_b32_e32 v11, v2
	v_mov_b32_e32 v189, v2
	v_mul_u32_u24_e32 v3, 0x90, v3
	v_lshlrev_b32_e32 v13, 6, v9
	v_cmp_gt_u32_e64 s[16:17], v8, v212
	v_lshlrev_b32_e32 v8, 5, v9
	v_lshl_add_u32 v152, v15, 2, s18
	v_lshl_add_u64 v[120:121], s[38:39], 0, v[10:11]
	v_lshl_add_u32 v156, v0, 2, s18
	v_lshl_add_u64 v[10:11], s[86:87], 0, v[188:189]
	s_mov_b64 s[18:19], 0x41c45800
	v_add3_u32 v157, v3, v7, 0
	v_mul_u32_u24_e32 v3, 0x90, v212
	s_mov_b32 s1, 0
	v_add_u32_e32 v140, 0xffffff80, v210
	v_cmp_eq_u32_e64 s[2:3], 0, v186
	v_add_u32_e32 v147, 0xfffffec0, v146
	v_cmp_gt_u32_e64 s[10:11], v6, v212
	v_cmp_ge_u32_e64 s[12:13], v6, v212
	v_subrev_u32_e32 v150, 64, v146
	v_add_u32_e32 v151, 0xffffff40, v146
	s_waitcnt vmcnt(0)
	v_lshl_or_b32 v154, v5, 4, v14
	v_or_b32_e32 v155, 0xfffffe00, v0
	v_lshl_add_u64 v[122:123], v[10:11], 0, s[18:19]
	s_lshl_b32 s48, s94, 6
	s_lshl_b32 s49, s82, 6
	s_lshl_b32 s50, s77, 6
	v_add3_u32 v158, v3, v188, 0
	s_movk_i32 s51, 0x2200
	v_lshlrev_b32_e32 v124, 1, v4
	s_mov_b64 s[30:31], 0x1800
	s_movk_i32 s52, 0x1000
	v_lshlrev_b32_e32 v126, 1, v8
	s_mov_b64 s[34:35], 0x2000
	s_mov_b64 s[36:37], 0x2100
	v_add_u32_e32 v159, v12, v13
	v_mov_b32_e32 v160, 0x358637bd
	s_mov_b32 s53, 0xf800000
	v_mov_b32_e32 v161, 0x260
	s_mov_b32 s54, 0x3e38aa3b
	v_lshlrev_b32_e32 v128, 1, v6
	s_mov_b64 s[38:39], 0x3d800800
	s_mov_b32 s55, 0x3d800000
	s_mov_b64 s[44:45], 0x44000
	s_mov_b32 s56, s94
	s_mov_b32 s57, s94
	s_branch .LBB0_1169

; __device__ __forceinline__ void xcd_barrier(const XcdBarrier& b) {
;     ...
;     }
;     __syncthreads();
.LBB0_1284:
	s_or_b64 exec, exec, s[2:3]
	v_readfirstlane_b32 s4, v0
	s_lshr_b32 s4, s4, 6
	s_cmp_lg_u32 s4, 0
	s_cbranch_scc1 .Lsf11_notw0
	v_mov_b32_e32 v2, 0x20020
	v_mov_b32_e32 v4, 12
	ds_write_b32 v2, v4
	s_branch .Lsf11_skip

; __device__ __forceinline__ void transpose_item_f8(const float* W, int N, unsigned char* WT, int ldt, int kind, int off, int item, int lane, float scale) {
;     const int nblk = N >> 6, kb = item / nblk, nb = item - kb * nblk, k0 = 128 * kb + 16 * (lane & 7), n = 64 * nb + 4 * (lane >> 3);
; __device__ __forceinline__ void moe_convert(Frame& F, int lo, int hi, int rank, int nrank) {
;     ...
;     for (int it = lo + rank; it < hi; it += nrank) {
;         int r = it; const float* W; unsigned char* WT; int N, ldt, kind, off; float f8s;
;         if (r < 14336) { const int e = r / 1792; r -= e * 1792; W = F.in[IN_WMG] + (size_t)e * 2048 * DFFE; N = DFFE; WT = F.ws + WS_WGU1 + (size_t)e * 14336 * 2048; ldt = 2048; kind = 1; off = 0; f8s = 32.f; }
;         else if ((r -= 14336) < 14336) { const int e = r / 1792; r -= e * 1792; W = F.in[IN_WMU] + (size_t)e * 2048 * DFFE; N = DFFE; WT = F.ws + WS_WGU1 + (size_t)e * 14336 * 2048; ldt = 2048; kind = 1; off = 128; f8s = 256.f; }
;         else { r -= 14336; const int e = r / 1792; r -= e * 1792; W = F.in[IN_WMD] + (size_t)e * DFFE * 2048; N = 2048; WT = F.ws + WS_WDN1 + (size_t)e * 2048 * DFFE; ldt = DFFE; kind = 0; off = 0; f8s = 64.f; }
;         transpose_item_f8(W, N, WT, ldt, kind, off, r, F.lane, f8s);
.Lsf11_loop:
	ds_read_b32 v9, v8
	s_waitcnt lgkmcnt(0)
	v_readfirstlane_b32 s5, v9
	s_cmp_eq_u32 s5, 12
	s_cbranch_scc1 .Lsf11_done
	ds_add_rtn_u32 v9, v8, v18 offset:4
	s_waitcnt lgkmcnt(0)
	v_readfirstlane_b32 s18, v9
	s_cmp_ge_u32 s18, 96
	s_cbranch_scc1 .Lsf11_done
	s_add_i32 s18, s18, s33
	s_and_b32 s27, s18, 1
	s_lshr_b32 s19, s18, 1
	s_add_i32 s19, s19, 0x5800
	s_cmp_lt_u32 s19, 0x7000
	s_cbranch_scc0 .Lsf11_down
	s_add_i32 s20, s19, 0xffffc800
	s_lshr_b32 s21, s20, 8
	s_mul_i32 s21, s21, 37
	s_lshr_b32 s21, s21, 8
	s_mul_i32 s28, s21, 0x700
	s_sub_i32 s20, s20, s28
	s_mul_i32 s28, s21, 0x3800000
	s_add_u32 s14, s10, s28
	s_addc_u32 s15, s11, 0
	s_mul_i32 s28, s21, 0x1c00000
	s_add_u32 s28, s28, 0x7800000
	s_add_u32 s16, s86, s28
	s_addc_u32 s17, s87, 0
	s_movk_i32 s24, 0x7000
	s_movk_i32 s25, 0x800
	s_mov_b32 s26, 0x43800000
	s_lshr_b32 s22, s20, 4
	s_mul_i32 s22, s22, 0x2493
	s_lshr_b32 s22, s22, 16
	s_mul_i32 s28, s22, 0x70
	s_sub_i32 s23, s20, s28
	s_mov_b32 s29, 1
	s_branch .Lsf11_dec

; __device__ __forceinline__ void mix_b(Frame& F, int l) {
;     if (!(FAST_GLA && FAST_MLSTM && FAST_SWA)) mix_naive(F, l);
;     if (FAST_MLSTM) for (int rep = 0; rep < PROBE_SUBREP(204); ++rep) for (int ug = F.vcu; ug < 256; ug += F.G) mlstm_out_group(F, l, ug);
.Lsf11_skip:
	s_waitcnt lgkmcnt(0)
	s_barrier
.LBB0_1285:
	s_cmp_lt_i32 s68, 13
	s_cselect_b64 s[2:3], -1, 0
	s_and_b64 s[2:3], s[2:3], s[0:1]
	v_readlane_b32 s0, v247, 19
	v_readlane_b32 s1, v247, 20
	s_and_b64 s[0:1], s[2:3], s[0:1]
	s_andn2_b64 vcc, exec, s[0:1]
	s_cbranch_vccnz .LBB0_1388
; #define LAS __attribute__((address_space(3)))
; #define MFMA16(a, b, c) __builtin_amdgcn_mfma_f32_16x16x32_bf16((a), (b), (c), 0, 0, 0)
; __device__ __forceinline__ void mlstm_out_group(Frame& F, int l, int ug) {
;     ...
;         for (int prep = 0; prep < PROBE_SUBREP(210); ++prep) {
;             const int j = 16 * w + n; const float Mj = GF[128 + j], bj = GF[256 + j];
;             const size_t row = (size_t)(t0 + j);
;             v2u mx8[8];
; #pragma unroll
;             for (int mt = 0; mt < 8; ++mt) { const int v = 16 * mt + 4 * g; mx8[mt] = *(const v2u*)(proj + row * PROJ_LD + C_MO + h * 128 + v); }
;             bf16x8 qf[2];
; #pragma unroll
;             for (int ks = 0; ks < 2; ++ks) qf[ks] = frag_row(QC, 144, 16 * w, 32 * ks, lane);
;             f32x4 p[8];
; #pragma unroll
;             for (int st = 0; st < 8; ++st) { p[st] = (f32x4){0.f, 0.f, 0.f, 0.f};
;                 if (st <= w) {
; #pragma unroll
;                     for (int ks = 0; ks < 2; ++ks) p[st] = MFMA16(frag_row(KC, 144, 16 * st, 32 * ks, lane), qf[ks], p[st]);
;                     const f32x4 as = *(const LAS f32x4*)(GF + 16 * st + 4 * g);
; #pragma unroll
;                     for (int r = 0; r < 4; ++r) { const float e = __expf(as[r] - Mj); p[st][r] = (st < w || 4 * g + r <= n) ? p[st][r] * e : 0.f; } } }
;             f32x4 o[9];
;             const float wi = __expf(mst - Mj);
; #pragma unroll
;             for (int mt = 0; mt < 9; ++mt) { o[mt] = (f32x4){0.f, 0.f, 0.f, 0.f};
; #pragma unroll
;                 for (int ks = 0; ks < 2; ++ks) o[mt] = MFMA16(frag_row(CS, 144, 16 * mt, 32 * ks, lane), qf[ks], o[mt]);
;                 o[mt] = o[mt] * wi; }
;             const bf16x8 ones = (n == 0) ? pack8(1.f, 1.f, 1.f, 1.f, 1.f, 1.f, 1.f, 1.f) : pack8(0.f, 0.f, 0.f, 0.f, 0.f, 0.f, 0.f, 0.f);
; #pragma unroll
;             for (int kk = 0; kk < 4; ++kk) { if (2 * kk <= w) {
;                 const bf16x8 pf = pack8(p[2 * kk][0], p[2 * kk][1], p[2 * kk][2], p[2 * kk][3], p[2 * kk + 1][0], p[2 * kk + 1][1], p[2 * kk + 1][2], p[2 * kk + 1][3]);
; #pragma unroll
;                 for (int mt = 0; mt < 8; ++mt) o[mt] = MFMA16(frag_tr2(VT, 272, 32 * kk, 32 * kk + 16, 16 * mt, lane), pf, o[mt]);
;                 o[8] = MFMA16(ones, pf, o[8]); } }
	v_writelane_b32 v247, s2, 28
	s_add_u32 s0, s86, 0x4ac00000
	s_addc_u32 s1, s87, 0
	v_writelane_b32 v247, s3, 29
	v_writelane_b32 v247, s65, 12
	v_writelane_b32 v247, s64, 9
	v_writelane_b32 v247, s66, 21
	v_and_b32_e32 v124, 12, v214
	v_lshl_or_b32 v125, s77, 4, v212
	v_writelane_b32 v247, s67, 22
	v_writelane_b32 v247, s0, 32
	s_waitcnt vmcnt(0)
	v_or_b32_e32 v12, 2, v124
	s_movk_i32 s19, 0x90
	v_writelane_b32 v247, s1, 33
	s_add_u32 s0, s86, 0x4dc00000
	s_addc_u32 s1, s87, 0
	v_writelane_b32 v247, s0, 34
	v_cmp_eq_u32_e32 vcc, 0, v212
	v_mov_b32_e32 v11, 0x3f803f80
	v_writelane_b32 v247, s1, 35
	s_add_u32 s0, s86, 0x4ed00000
	s_addc_u32 s1, s87, 0
	v_writelane_b32 v247, s0, 36
	v_mad_u32_u24 v154, v1, s19, 0
	v_mul_lo_u32 v6, v125, s19
	v_writelane_b32 v247, s1, 37
	v_cndmask_b32_e32 v50, 0, v11, vcc
	v_readlane_b32 s0, v247, 0
	v_readlane_b32 s1, v247, 1
	s_load_dwordx2 s[0:1], s[0:1], 0x50
	v_cmp_gt_u32_e32 vcc, v124, v212
	s_mov_b32 s24, s77
	v_writelane_b32 v246, s82, 18
	s_mov_b32 s25, s80
	s_waitcnt lgkmcnt(0)
	s_add_u32 s0, s0, 0x800
	v_writelane_b32 v247, s0, 10
	s_addc_u32 s0, s1, 0
	s_add_i32 s18, 0, 0x11800
	s_add_i32 s20, 0, 0x16900
	s_cmp_gt_u32 s80, 63
	v_writelane_b32 v247, s0, 19
	s_movk_i32 s0, 0x80
	v_mov_b32_e32 v3, s18
	v_lshl_add_u32 v155, v0, 2, s20
	s_cselect_b64 s[70:71], -1, 0
	s_cmp_lt_u32 s80, 64
	v_lshl_add_u32 v157, v125, 2, s20
	v_lshl_add_u32 v158, v124, 2, s20
	v_cmp_gt_u32_e64 s[20:21], v12, v212
	v_or_b32_e32 v12, 3, v214
	v_cmp_gt_u32_e64 s[4:5], s0, v0
	v_mad_u32_u24 v3, v1, s19, v3
	s_cselect_b64 s[0:1], -1, 0
	v_add_u32_e32 v8, s18, v188
	v_cmp_ge_u32_e64 s[18:19], v124, v212
	v_cmp_gt_u32_e64 s[22:23], v12, v212
	s_and_b64 s[72:73], s[0:1], vcc
	s_and_b64 s[74:75], s[0:1], s[18:19]
	s_and_b64 s[76:77], s[0:1], s[20:21]
	s_and_b64 s[78:79], s[0:1], s[22:23]
	s_cmp_eq_u32 s24, 1
	s_cselect_b64 s[0:1], -1, 0
	s_and_b64 s[26:27], s[0:1], vcc
	v_writelane_b32 v247, s26, 38
	v_writelane_b32 v246, s83, 19
	v_lshlrev_b32_e32 v156, 3, v186
	v_writelane_b32 v247, s27, 39
	s_and_b64 s[26:27], s[0:1], s[18:19]
	v_writelane_b32 v247, s26, 40
	v_and_or_b32 v9, v1, 3, v124
	v_and_b32_e32 v10, 24, v156
	v_writelane_b32 v247, s27, 41
	s_and_b64 s[26:27], s[0:1], s[20:21]
	v_writelane_b32 v247, s26, 42
	s_and_b64 s[0:1], s[0:1], s[22:23]
	s_cmpk_gt_u32 s80, 0x7f
	v_writelane_b32 v247, s27, 43
	v_writelane_b32 v247, s0, 44
	s_cselect_b64 s[88:89], -1, 0
	s_cmp_eq_u32 s24, 2
	v_writelane_b32 v247, s1, 45
	s_cselect_b64 s[0:1], -1, 0
	s_and_b64 s[26:27], s[0:1], vcc
	v_writelane_b32 v247, s26, 46
	v_lshlrev_b32_e32 v2, 4, v215
	v_or_b32_e32 v13, 0x800, v213
	v_writelane_b32 v247, s27, 47
	s_and_b64 s[26:27], s[0:1], s[18:19]
	v_writelane_b32 v247, s26, 48
	v_lshlrev_b32_e32 v126, 1, v2
	v_or_b32_e32 v14, 0xc00, v213
	v_writelane_b32 v247, s27, 49
	s_and_b64 s[26:27], s[0:1], s[20:21]
	v_writelane_b32 v247, s26, 50
	s_and_b64 s[0:1], s[0:1], s[22:23]
	s_cmpk_gt_u32 s80, 0xbf
	v_writelane_b32 v247, s27, 51
	v_writelane_b32 v247, s0, 52
	s_cselect_b64 s[56:57], -1, 0
	s_cmp_eq_u32 s24, 3
	v_writelane_b32 v247, s1, 53
	s_cselect_b64 s[0:1], -1, 0
	s_and_b64 s[26:27], s[0:1], vcc
	v_writelane_b32 v247, s26, 54
	v_mov_b32_e32 v119, 0
	v_lshlrev_b32_e32 v120, 5, v215
	v_writelane_b32 v247, s27, 55
	s_and_b64 s[26:27], s[0:1], s[18:19]
	v_writelane_b32 v247, s26, 56
	v_lshl_add_u32 v4, v1, 7, v154
	v_lshlrev_b32_e32 v5, 6, v215
	v_writelane_b32 v247, s27, 57
	s_and_b64 s[26:27], s[0:1], s[20:21]
	v_writelane_b32 v247, s26, 58
	s_and_b64 s[0:1], s[0:1], s[22:23]
	s_cmpk_gt_u32 s80, 0xff
	v_writelane_b32 v247, s27, 59
	v_writelane_b32 v247, s0, 60
	s_cselect_b64 s[50:51], -1, 0
	s_cmp_eq_u32 s24, 4
	v_writelane_b32 v247, s1, 61
	s_cselect_b64 s[0:1], -1, 0
	s_and_b64 s[26:27], s[0:1], vcc
	v_writelane_b32 v247, s26, 62
	v_add_u32_e32 v6, 0, v6
	v_add_u32_e32 v7, 0, v188
	v_writelane_b32 v247, s27, 63
	s_and_b64 s[26:27], s[0:1], s[18:19]
	v_writelane_b32 v246, s26, 0
	v_mul_u32_u24_e32 v11, 0x90, v212
	v_add_u32_e32 v161, 0, v213
	v_writelane_b32 v246, s27, 1
	s_and_b64 s[26:27], s[0:1], s[20:21]
	v_writelane_b32 v246, s26, 2
	s_and_b64 s[0:1], s[0:1], s[22:23]
	s_cmpk_gt_u32 s80, 0x13f
	v_writelane_b32 v246, s27, 3
	v_writelane_b32 v246, s0, 4
	s_cselect_b64 s[62:63], -1, 0
	s_cmp_eq_u32 s24, 5
	v_writelane_b32 v246, s1, 5
	s_cselect_b64 s[0:1], -1, 0
	s_and_b64 s[26:27], s[0:1], vcc
	v_writelane_b32 v246, s26, 6
	v_lshlrev_b32_e32 v122, 6, v1
	s_mov_b32 s97, 0
	v_writelane_b32 v246, s27, 7
	s_and_b64 s[26:27], s[0:1], s[18:19]
	v_writelane_b32 v246, s26, 8
	v_cmp_gt_u32_e64 s[6:7], 64, v0
	v_cmp_eq_u32_e64 s[8:9], 0, v186
	v_writelane_b32 v246, s27, 9
	s_and_b64 s[26:27], s[0:1], s[20:21]
	v_writelane_b32 v246, s26, 10
	s_and_b64 s[0:1], s[0:1], s[22:23]
	s_cmpk_gt_u32 s80, 0x17f
	v_writelane_b32 v246, s27, 11
	v_writelane_b32 v246, s0, 12
	s_cselect_b64 s[34:35], -1, 0
	s_cmp_eq_u32 s24, 6
	v_writelane_b32 v246, s1, 13
	s_cselect_b64 s[0:1], -1, 0
	s_and_b64 s[26:27], s[0:1], vcc
	s_and_b64 s[46:47], s[0:1], s[18:19]
	s_and_b64 s[80:81], s[0:1], s[20:21]
	s_and_b64 s[0:1], s[0:1], s[22:23]
	s_cmpk_gt_u32 s25, 0x1bf
	s_cselect_b64 s[82:83], -1, 0
	s_cmp_eq_u32 s24, 7
	s_cselect_b64 s[24:25], -1, 0
	s_and_b64 s[86:87], s[24:25], s[18:19]
	s_movk_i32 s18, 0x110
	v_mad_u32_u24 v9, v9, s18, 0
	v_add_u32_e32 v12, 0x9000, v9
	v_add_u32_e32 v159, v9, v10
	v_sub_u32_e32 v9, 0x437, v0
	v_lshrrev_b32_e32 v9, 9, v9
	s_and_b64 s[90:91], s[24:25], s[20:21]
	s_and_b64 s[92:93], s[24:25], s[22:23]
	v_cmp_ne_u32_e64 s[18:19], 0, v9
	v_cmp_lt_u32_e64 s[20:21], 1, v9
	v_cmp_lt_u32_e64 s[22:23], 2, v9
	v_or_b32_e32 v9, 0x400, v213
	v_add_u32_e32 v2, 0, v9
	v_writelane_b32 v246, s26, 14
	v_add_u32_e32 v163, 0x16090, v2
	v_add_u32_e32 v2, 0, v13
	v_writelane_b32 v246, s27, 15
	s_and_b64 s[84:85], s[24:25], vcc
	v_add_u32_e32 v164, 0x16090, v2
	v_add_u32_e32 v2, 0, v14
	s_mov_b32 s24, s94
	v_cmp_gt_u32_e64 s[10:11], 2, v186
	v_cmp_gt_u32_e64 s[12:13], 4, v186
	v_cmp_gt_u32_e64 s[14:15], 8, v186
	v_cmp_gt_u32_e64 s[2:3], 16, v186
	v_cmp_gt_u32_e64 s[16:17], 32, v186
	v_mov_b32_e32 v51, v50
	v_mov_b32_e32 v52, v50
	v_mov_b32_e32 v53, v50
	v_mov_b32_e32 v128, v126
	v_mov_b32_e32 v129, v119
	s_movk_i32 s33, 0x2200
	v_lshlrev_b32_e32 v130, 1, v120
	v_mov_b32_e32 v131, v119
	v_add_u32_e32 v160, v3, v120
	v_add_u32_e32 v162, 0x16000, v161
	v_add_u32_e32 v165, 0x16090, v2
	v_add_u32_e32 v166, v4, v5
	v_lshlrev_b32_e32 v132, 1, v124
	v_add_u32_e32 v167, v6, v188
	v_add_u32_e32 v168, v8, v11
	v_add_u32_e32 v169, v12, v10
	v_mov_b32_e32 v170, 0x358637bd
	v_mov_b32_e32 v171, 0x260
	v_mov_b32_e32 v172, 0x41b17218
	v_mbcnt_lo_u32_b32 v173, -1, 0
	v_mov_b32_e32 v174, 0xff800000
	v_add_u32_e32 v121, v7, v11
	v_writelane_b32 v246, s24, 16
	s_mov_b32 s28, s94
	s_nop 0
	v_writelane_b32 v246, s25, 17
	s_branch .LBB0_1288

; __device__ __forceinline__ void xcd_barrier(const XcdBarrier& b) {
;     ...
;     }
;     __syncthreads();
.LBB0_1437:
	s_or_b64 exec, exec, s[2:3]
	v_readfirstlane_b32 s4, v0
	s_lshr_b32 s4, s4, 6
	s_cmp_lg_u32 s4, 0
	s_cbranch_scc1 .Lsf12_notw0
	v_mov_b32_e32 v2, 0x20020
	v_mov_b32_e32 v4, 13
	ds_write_b32 v2, v4
	s_branch .Lsf12_skip

; __device__ __forceinline__ void transpose_item_f8(const float* W, int N, unsigned char* WT, int ldt, int kind, int off, int item, int lane, float scale) {
;     const int nblk = N >> 6, kb = item / nblk, nb = item - kb * nblk, k0 = 128 * kb + 16 * (lane & 7), n = 64 * nb + 4 * (lane >> 3);
; __device__ __forceinline__ void moe_convert(Frame& F, int lo, int hi, int rank, int nrank) {
;     ...
;     for (int it = lo + rank; it < hi; it += nrank) {
;         int r = it; const float* W; unsigned char* WT; int N, ldt, kind, off; float f8s;
;         if (r < 14336) { const int e = r / 1792; r -= e * 1792; W = F.in[IN_WMG] + (size_t)e * 2048 * DFFE; N = DFFE; WT = F.ws + WS_WGU1 + (size_t)e * 14336 * 2048; ldt = 2048; kind = 1; off = 0; f8s = 32.f; }
;         else if ((r -= 14336) < 14336) { const int e = r / 1792; r -= e * 1792; W = F.in[IN_WMU] + (size_t)e * 2048 * DFFE; N = DFFE; WT = F.ws + WS_WGU1 + (size_t)e * 14336 * 2048; ldt = 2048; kind = 1; off = 128; f8s = 256.f; }
;         else { r -= 14336; const int e = r / 1792; r -= e * 1792; W = F.in[IN_WMD] + (size_t)e * DFFE * 2048; N = 2048; WT = F.ws + WS_WDN1 + (size_t)e * 2048 * DFFE; ldt = DFFE; kind = 0; off = 0; f8s = 64.f; }
;         transpose_item_f8(W, N, WT, ldt, kind, off, r, F.lane, f8s);
.Lsf12_loop:
	ds_read_b32 v9, v8
	s_waitcnt lgkmcnt(0)
	v_readfirstlane_b32 s5, v9
	s_cmp_eq_u32 s5, 13
	s_cbranch_scc1 .Lsf12_done
	ds_add_rtn_u32 v9, v8, v18 offset:4
	s_waitcnt lgkmcnt(0)
	v_readfirstlane_b32 s18, v9
	s_cmp_ge_u32 s18, 96
	s_cbranch_scc1 .Lsf12_done
	s_add_i32 s18, s18, s33
	s_and_b32 s27, s18, 1
	s_lshr_b32 s19, s18, 1
	s_add_i32 s19, s19, 0x5800
	s_cmp_lt_u32 s19, 0x7000
	s_cbranch_scc0 .Lsf12_down
	s_add_i32 s20, s19, 0xffffc800
	s_lshr_b32 s21, s20, 8
	s_mul_i32 s21, s21, 37
	s_lshr_b32 s21, s21, 8
	s_mul_i32 s28, s21, 0x700
	s_sub_i32 s20, s20, s28
	s_mul_i32 s28, s21, 0x3800000
	s_add_u32 s14, s10, s28
	s_addc_u32 s15, s11, 0
	s_mul_i32 s28, s21, 0x1c00000
	s_add_u32 s28, s28, 0x7800000
	s_add_u32 s16, s86, s28
	s_addc_u32 s17, s87, 0
	s_movk_i32 s24, 0x7000
	s_movk_i32 s25, 0x800
	s_mov_b32 s26, 0x43800000
	s_lshr_b32 s22, s20, 4
	s_mul_i32 s22, s22, 0x2493
	s_lshr_b32 s22, s22, 16
	s_mul_i32 s28, s22, 0x70
	s_sub_i32 s23, s20, s28
	s_mov_b32 s29, 1
	s_branch .Lsf12_dec

;     __host__ __device__ bool next(int i, Unit& u) const {
;         const long L = (long)i * G + c; if (L >= nwg) return false;
;         int wgid = (int)L; { const int q = nwg / NXCD, r = nwg % NXCD, xcd = wgid % NXCD, off = wgid / NXCD; wgid = (xcd < r ? xcd * (q + 1) : r * (q + 1) + (xcd - r) * q) + off; }
;         const int nig = WGM * nN, gid = wgid / nig, fm = gid * WGM, gsz = (nM - fm) < WGM ? (nM - fm) : WGM;
;         u.pm = fm + ((wgid % nig) % gsz); u.pn = (wgid % nig) / gsz; return true;
.Lsf12_skip:
	s_waitcnt lgkmcnt(0)
	s_barrier
.LBB0_1438:
	s_cmp_lt_i32 s68, 14
	s_cselect_b64 s[2:3], -1, 0
	s_and_b64 s[0:1], s[2:3], s[0:1]
	s_andn2_b64 vcc, exec, s[0:1]
	s_cbranch_vccnz .LBB0_1463
	v_readlane_b32 s2, v247, 6
	s_cmpk_gt_i32 s2, 0x1ff
	v_readfirstlane_b32 s8, v0
	s_cbranch_scc1 .LBB0_1463
	v_readlane_b32 s3, v247, 6
	s_ashr_i32 s26, s3, 31
	s_lshr_b32 s2, s26, 29
	s_add_i32 s5, s3, s2
	s_and_b32 s2, s5, -8
	s_sub_i32 s6, s3, s2
	s_cmp_gt_i32 s6, -1
	s_cbranch_scc0 .LBB0_1442
	s_lshl_b32 s4, s6, 6
	s_cbranch_execz .LBB0_1443
	s_branch .LBB0_1444

; __device__ __forceinline__ void xcd_barrier(const XcdBarrier& b) {
;     ...
;     }
;     __syncthreads();
.LBB0_1512:
	s_or_b64 exec, exec, s[0:1]
	v_readfirstlane_b32 s4, v0
	s_lshr_b32 s4, s4, 6
	s_cmp_lg_u32 s4, 0
	s_cbranch_scc1 .Lsf13_notw0
	v_mov_b32_e32 v2, 0x20020
	v_mov_b32_e32 v4, 14
	ds_write_b32 v2, v4
	s_branch .Lsf13_skip

; __device__ __forceinline__ void transpose_item_f8(const float* W, int N, unsigned char* WT, int ldt, int kind, int off, int item, int lane, float scale) {
;     const int nblk = N >> 6, kb = item / nblk, nb = item - kb * nblk, k0 = 128 * kb + 16 * (lane & 7), n = 64 * nb + 4 * (lane >> 3);
; __device__ __forceinline__ void moe_convert(Frame& F, int lo, int hi, int rank, int nrank) {
;     ...
;     for (int it = lo + rank; it < hi; it += nrank) {
;         int r = it; const float* W; unsigned char* WT; int N, ldt, kind, off; float f8s;
;         if (r < 14336) { const int e = r / 1792; r -= e * 1792; W = F.in[IN_WMG] + (size_t)e * 2048 * DFFE; N = DFFE; WT = F.ws + WS_WGU1 + (size_t)e * 14336 * 2048; ldt = 2048; kind = 1; off = 0; f8s = 32.f; }
;         else if ((r -= 14336) < 14336) { const int e = r / 1792; r -= e * 1792; W = F.in[IN_WMU] + (size_t)e * 2048 * DFFE; N = DFFE; WT = F.ws + WS_WGU1 + (size_t)e * 14336 * 2048; ldt = 2048; kind = 1; off = 128; f8s = 256.f; }
;         else { r -= 14336; const int e = r / 1792; r -= e * 1792; W = F.in[IN_WMD] + (size_t)e * DFFE * 2048; N = 2048; WT = F.ws + WS_WDN1 + (size_t)e * 2048 * DFFE; ldt = DFFE; kind = 0; off = 0; f8s = 64.f; }
;         transpose_item_f8(W, N, WT, ldt, kind, off, r, F.lane, f8s);
.Lsf13_loop:
	ds_read_b32 v9, v8
	s_waitcnt lgkmcnt(0)
	v_readfirstlane_b32 s5, v9
	s_cmp_eq_u32 s5, 14
	s_cbranch_scc1 .Lsf13_done
	ds_add_rtn_u32 v9, v8, v18 offset:4
	s_waitcnt lgkmcnt(0)
	v_readfirstlane_b32 s18, v9
	s_cmp_ge_u32 s18, 96
	s_cbranch_scc1 .Lsf13_done
	s_add_i32 s18, s18, s33
	s_and_b32 s27, s18, 1
	s_lshr_b32 s19, s18, 1
	s_add_i32 s19, s19, 0x5800
	s_cmp_lt_u32 s19, 0x7000
	s_cbranch_scc0 .Lsf13_down
	s_add_i32 s20, s19, 0xffffc800
	s_lshr_b32 s21, s20, 8
	s_mul_i32 s21, s21, 37
	s_lshr_b32 s21, s21, 8
	s_mul_i32 s28, s21, 0x700
	s_sub_i32 s20, s20, s28
	s_mul_i32 s28, s21, 0x3800000
	s_add_u32 s14, s10, s28
	s_addc_u32 s15, s11, 0
	s_mul_i32 s28, s21, 0x1c00000
	s_add_u32 s28, s28, 0x7800000
	s_add_u32 s16, s86, s28
	s_addc_u32 s17, s87, 0
	s_movk_i32 s24, 0x7000
	s_movk_i32 s25, 0x800
	s_mov_b32 s26, 0x43800000
	s_lshr_b32 s22, s20, 4
	s_mul_i32 s22, s22, 0x2493
	s_lshr_b32 s22, s22, 16
	s_mul_i32 s28, s22, 0x70
	s_sub_i32 s23, s20, s28
	s_mov_b32 s29, 1
	s_branch .Lsf13_dec

; template <bool ROUTER, bool XBF>
; __device__ __forceinline__ void norm_phase(Frame& F, const void* xin_, const float* g, const float* modl, int sh_off, int sc_off) {
;     ...
;     if (ROUTER) {
;         for (int i = F.tid; i < 2048 * 8; i += NWAVES * 64) wrT[(i & 7) * 2048 + (i >> 3)] = F.in[IN_WROUTER][i];
;         if (F.tid < 8) lcnt[F.tid] = 0;
;         __syncthreads();
;     }
.Lsf13_skip:
	s_waitcnt lgkmcnt(0)
	s_barrier
.LBB0_1513:
	s_cmp_lt_i32 s68, 15
	s_cselect_b64 s[0:1], -1, 0
	s_and_b64 s[26:27], s[0:1], s[2:3]
	s_andn2_b64 vcc, exec, s[26:27]
	s_cbranch_vccnz .LBB0_1545
	v_readlane_b32 s4, v247, 0
	v_readlane_b32 s5, v247, 1
	s_load_dwordx2 s[2:3], s[4:5], 0x28
	s_load_dwordx2 s[0:1], s[4:5], 0xb0
	v_or_b32_e32 v1, 0x200, v0
	s_waitcnt vmcnt(0)
	v_mov_b32_e32 v6, 16
	s_mov_b64 s[4:5], 0
	v_mov_b32_e32 v5, 0
	v_mov_b64_e32 v[2:3], v[0:1]

; __device__ __forceinline__ void xcd_barrier(const XcdBarrier& b) {
;     ...
;     }
;     __syncthreads();
.LBB0_1594:
	s_or_b64 exec, exec, s[2:3]
	v_readfirstlane_b32 s4, v0
	s_lshr_b32 s4, s4, 6
	s_cmp_lg_u32 s4, 0
	s_cbranch_scc1 .Lsf14_notw0
	v_mov_b32_e32 v2, 0x20020
	v_mov_b32_e32 v4, 15
	ds_write_b32 v2, v4
	s_branch .Lsf14_skip

; __device__ __forceinline__ void transpose_item_f8(const float* W, int N, unsigned char* WT, int ldt, int kind, int off, int item, int lane, float scale) {
;     const int nblk = N >> 6, kb = item / nblk, nb = item - kb * nblk, k0 = 128 * kb + 16 * (lane & 7), n = 64 * nb + 4 * (lane >> 3);
; __device__ __forceinline__ void moe_convert(Frame& F, int lo, int hi, int rank, int nrank) {
;     ...
;     for (int it = lo + rank; it < hi; it += nrank) {
;         int r = it; const float* W; unsigned char* WT; int N, ldt, kind, off; float f8s;
;         if (r < 14336) { const int e = r / 1792; r -= e * 1792; W = F.in[IN_WMG] + (size_t)e * 2048 * DFFE; N = DFFE; WT = F.ws + WS_WGU1 + (size_t)e * 14336 * 2048; ldt = 2048; kind = 1; off = 0; f8s = 32.f; }
;         else if ((r -= 14336) < 14336) { const int e = r / 1792; r -= e * 1792; W = F.in[IN_WMU] + (size_t)e * 2048 * DFFE; N = DFFE; WT = F.ws + WS_WGU1 + (size_t)e * 14336 * 2048; ldt = 2048; kind = 1; off = 128; f8s = 256.f; }
;         else { r -= 14336; const int e = r / 1792; r -= e * 1792; W = F.in[IN_WMD] + (size_t)e * DFFE * 2048; N = 2048; WT = F.ws + WS_WDN1 + (size_t)e * 2048 * DFFE; ldt = DFFE; kind = 0; off = 0; f8s = 64.f; }
;         transpose_item_f8(W, N, WT, ldt, kind, off, r, F.lane, f8s);
.Lsf14_loop:
	ds_read_b32 v9, v8
	s_waitcnt lgkmcnt(0)
	v_readfirstlane_b32 s5, v9
	s_cmp_eq_u32 s5, 15
	s_cbranch_scc1 .Lsf14_done
	ds_add_rtn_u32 v9, v8, v18 offset:4
	s_waitcnt lgkmcnt(0)
	v_readfirstlane_b32 s18, v9
	s_cmp_ge_u32 s18, 96
	s_cbranch_scc1 .Lsf14_done
	s_add_i32 s18, s18, s33
	s_and_b32 s27, s18, 1
	s_lshr_b32 s19, s18, 1
	s_add_i32 s19, s19, 0x5800
	s_cmp_lt_u32 s19, 0x7000
	s_cbranch_scc0 .Lsf14_down
	s_add_i32 s20, s19, 0xffffc800
	s_lshr_b32 s21, s20, 8
	s_mul_i32 s21, s21, 37
	s_lshr_b32 s21, s21, 8
	s_mul_i32 s28, s21, 0x700
	s_sub_i32 s20, s20, s28
	s_mul_i32 s28, s21, 0x3800000
	s_add_u32 s14, s10, s28
	s_addc_u32 s15, s11, 0
	s_mul_i32 s28, s21, 0x1c00000
	s_add_u32 s28, s28, 0x7800000
	s_add_u32 s16, s86, s28
	s_addc_u32 s17, s87, 0
	s_movk_i32 s24, 0x7000
	s_movk_i32 s25, 0x800
	s_mov_b32 s26, 0x43800000
	s_lshr_b32 s22, s20, 4
	s_mul_i32 s22, s22, 0x2493
	s_lshr_b32 s22, s22, 16
	s_mul_i32 s28, s22, 0x70
	s_sub_i32 s23, s20, s28
	s_mov_b32 s29, 1
	s_branch .Lsf14_dec

; #define LAS __attribute__((address_space(3)))
; __device__ __forceinline__ int moe_tables(Frame& F) {
;     LAS int* seg = (LAS int*)(F.lds + MISC_OFF + 1024); LAS int* tile_e = (LAS int*)(F.lds + MISC_OFF + 64);
;     if (F.tid == 0) { int s = 0;
;         for (int e = 0; e < 8; ++e) { seg[e] = s; const int c = (int)__hip_atomic_load(F.ctl + CW_CNT + 64 * e, RLX_AGENT); const int nt = (c + 255) >> 8; for (int i = 0; i < nt; ++i) tile_e[(s >> 8) + i] = e; s += nt << 8; }
;         seg[8] = s; }
;     __syncthreads();
;     return seg[8] >> 8;
; }
.Lsf14_skip:
	s_waitcnt lgkmcnt(0)
	s_barrier
.LBB0_1595:
	s_cmp_lt_i32 s68, 16
	s_cselect_b64 s[2:3], -1, 0
	s_add_u32 s8, s86, 0x5f800000
	s_addc_u32 s9, s87, 0
	s_and_b64 s[4:5], s[2:3], s[0:1]
	s_andn2_b64 vcc, exec, s[4:5]
	s_cbranch_vccnz .LBB0_1725
	v_cmp_eq_u32_e32 vcc, 0, v0
	s_and_saveexec_b64 s[6:7], vcc
	s_cbranch_execz .LBB0_1694
	s_add_i32 s0, 0, 0x20400
	v_mov_b32_e32 v1, 0
	s_waitcnt vmcnt(0)
	v_mov_b32_e32 v2, s0
	ds_write_b32 v2, v1
	v_mov_b32_e32 v1, 0x8000
	global_load_dword v248, v1, s[86:87] sc1
	global_load_dword v249, v1, s[86:87] offset:256 sc1
	global_load_dword v250, v1, s[86:87] offset:512 sc1
	global_load_dword v251, v1, s[86:87] offset:768 sc1
	global_load_dword v252, v1, s[86:87] offset:1024 sc1
	global_load_dword v253, v1, s[86:87] offset:1280 sc1
	global_load_dword v254, v1, s[86:87] offset:1536 sc1
	global_load_dword v255, v1, s[86:87] offset:1792 sc1
	s_waitcnt vmcnt(0)
	v_mov_b32_e32 v2, v248
	s_nop 0
	v_readfirstlane_b32 s10, v2
	s_addk_i32 s10, 0xff
	s_ashr_i32 s11, s10, 8
	s_cmp_lt_i32 s11, 1
	s_cbranch_scc1 .LBB0_1609
	s_cmp_lt_u32 s11, 4
	s_cbranch_scc1 .LBB0_1606
	s_add_i32 s0, s11, -4
	s_lshr_b32 s12, s0, 2
	s_add_i32 s12, s12, 1
	s_cmp_lt_u32 s0, 28
	s_mov_b32 s0, 0
	s_cbranch_scc1 .LBB0_1602
	s_mov_b32 s2, s0
	s_mov_b32 s3, s0
	s_mov_b32 s1, s0
	v_mov_b64_e32 v[4:5], s[2:3]
	s_add_i32 s13, 0, 0x20040
	s_and_b32 s14, s12, 0x7ffffff8
	v_mov_b64_e32 v[2:3], s[0:1]

; __device__ __forceinline__ void xcd_barrier(const XcdBarrier& b) {
;     ...
;     }
;     __syncthreads();
.LBB0_1774:
	s_or_b64 exec, exec, s[2:3]
	v_readfirstlane_b32 s4, v0
	s_lshr_b32 s4, s4, 6
	s_cmp_lg_u32 s4, 0
	s_cbranch_scc1 .Lsf15_notw0
	v_mov_b32_e32 v2, 0x20020
	v_mov_b32_e32 v4, 16
	ds_write_b32 v2, v4
	s_branch .Lsf15_skip

; __device__ __forceinline__ void transpose_item_f8(const float* W, int N, unsigned char* WT, int ldt, int kind, int off, int item, int lane, float scale) {
;     const int nblk = N >> 6, kb = item / nblk, nb = item - kb * nblk, k0 = 128 * kb + 16 * (lane & 7), n = 64 * nb + 4 * (lane >> 3);
; __device__ __forceinline__ void moe_convert(Frame& F, int lo, int hi, int rank, int nrank) {
;     ...
;     for (int it = lo + rank; it < hi; it += nrank) {
;         int r = it; const float* W; unsigned char* WT; int N, ldt, kind, off; float f8s;
;         if (r < 14336) { const int e = r / 1792; r -= e * 1792; W = F.in[IN_WMG] + (size_t)e * 2048 * DFFE; N = DFFE; WT = F.ws + WS_WGU1 + (size_t)e * 14336 * 2048; ldt = 2048; kind = 1; off = 0; f8s = 32.f; }
;         else if ((r -= 14336) < 14336) { const int e = r / 1792; r -= e * 1792; W = F.in[IN_WMU] + (size_t)e * 2048 * DFFE; N = DFFE; WT = F.ws + WS_WGU1 + (size_t)e * 14336 * 2048; ldt = 2048; kind = 1; off = 128; f8s = 256.f; }
;         else { r -= 14336; const int e = r / 1792; r -= e * 1792; W = F.in[IN_WMD] + (size_t)e * DFFE * 2048; N = 2048; WT = F.ws + WS_WDN1 + (size_t)e * 2048 * DFFE; ldt = DFFE; kind = 0; off = 0; f8s = 64.f; }
;         transpose_item_f8(W, N, WT, ldt, kind, off, r, F.lane, f8s);
.Lsf15_loop:
	ds_add_rtn_u32 v9, v8, v18 offset:4
	s_waitcnt lgkmcnt(0)
	v_readfirstlane_b32 s18, v9
	s_cmp_ge_u32 s18, 96
	s_cbranch_scc1 .Lsf15_done
	s_add_i32 s18, s18, s33
	s_and_b32 s27, s18, 1
	s_lshr_b32 s19, s18, 1
	s_add_i32 s19, s19, 0x5800
	s_cmp_lt_u32 s19, 0x7000
	s_cbranch_scc0 .Lsf15_down
	s_add_i32 s20, s19, 0xffffc800
	s_lshr_b32 s21, s20, 8
	s_mul_i32 s21, s21, 37
	s_lshr_b32 s21, s21, 8
	s_mul_i32 s28, s21, 0x700
	s_sub_i32 s20, s20, s28
	s_mul_i32 s28, s21, 0x3800000
	s_add_u32 s14, s10, s28
	s_addc_u32 s15, s11, 0
	s_mul_i32 s28, s21, 0x1c00000
	s_add_u32 s28, s28, 0x7800000
	s_add_u32 s16, s86, s28
	s_addc_u32 s17, s87, 0
	s_movk_i32 s24, 0x7000
	s_movk_i32 s25, 0x800
	s_mov_b32 s26, 0x43800000
	s_lshr_b32 s22, s20, 4
	s_mul_i32 s22, s22, 0x2493
	s_lshr_b32 s22, s22, 16
	s_mul_i32 s28, s22, 0x70
	s_sub_i32 s23, s20, s28
	s_mov_b32 s29, 1
	s_branch .Lsf15_dec

; #define LAS __attribute__((address_space(3)))
; __device__ __forceinline__ int moe_tables(Frame& F) {
;     LAS int* seg = (LAS int*)(F.lds + MISC_OFF + 1024); LAS int* tile_e = (LAS int*)(F.lds + MISC_OFF + 64);
;     if (F.tid == 0) { int s = 0;
;         for (int e = 0; e < 8; ++e) { seg[e] = s; const int c = (int)__hip_atomic_load(F.ctl + CW_CNT + 64 * e, RLX_AGENT); const int nt = (c + 255) >> 8; for (int i = 0; i < nt; ++i) tile_e[(s >> 8) + i] = e; s += nt << 8; }
;         seg[8] = s; }
;     __syncthreads();
;     return seg[8] >> 8;
; }
.Lsf15_skip:
	s_waitcnt lgkmcnt(0)
	s_barrier
.LBB0_1775:
	s_cmp_lt_i32 s68, 17
	s_cselect_b64 s[2:3], -1, 0
	s_and_b64 s[4:5], s[2:3], s[0:1]
	s_andn2_b64 vcc, exec, s[4:5]
	s_cbranch_vccnz .LBB0_1890
	v_cmp_eq_u32_e32 vcc, 0, v0
	s_and_saveexec_b64 s[6:7], vcc
	s_cbranch_execz .LBB0_1874
	s_add_i32 s0, 0, 0x20400
	v_mov_b32_e32 v1, 0
	s_waitcnt vmcnt(0)
	v_mov_b32_e32 v2, s0
	ds_write_b32 v2, v1
	v_mov_b32_e32 v1, 0x8000
	global_load_dword v248, v1, s[86:87] sc1
	global_load_dword v249, v1, s[86:87] offset:256 sc1
	global_load_dword v250, v1, s[86:87] offset:512 sc1
	global_load_dword v251, v1, s[86:87] offset:768 sc1
	global_load_dword v252, v1, s[86:87] offset:1024 sc1
	global_load_dword v253, v1, s[86:87] offset:1280 sc1
	global_load_dword v254, v1, s[86:87] offset:1536 sc1
	global_load_dword v255, v1, s[86:87] offset:1792 sc1
	s_waitcnt vmcnt(0)
	v_mov_b32_e32 v2, v248
	s_nop 0
	v_readfirstlane_b32 s10, v2
	s_addk_i32 s10, 0xff
	s_ashr_i32 s11, s10, 8
	s_cmp_lt_i32 s11, 1
	s_cbranch_scc1 .LBB0_1789
	s_cmp_lt_u32 s11, 4
	s_cbranch_scc1 .LBB0_1786
	s_add_i32 s0, s11, -4
	s_lshr_b32 s12, s0, 2
	s_add_i32 s12, s12, 1
	s_cmp_lt_u32 s0, 28
	s_mov_b32 s0, 0
	s_cbranch_scc1 .LBB0_1782
	s_mov_b32 s2, s0
	s_mov_b32 s3, s0
	s_mov_b32 s1, s0
	v_mov_b64_e32 v[4:5], s[2:3]
	s_add_i32 s13, 0, 0x20040
	s_and_b32 s14, s12, 0x7ffffff8
	v_mov_b64_e32 v[2:3], s[0:1]
